# tail-converter bf16 weight stores marked non-temporal (consumed >500 us later) so they do not evict HID/PROJ that the next phase reads
# speedup vs baseline: 1.0116x; 1.0055x over previous
; __device__ __forceinline__ void conv_load(const ConvItem& ci, int lane, float (&v)[64]) {
;     const bool okc = ci.srcc >= 0 && (ci.srcc + lane) < ci.ncols;
;     const float* base = ci.W + (okc ? ci.srcc + lane : 0);
;     const int kmax = ci.Ksrc - 1;
; #pragma unroll
;     for (int i = 0; i < 64; ++i) { const int k = ci.k0 + i, kk = k < kmax ? k : kmax; v[i] = __builtin_nontemporal_load(base + (size_t)kk * ci.ldw); }
; #pragma unroll
;     for (int i = 0; i < 64; ++i) v[i] = (okc && (ci.k0 + i) < ci.Ksrc) ? v[i] : 0.f;
; }
.Lcvp10_30:
	s_cmp_lt_i32 s58, s76
	s_cselect_b64 s[4:5], -1, 0
	s_and_b64 s[4:5], vcc, s[4:5]
	s_cmp_lt_i32 s64, s76
	s_waitcnt vmcnt(62)
	v_cndmask_b32_e64 v21, 0, v21, s[4:5]
	s_cselect_b64 s[4:5], -1, 0
	s_and_b64 s[4:5], vcc, s[4:5]
	s_cmp_lt_i32 s65, s76
	v_cndmask_b32_e64 v20, 0, v20, s[4:5]
	s_cselect_b64 s[4:5], -1, 0
	s_and_b64 s[4:5], vcc, s[4:5]
	s_cmp_lt_i32 s78, s76
	s_waitcnt vmcnt(61)
	v_cndmask_b32_e64 v19, 0, v19, s[4:5]
	s_cselect_b64 s[4:5], -1, 0
	s_and_b64 s[4:5], vcc, s[4:5]
	s_cmp_lt_i32 s79, s76
	s_waitcnt vmcnt(60)
	v_cndmask_b32_e64 v18, 0, v18, s[4:5]
	s_cselect_b64 s[4:5], -1, 0
	s_and_b64 s[4:5], vcc, s[4:5]
	s_cmp_lt_i32 s80, s76
	s_waitcnt vmcnt(59)
	v_cndmask_b32_e64 v17, 0, v17, s[4:5]
	s_cselect_b64 s[4:5], -1, 0
	s_and_b64 s[4:5], vcc, s[4:5]
	s_cmp_lt_i32 s81, s76
	s_waitcnt vmcnt(58)
	v_cndmask_b32_e64 v16, 0, v16, s[4:5]
	s_cselect_b64 s[4:5], -1, 0
	s_and_b64 s[4:5], vcc, s[4:5]
	s_cmp_lt_i32 s82, s76
	s_waitcnt vmcnt(57)
	v_cndmask_b32_e64 v15, 0, v15, s[4:5]
	s_cselect_b64 s[4:5], -1, 0
	s_and_b64 s[4:5], vcc, s[4:5]
	s_cmp_lt_i32 s83, s76
	s_waitcnt vmcnt(56)
	v_cndmask_b32_e64 v8, 0, v8, s[4:5]
	s_cselect_b64 s[4:5], -1, 0
	s_and_b64 s[4:5], vcc, s[4:5]
	s_cmp_lt_i32 s85, s76
	s_waitcnt vmcnt(55)
	v_cndmask_b32_e64 v29, 0, v29, s[4:5]
	s_cselect_b64 s[4:5], -1, 0
	s_and_b64 s[4:5], vcc, s[4:5]
	s_cmp_lt_i32 s86, s76
	s_waitcnt vmcnt(54)
	v_cndmask_b32_e64 v28, 0, v28, s[4:5]
	s_cselect_b64 s[4:5], -1, 0
	s_and_b64 s[4:5], vcc, s[4:5]
	s_cmp_lt_i32 s87, s76
	s_waitcnt vmcnt(53)
	v_cndmask_b32_e64 v27, 0, v27, s[4:5]
	s_cselect_b64 s[4:5], -1, 0
	s_and_b64 s[4:5], vcc, s[4:5]
	s_cmp_lt_i32 s88, s76
	s_waitcnt vmcnt(52)
	v_cndmask_b32_e64 v26, 0, v26, s[4:5]
	s_cselect_b64 s[4:5], -1, 0
	s_and_b64 s[4:5], vcc, s[4:5]
	s_cmp_lt_i32 s89, s76
	s_waitcnt vmcnt(51)
	v_cndmask_b32_e64 v25, 0, v25, s[4:5]
	s_cselect_b64 s[4:5], -1, 0
	s_and_b64 s[4:5], vcc, s[4:5]
	s_cmp_lt_i32 s90, s76
	s_waitcnt vmcnt(50)
	v_cndmask_b32_e64 v24, 0, v24, s[4:5]
	s_cselect_b64 s[4:5], -1, 0
	s_and_b64 s[4:5], vcc, s[4:5]
	s_cmp_lt_i32 s92, s76
	s_waitcnt vmcnt(49)
	v_cndmask_b32_e64 v23, 0, v23, s[4:5]
	s_cselect_b64 s[4:5], -1, 0
	s_and_b64 s[4:5], vcc, s[4:5]
	s_cmp_lt_i32 s93, s76
	s_waitcnt vmcnt(48)
	v_cndmask_b32_e64 v22, 0, v22, s[4:5]
	s_cselect_b64 s[4:5], -1, 0
	s_and_b64 s[4:5], vcc, s[4:5]
	s_cmp_lt_i32 s94, s76
	s_waitcnt vmcnt(47)
	v_cndmask_b32_e64 v37, 0, v37, s[4:5]
	s_cselect_b64 s[4:5], -1, 0
	s_and_b64 s[4:5], vcc, s[4:5]
	s_cmp_lt_i32 s95, s76
	s_waitcnt vmcnt(46)
	v_cndmask_b32_e64 v36, 0, v36, s[4:5]
	s_cselect_b64 s[4:5], -1, 0
	s_and_b64 s[4:5], vcc, s[4:5]
	s_cmp_lt_i32 s50, s76
	s_waitcnt vmcnt(45)
	v_cndmask_b32_e64 v35, 0, v35, s[4:5]
	s_cselect_b64 s[4:5], -1, 0
	s_and_b64 s[4:5], vcc, s[4:5]
	s_cmp_lt_i32 s51, s76
	s_waitcnt vmcnt(44)
	v_cndmask_b32_e64 v34, 0, v34, s[4:5]
	s_cselect_b64 s[4:5], -1, 0
	s_and_b64 s[4:5], vcc, s[4:5]
	s_cmp_lt_i32 s52, s76
	s_waitcnt vmcnt(43)
	v_cndmask_b32_e64 v33, 0, v33, s[4:5]
	s_cselect_b64 s[4:5], -1, 0
	s_and_b64 s[4:5], vcc, s[4:5]
	s_cmp_lt_i32 s53, s76
	s_waitcnt vmcnt(42)
	v_cndmask_b32_e64 v32, 0, v32, s[4:5]
	s_cselect_b64 s[4:5], -1, 0
	s_and_b64 s[4:5], vcc, s[4:5]
	s_cmp_lt_i32 s6, s76
	s_waitcnt vmcnt(41)
	v_cndmask_b32_e64 v31, 0, v31, s[4:5]
	s_cselect_b64 s[4:5], -1, 0
	s_and_b64 s[4:5], vcc, s[4:5]
	s_cmp_lt_i32 s7, s76
	s_waitcnt vmcnt(40)
	v_cndmask_b32_e64 v30, 0, v30, s[4:5]
	s_cselect_b64 s[4:5], -1, 0
	s_and_b64 s[4:5], vcc, s[4:5]
	s_cmp_lt_i32 s8, s76
	s_waitcnt vmcnt(39)
	v_cndmask_b32_e64 v45, 0, v45, s[4:5]
	s_cselect_b64 s[4:5], -1, 0
	s_and_b64 s[4:5], vcc, s[4:5]
	s_cmp_lt_i32 s9, s76
	s_waitcnt vmcnt(38)
	v_cndmask_b32_e64 v44, 0, v44, s[4:5]
	s_cselect_b64 s[4:5], -1, 0
	s_and_b64 s[4:5], vcc, s[4:5]
	s_cmp_lt_i32 s10, s76
	s_waitcnt vmcnt(37)
	v_cndmask_b32_e64 v43, 0, v43, s[4:5]
	s_cselect_b64 s[4:5], -1, 0
	s_and_b64 s[4:5], vcc, s[4:5]
	s_cmp_lt_i32 s11, s76
	s_waitcnt vmcnt(36)
	v_cndmask_b32_e64 v42, 0, v42, s[4:5]
	s_cselect_b64 s[4:5], -1, 0
	s_and_b64 s[4:5], vcc, s[4:5]
	s_cmp_lt_i32 s14, s76
	s_waitcnt vmcnt(35)
	v_cndmask_b32_e64 v41, 0, v41, s[4:5]
	s_cselect_b64 s[4:5], -1, 0
	s_and_b64 s[4:5], vcc, s[4:5]
	s_cmp_lt_i32 s15, s76
	s_waitcnt vmcnt(34)
	v_cndmask_b32_e64 v40, 0, v40, s[4:5]
	s_cselect_b64 s[4:5], -1, 0
	s_and_b64 s[4:5], vcc, s[4:5]
	s_cmp_lt_i32 s16, s76
	s_waitcnt vmcnt(33)
	v_cndmask_b32_e64 v39, 0, v39, s[4:5]
	s_cselect_b64 s[4:5], -1, 0
	s_and_b64 s[4:5], vcc, s[4:5]
	s_cmp_lt_i32 s17, s76
	s_waitcnt vmcnt(32)
	v_cndmask_b32_e64 v38, 0, v38, s[4:5]
	s_cselect_b64 s[4:5], -1, 0
	s_and_b64 s[4:5], vcc, s[4:5]
	s_cmp_lt_i32 s12, s76
	s_waitcnt vmcnt(31)
	v_cndmask_b32_e64 v53, 0, v53, s[4:5]
	s_cselect_b64 s[4:5], -1, 0
	s_and_b64 s[4:5], vcc, s[4:5]
	s_cmp_lt_i32 s13, s76
	s_waitcnt vmcnt(30)
	v_cndmask_b32_e64 v52, 0, v52, s[4:5]
	s_cselect_b64 s[4:5], -1, 0
	s_and_b64 s[4:5], vcc, s[4:5]
	s_cmp_lt_i32 s20, s76
	s_waitcnt vmcnt(29)
	v_cndmask_b32_e64 v51, 0, v51, s[4:5]
	s_cselect_b64 s[4:5], -1, 0
	s_and_b64 s[4:5], vcc, s[4:5]
	s_cmp_lt_i32 s21, s76
	s_waitcnt vmcnt(28)
	v_cndmask_b32_e64 v50, 0, v50, s[4:5]
	s_cselect_b64 s[4:5], -1, 0
	s_and_b64 s[4:5], vcc, s[4:5]
	s_cmp_lt_i32 s24, s76
	s_waitcnt vmcnt(27)
	v_cndmask_b32_e64 v49, 0, v49, s[4:5]
	s_cselect_b64 s[4:5], -1, 0
	s_and_b64 s[4:5], vcc, s[4:5]
	s_cmp_lt_i32 s25, s76
	s_waitcnt vmcnt(26)
	v_cndmask_b32_e64 v48, 0, v48, s[4:5]
	s_cselect_b64 s[4:5], -1, 0
	s_and_b64 s[4:5], vcc, s[4:5]
	s_cmp_lt_i32 s26, s76
	s_waitcnt vmcnt(25)
	v_cndmask_b32_e64 v47, 0, v47, s[4:5]
	s_cselect_b64 s[4:5], -1, 0
	s_and_b64 s[4:5], vcc, s[4:5]
	s_cmp_lt_i32 s27, s76
	s_waitcnt vmcnt(24)
; #define LAS __attribute__((address_space(3)))
; #define LDS_WAIT() asm volatile("s_waitcnt lgkmcnt(0)" ::: "memory")
; __device__ __forceinline__ void conv_load(const ConvItem& ci, int lane, float (&v)[64]) {
;     ...
;     for (int i = 0; i < 64; ++i) { const int k = ci.k0 + i, kk = k < kmax ? k : kmax; v[i] = __builtin_nontemporal_load(base + (size_t)kk * ci.ldw); }
; #pragma unroll
;     for (int i = 0; i < 64; ++i) v[i] = (okc && (ci.k0 + i) < ci.Ksrc) ? v[i] : 0.f;
; }
; __device__ __forceinline__ void conv_store(const ConvItem& ci, LAS float* scr, int lane, const float (&v)[64]) {
;     const int c = lane & 7;
;     f32x4 s0 = {1.f, 1.f, 1.f, 1.f}, s1 = s0;
;     if (ci.ks) { const int kb = ci.k0 + 8 * c < ci.Ksrc - 8 ? ci.k0 + 8 * c : ci.Ksrc - 8; s0 = *(const f32x4*)(ci.ks + kb); s1 = *(const f32x4*)(ci.ks + kb + 4); }
; #pragma unroll
;     for (int i = 0; i < 64; ++i) scr[i * 65 + lane] = v[i];
;     LDS_WAIT(); asm volatile("" ::: "memory");
	v_cndmask_b32_e64 v46, 0, v46, s[4:5]
	s_cselect_b64 s[4:5], -1, 0
	s_and_b64 s[4:5], vcc, s[4:5]
	s_cmp_lt_i32 s18, s76
	s_waitcnt vmcnt(23)
	v_cndmask_b32_e64 v61, 0, v61, s[4:5]
	s_cselect_b64 s[4:5], -1, 0
	s_and_b64 s[4:5], vcc, s[4:5]
	s_cmp_lt_i32 s19, s76
	s_waitcnt vmcnt(22)
	v_cndmask_b32_e64 v60, 0, v60, s[4:5]
	s_cselect_b64 s[4:5], -1, 0
	s_and_b64 s[4:5], vcc, s[4:5]
	s_cmp_lt_i32 s28, s76
	s_waitcnt vmcnt(21)
	v_cndmask_b32_e64 v59, 0, v59, s[4:5]
	s_cselect_b64 s[4:5], -1, 0
	s_and_b64 s[4:5], vcc, s[4:5]
	s_cmp_lt_i32 s29, s76
	s_waitcnt vmcnt(20)
	v_cndmask_b32_e64 v58, 0, v58, s[4:5]
	s_cselect_b64 s[4:5], -1, 0
	s_and_b64 s[4:5], vcc, s[4:5]
	s_cmp_lt_i32 s22, s76
	s_waitcnt vmcnt(19)
	v_cndmask_b32_e64 v57, 0, v57, s[4:5]
	s_cselect_b64 s[4:5], -1, 0
	s_and_b64 s[4:5], vcc, s[4:5]
	s_cmp_lt_i32 s23, s76
	s_waitcnt vmcnt(18)
	v_cndmask_b32_e64 v56, 0, v56, s[4:5]
	s_cselect_b64 s[4:5], -1, 0
	s_and_b64 s[4:5], vcc, s[4:5]
	s_cmp_lt_i32 s30, s76
	s_waitcnt vmcnt(17)
	v_cndmask_b32_e64 v55, 0, v55, s[4:5]
	s_cselect_b64 s[4:5], -1, 0
	s_and_b64 s[4:5], vcc, s[4:5]
	s_cmp_lt_i32 s31, s76
	s_waitcnt vmcnt(16)
	v_cndmask_b32_e64 v54, 0, v54, s[4:5]
	s_cselect_b64 s[4:5], -1, 0
	s_and_b64 s[4:5], vcc, s[4:5]
	s_cmp_lt_i32 s36, s76
	s_waitcnt vmcnt(15)
	v_cndmask_b32_e64 v70, 0, v70, s[4:5]
	s_cselect_b64 s[4:5], -1, 0
	s_and_b64 s[4:5], vcc, s[4:5]
	s_cmp_lt_i32 s37, s76
	s_waitcnt vmcnt(14)
	v_cndmask_b32_e64 v69, 0, v69, s[4:5]
	s_cselect_b64 s[4:5], -1, 0
	s_and_b64 s[4:5], vcc, s[4:5]
	s_cmp_lt_i32 s38, s76
	s_waitcnt vmcnt(13)
	v_cndmask_b32_e64 v68, 0, v68, s[4:5]
	s_cselect_b64 s[4:5], -1, 0
	s_and_b64 s[4:5], vcc, s[4:5]
	s_cmp_lt_i32 s39, s76
	s_waitcnt vmcnt(12)
	v_cndmask_b32_e64 v67, 0, v67, s[4:5]
	s_cselect_b64 s[4:5], -1, 0
	s_and_b64 s[4:5], vcc, s[4:5]
	s_cmp_lt_i32 s34, s76
	s_waitcnt vmcnt(11)
	v_cndmask_b32_e64 v66, 0, v66, s[4:5]
	s_cselect_b64 s[4:5], -1, 0
	s_and_b64 s[4:5], vcc, s[4:5]
	s_cmp_lt_i32 s35, s76
	s_waitcnt vmcnt(10)
	v_cndmask_b32_e64 v64, 0, v64, s[4:5]
	s_cselect_b64 s[4:5], -1, 0
	s_and_b64 s[4:5], vcc, s[4:5]
	s_cmp_lt_i32 s42, s76
	s_waitcnt vmcnt(9)
	v_cndmask_b32_e64 v63, 0, v63, s[4:5]
	s_cselect_b64 s[4:5], -1, 0
	s_and_b64 s[4:5], vcc, s[4:5]
	s_cmp_lt_i32 s43, s76
	s_waitcnt vmcnt(8)
	v_cndmask_b32_e64 v62, 0, v62, s[4:5]
	s_cselect_b64 s[4:5], -1, 0
	s_and_b64 s[4:5], vcc, s[4:5]
	s_cmp_lt_i32 s54, s76
	s_waitcnt vmcnt(7)
	v_cndmask_b32_e64 v65, 0, v65, s[4:5]
	s_cselect_b64 s[4:5], -1, 0
	s_and_b64 s[4:5], vcc, s[4:5]
	s_cmp_lt_i32 s55, s76
	s_waitcnt vmcnt(6)
	v_cndmask_b32_e64 v74, 0, v74, s[4:5]
	s_cselect_b64 s[4:5], -1, 0
	s_and_b64 s[4:5], vcc, s[4:5]
	s_cmp_lt_i32 s46, s76
	ds_write2_b32 v12, v21, v20 offset1:65
	ds_write2_b32 v12, v19, v18 offset0:130 offset1:195
	v_add_u32_e32 v18, 0x400, v12
	s_waitcnt vmcnt(5)
	v_cndmask_b32_e64 v73, 0, v73, s[4:5]
	s_cselect_b64 s[4:5], -1, 0
	ds_write2_b32 v18, v17, v16 offset0:4 offset1:69
	ds_write2_b32 v18, v15, v8 offset0:134 offset1:199
	v_add_u32_e32 v8, 0x800, v12
	s_and_b64 s[4:5], vcc, s[4:5]
	ds_write2_b32 v8, v29, v28 offset0:8 offset1:73
	ds_write2_b32 v8, v27, v26 offset0:138 offset1:203
	v_add_u32_e32 v8, 0xc00, v12
	s_cmp_lt_i32 s47, s76
	ds_write2_b32 v8, v25, v24 offset0:12 offset1:77
	ds_write2_b32 v8, v23, v22 offset0:142 offset1:207
	v_add_u32_e32 v8, 0x1000, v12
	s_waitcnt vmcnt(4)
	v_cndmask_b32_e64 v72, 0, v72, s[4:5]
	s_cselect_b64 s[4:5], -1, 0
	ds_write2_b32 v8, v37, v36 offset0:16 offset1:81
	ds_write2_b32 v8, v35, v34 offset0:146 offset1:211
	v_add_u32_e32 v8, 0x1400, v12
	s_and_b64 s[4:5], vcc, s[4:5]
	ds_write2_b32 v8, v33, v32 offset0:20 offset1:85
	ds_write2_b32 v8, v31, v30 offset0:150 offset1:215
	v_add_u32_e32 v8, 0x1800, v12
	s_cmp_lt_i32 s48, s76
	ds_write2_b32 v8, v45, v44 offset0:24 offset1:89
	ds_write2_b32 v8, v43, v42 offset0:154 offset1:219
	v_add_u32_e32 v8, 0x1c00, v12
	s_waitcnt vmcnt(3)
	v_cndmask_b32_e64 v71, 0, v71, s[4:5]
	s_cselect_b64 s[4:5], -1, 0
	ds_write2_b32 v8, v41, v40 offset0:28 offset1:93
	ds_write2_b32 v8, v39, v38 offset0:158 offset1:223
	v_add_u32_e32 v8, 0x2000, v12
	s_and_b64 s[4:5], vcc, s[4:5]
	ds_write2_b32 v8, v53, v52 offset0:32 offset1:97
	ds_write2_b32 v8, v51, v50 offset0:162 offset1:227
	v_add_u32_e32 v8, 0x2400, v12
	s_cmp_lt_i32 s49, s76
	ds_write2_b32 v8, v49, v48 offset0:36 offset1:101
	ds_write2_b32 v8, v47, v46 offset0:166 offset1:231
	v_add_u32_e32 v8, 0x2800, v12
	s_waitcnt vmcnt(2)
	v_cndmask_b32_e64 v77, 0, v77, s[4:5]
	s_cselect_b64 s[4:5], -1, 0
	ds_write2_b32 v8, v61, v60 offset0:40 offset1:105
	ds_write2_b32 v8, v59, v58 offset0:170 offset1:235
	v_add_u32_e32 v8, 0x2c00, v12
	s_and_b64 s[4:5], vcc, s[4:5]
	ds_write2_b32 v8, v57, v56 offset0:44 offset1:109
	ds_write2_b32 v8, v55, v54 offset0:174 offset1:239
	v_add_u32_e32 v8, 0x3000, v12
	s_cmp_lt_i32 s44, s76
	ds_write2_b32 v8, v70, v69 offset0:48 offset1:113
	ds_write2_b32 v8, v68, v67 offset0:178 offset1:243
	v_add_u32_e32 v8, 0x3400, v12
	s_waitcnt vmcnt(1)
	v_cndmask_b32_e64 v76, 0, v76, s[4:5]
	s_cselect_b64 s[4:5], -1, 0
	ds_write2_b32 v8, v66, v64 offset0:52 offset1:117
	ds_write2_b32 v8, v63, v62 offset0:182 offset1:247
	v_add_u32_e32 v8, 0x3800, v12
	s_and_b64 vcc, vcc, s[4:5]
	ds_write2_b32 v8, v65, v74 offset0:56 offset1:121
	ds_write2_b32 v8, v73, v72 offset0:186 offset1:251
	v_add_u32_e32 v8, 0x3c00, v12
	s_waitcnt vmcnt(0)
	v_cndmask_b32_e32 v75, 0, v75, vcc
	ds_write2_b32 v8, v71, v77 offset0:60 offset1:125
	ds_write2_b32 v8, v76, v75 offset0:190 offset1:255
	s_waitcnt lgkmcnt(0)
; __device__ __forceinline__ unsigned cvt_pk_bf16(float lo, float hi) { unsigned r; asm volatile("v_cvt_pk_bf16_f32 %0, %1, %2" : "=v"(r) : "v"(lo), "v"(hi)); return r; }
; #define LAS __attribute__((address_space(3)))
; #define LDS_WAIT() asm volatile("s_waitcnt lgkmcnt(0)" ::: "memory")
; __device__ __forceinline__ void conv_store(const ConvItem& ci, LAS float* scr, int lane, const float (&v)[64]) {
;     ...
;     LDS_WAIT(); asm volatile("" ::: "memory");
; #pragma unroll
;     for (int j = 0; j < 8; ++j) { const int n = (lane >> 3) + 8 * j; const LAS float* s = scr + (8 * c) * 65 + n;
;         v4u o; o.x = cvt_pk_bf16(s[0 * 65] * s0[0], s[1 * 65] * s0[1]); o.y = cvt_pk_bf16(s[2 * 65] * s0[2], s[3 * 65] * s0[3]); o.z = cvt_pk_bf16(s[4 * 65] * s1[0], s[5 * 65] * s1[1]); o.w = cvt_pk_bf16(s[6 * 65] * s1[2], s[7 * 65] * s1[3]);
;         *(v4u*)(ci.dst + (size_t)(ci.drow0 + n) * ci.ldd + ci.k0 + 8 * c) = o; }
	v_add_u32_e32 v192, 0x400, v14
	ds_read2_b32 v[128:129], v14 offset1:65
	ds_read2_b32 v[130:131], v14 offset0:130 offset1:195
	ds_read2_b32 v[132:133], v192 offset0:4 offset1:69
	ds_read2_b32 v[134:135], v192 offset0:134 offset1:199
	ds_read2_b32 v[136:137], v14 offset0:8 offset1:73
	ds_read2_b32 v[138:139], v14 offset0:138 offset1:203
	ds_read2_b32 v[140:141], v192 offset0:12 offset1:77
	ds_read2_b32 v[142:143], v192 offset0:142 offset1:207
	ds_read2_b32 v[144:145], v14 offset0:16 offset1:81
	ds_read2_b32 v[146:147], v14 offset0:146 offset1:211
	ds_read2_b32 v[148:149], v192 offset0:20 offset1:85
	ds_read2_b32 v[150:151], v192 offset0:150 offset1:215
	ds_read2_b32 v[152:153], v14 offset0:24 offset1:89
	ds_read2_b32 v[154:155], v14 offset0:154 offset1:219
	ds_read2_b32 v[156:157], v192 offset0:28 offset1:93
	ds_read2_b32 v[158:159], v192 offset0:158 offset1:223
	ds_read2_b32 v[160:161], v14 offset0:32 offset1:97
	ds_read2_b32 v[162:163], v14 offset0:162 offset1:227
	ds_read2_b32 v[164:165], v192 offset0:36 offset1:101
	ds_read2_b32 v[166:167], v192 offset0:166 offset1:231
	ds_read2_b32 v[168:169], v14 offset0:40 offset1:105
	ds_read2_b32 v[170:171], v14 offset0:170 offset1:235
	ds_read2_b32 v[172:173], v192 offset0:44 offset1:109
	ds_read2_b32 v[174:175], v192 offset0:174 offset1:239
	ds_read2_b32 v[176:177], v14 offset0:48 offset1:113
	ds_read2_b32 v[178:179], v14 offset0:178 offset1:243
	ds_read2_b32 v[180:181], v192 offset0:52 offset1:117
	ds_read2_b32 v[182:183], v192 offset0:182 offset1:247
	ds_read2_b32 v[184:185], v14 offset0:56 offset1:121
	ds_read2_b32 v[186:187], v14 offset0:186 offset1:251
	ds_read2_b32 v[188:189], v192 offset0:60 offset1:125
	ds_read2_b32 v[190:191], v192 offset0:190 offset1:255
	s_waitcnt lgkmcnt(0)
	v_add_u32_e32 v24, s59, v13
	v_mul_lo_u32 v22, s57, v24
	s_ashr_i32 s59, s58, 31
	v_readlane_b32 s76, v254, 31
	s_waitcnt lgkmcnt(0)
	v_mul_f32_e32 v8, v4, v128
	v_mul_f32_e32 v15, v5, v129
	v_cvt_pk_bf16_f32 v16, v8, v15
	s_add_i32 s3, s3, s33
	s_add_i32 s66, s66, s67
	s_add_i32 s68, s68, s69
	s_add_i32 s70, s70, s71
	s_waitcnt lgkmcnt(0)
	v_mul_f32_e32 v15, v7, v131
	v_mul_f32_e32 v8, v6, v130
	v_cvt_pk_bf16_f32 v17, v8, v15
	v_add_u32_e32 v15, 0x400, v14
	s_add_i32 s72, s72, s73
	s_add_i32 s74, s74, s75
	v_readlane_b32 s78, v254, 33
	v_readlane_b32 s79, v254, 34
	s_waitcnt lgkmcnt(0)
	v_mul_f32_e32 v8, v0, v132
	v_mul_f32_e32 v18, v1, v133
	v_cvt_pk_bf16_f32 v18, v8, v18
	v_readlane_b32 s80, v255, 21
	v_readlane_b32 s77, v254, 32
	s_movk_i32 s78, 0x1580
	v_readlane_b32 s82, v255, 23
	s_waitcnt lgkmcnt(0)
	v_mul_f32_e32 v8, v2, v134
	v_mul_f32_e32 v19, v3, v135
	v_cvt_pk_bf16_f32 v19, v8, v19
	v_ashrrev_i32_e32 v8, 31, v24
	v_mul_lo_u32 v8, s56, v8
	v_mad_u64_u32 v[20:21], s[4:5], s56, v24, 0
	v_add3_u32 v21, v21, v8, v22
	v_lshl_add_u64 v[20:21], v[20:21], 1, s[60:61]
	s_lshl_b64 s[4:5], s[58:59], 1
	v_lshl_add_u64 v[20:21], v[20:21], 0, s[4:5]
	v_lshlrev_b32_e32 v8, 1, v10
	v_lshl_add_u64 v[20:21], v[20:21], 0, v[8:9]
	global_store_dwordx4 v[20:21], v[16:19], off nt
	s_cmpk_lt_i32 s3, 11008
	v_readlane_b32 s83, v255, 24
	s_waitcnt lgkmcnt(0)
	v_mul_f32_e32 v16, v4, v136
	v_mul_f32_e32 v17, v5, v137
	v_cvt_pk_bf16_f32 v16, v16, v17
	s_mov_b32 s79, 0x3f22f983
	s_mov_b32 s85, 0xbfc90fda
	s_brev_b32 s86, 1
	s_movk_i32 s87, 0x1f8
	s_waitcnt lgkmcnt(0)
	v_mul_f32_e32 v17, v6, v138
	v_mul_f32_e32 v18, v7, v139
	v_cvt_pk_bf16_f32 v17, v17, v18
	s_mov_b64 s[88:89], 0x80
	s_mov_b64 s[92:93], 0x4000
	s_mov_b64 s[94:95], 0x4800
	v_readlane_b32 s81, v255, 22
	s_waitcnt lgkmcnt(0)
	v_mul_f32_e32 v18, v0, v140
	v_mul_f32_e32 v19, v1, v141
	v_cvt_pk_bf16_f32 v18, v18, v19
	s_waitcnt lgkmcnt(0)
	v_mul_f32_e32 v19, v2, v142
	v_mul_f32_e32 v20, v3, v143
	v_cvt_pk_bf16_f32 v19, v19, v20
	v_add_u32_e32 v20, 8, v24
	v_ashrrev_i32_e32 v21, 31, v20
	v_mul_lo_u32 v22, s56, v21
	v_mul_lo_u32 v23, s57, v20
	v_mad_u64_u32 v[20:21], s[6:7], s56, v20, 0
	v_add3_u32 v21, v21, v22, v23
	v_lshl_add_u64 v[20:21], v[20:21], 1, s[60:61]
	v_lshl_add_u64 v[20:21], v[20:21], 0, s[4:5]
	v_lshl_add_u64 v[20:21], v[20:21], 0, v[8:9]
	global_store_dwordx4 v[20:21], v[16:19], off nt
	s_waitcnt lgkmcnt(0)
	s_nop 0
	v_mul_f32_e32 v16, v4, v144
	v_mul_f32_e32 v17, v5, v145
	v_cvt_pk_bf16_f32 v16, v16, v17
	s_waitcnt lgkmcnt(0)
	v_mul_f32_e32 v17, v6, v146
	v_mul_f32_e32 v18, v7, v147
	v_cvt_pk_bf16_f32 v17, v17, v18
	s_waitcnt lgkmcnt(0)
	v_mul_f32_e32 v18, v0, v148
	v_mul_f32_e32 v19, v1, v149
	v_cvt_pk_bf16_f32 v18, v18, v19
	s_waitcnt lgkmcnt(0)
; __device__ __forceinline__ unsigned cvt_pk_bf16(float lo, float hi) { unsigned r; asm volatile("v_cvt_pk_bf16_f32 %0, %1, %2" : "=v"(r) : "v"(lo), "v"(hi)); return r; }
; #define LAS __attribute__((address_space(3)))
; #define LDS_WAIT() asm volatile("s_waitcnt lgkmcnt(0)" ::: "memory")
; __device__ __forceinline__ void conv_store(const ConvItem& ci, LAS float* scr, int lane, const float (&v)[64]) {
;     ...
;     for (int j = 0; j < 8; ++j) { const int n = (lane >> 3) + 8 * j; const LAS float* s = scr + (8 * c) * 65 + n;
;         v4u o; o.x = cvt_pk_bf16(s[0 * 65] * s0[0], s[1 * 65] * s0[1]); o.y = cvt_pk_bf16(s[2 * 65] * s0[2], s[3 * 65] * s0[3]); o.z = cvt_pk_bf16(s[4 * 65] * s1[0], s[5 * 65] * s1[1]); o.w = cvt_pk_bf16(s[6 * 65] * s1[2], s[7 * 65] * s1[3]);
;         *(v4u*)(ci.dst + (size_t)(ci.drow0 + n) * ci.ldd + ci.k0 + 8 * c) = o; }
;     LDS_WAIT(); asm volatile("" ::: "memory");
; }
	v_mul_f32_e32 v19, v2, v150
	v_mul_f32_e32 v20, v3, v151
	v_cvt_pk_bf16_f32 v19, v19, v20
	v_add_u32_e32 v20, 16, v24
	v_ashrrev_i32_e32 v21, 31, v20
	v_mul_lo_u32 v22, s56, v21
	v_mul_lo_u32 v23, s57, v20
	v_mad_u64_u32 v[20:21], s[6:7], s56, v20, 0
	v_add3_u32 v21, v21, v22, v23
	v_lshl_add_u64 v[20:21], v[20:21], 1, s[60:61]
	v_lshl_add_u64 v[20:21], v[20:21], 0, s[4:5]
	v_lshl_add_u64 v[20:21], v[20:21], 0, v[8:9]
	global_store_dwordx4 v[20:21], v[16:19], off nt
	s_waitcnt lgkmcnt(0)
	s_nop 0
	v_mul_f32_e32 v16, v4, v152
	v_mul_f32_e32 v17, v5, v153
	v_cvt_pk_bf16_f32 v16, v16, v17
	s_waitcnt lgkmcnt(0)
	v_mul_f32_e32 v17, v6, v154
	v_mul_f32_e32 v18, v7, v155
	v_cvt_pk_bf16_f32 v17, v17, v18
	s_waitcnt lgkmcnt(0)
	v_mul_f32_e32 v18, v0, v156
	v_mul_f32_e32 v19, v1, v157
	v_cvt_pk_bf16_f32 v18, v18, v19
	s_waitcnt lgkmcnt(0)
	v_mul_f32_e32 v19, v2, v158
	v_mul_f32_e32 v20, v3, v159
	v_cvt_pk_bf16_f32 v19, v19, v20
	v_add_u32_e32 v20, 24, v24
	v_ashrrev_i32_e32 v21, 31, v20
	v_mul_lo_u32 v22, s56, v21
	v_mul_lo_u32 v23, s57, v20
	v_mad_u64_u32 v[20:21], s[6:7], s56, v20, 0
	v_add3_u32 v21, v21, v22, v23
	v_lshl_add_u64 v[20:21], v[20:21], 1, s[60:61]
	v_lshl_add_u64 v[20:21], v[20:21], 0, s[4:5]
	v_lshl_add_u64 v[20:21], v[20:21], 0, v[8:9]
	global_store_dwordx4 v[20:21], v[16:19], off nt
	s_waitcnt lgkmcnt(0)
	s_nop 0
	v_mul_f32_e32 v16, v4, v160
	v_mul_f32_e32 v17, v5, v161
	v_cvt_pk_bf16_f32 v16, v16, v17
	s_waitcnt lgkmcnt(0)
	v_mul_f32_e32 v17, v6, v162
	v_mul_f32_e32 v18, v7, v163
	v_cvt_pk_bf16_f32 v17, v17, v18
	s_waitcnt lgkmcnt(0)
	v_mul_f32_e32 v18, v0, v164
	v_mul_f32_e32 v19, v1, v165
	v_cvt_pk_bf16_f32 v18, v18, v19
	s_waitcnt lgkmcnt(0)
	v_mul_f32_e32 v19, v2, v166
	v_mul_f32_e32 v20, v3, v167
	v_cvt_pk_bf16_f32 v19, v19, v20
	v_add_u32_e32 v20, 32, v24
	v_ashrrev_i32_e32 v21, 31, v20
	v_mul_lo_u32 v22, s56, v21
	v_mul_lo_u32 v23, s57, v20
	v_mad_u64_u32 v[20:21], s[6:7], s56, v20, 0
	v_add3_u32 v21, v21, v22, v23
	v_lshl_add_u64 v[20:21], v[20:21], 1, s[60:61]
	v_lshl_add_u64 v[20:21], v[20:21], 0, s[4:5]
	v_lshl_add_u64 v[20:21], v[20:21], 0, v[8:9]
	global_store_dwordx4 v[20:21], v[16:19], off nt
	s_waitcnt lgkmcnt(0)
	s_nop 0
	v_mul_f32_e32 v16, v4, v168
	v_mul_f32_e32 v17, v5, v169
	v_cvt_pk_bf16_f32 v16, v16, v17
	s_waitcnt lgkmcnt(0)
	v_mul_f32_e32 v17, v6, v170
	v_mul_f32_e32 v18, v7, v171
	v_cvt_pk_bf16_f32 v17, v17, v18
	s_waitcnt lgkmcnt(0)
	v_mul_f32_e32 v18, v0, v172
	v_mul_f32_e32 v19, v1, v173
	v_cvt_pk_bf16_f32 v18, v18, v19
	s_waitcnt lgkmcnt(0)
	v_mul_f32_e32 v19, v2, v174
	v_mul_f32_e32 v20, v3, v175
	v_cvt_pk_bf16_f32 v19, v19, v20
	v_add_u32_e32 v20, 40, v24
	v_ashrrev_i32_e32 v21, 31, v20
	v_mul_lo_u32 v22, s56, v21
	v_mul_lo_u32 v23, s57, v20
	v_mad_u64_u32 v[20:21], s[6:7], s56, v20, 0
	v_add3_u32 v21, v21, v22, v23
	v_lshl_add_u64 v[20:21], v[20:21], 1, s[60:61]
	v_lshl_add_u64 v[20:21], v[20:21], 0, s[4:5]
	v_lshl_add_u64 v[20:21], v[20:21], 0, v[8:9]
	global_store_dwordx4 v[20:21], v[16:19], off nt
	s_waitcnt lgkmcnt(0)
	s_nop 0
	v_mul_f32_e32 v16, v4, v176
	v_mul_f32_e32 v17, v5, v177
	v_cvt_pk_bf16_f32 v16, v16, v17
	s_waitcnt lgkmcnt(0)
	v_mul_f32_e32 v17, v6, v178
	v_mul_f32_e32 v18, v7, v179
	v_cvt_pk_bf16_f32 v17, v17, v18
	s_waitcnt lgkmcnt(0)
	v_mul_f32_e32 v18, v0, v180
	v_mul_f32_e32 v19, v1, v181
	v_cvt_pk_bf16_f32 v18, v18, v19
	s_waitcnt lgkmcnt(0)
	v_mul_f32_e32 v19, v2, v182
	v_mul_f32_e32 v20, v3, v183
	v_cvt_pk_bf16_f32 v19, v19, v20
	v_add_u32_e32 v20, 48, v24
	v_ashrrev_i32_e32 v21, 31, v20
	v_mul_lo_u32 v22, s56, v21
	v_mul_lo_u32 v23, s57, v20
	v_mad_u64_u32 v[20:21], s[6:7], s56, v20, 0
	v_add3_u32 v21, v21, v22, v23
	v_lshl_add_u64 v[20:21], v[20:21], 1, s[60:61]
	v_lshl_add_u64 v[20:21], v[20:21], 0, s[4:5]
	v_lshl_add_u64 v[20:21], v[20:21], 0, v[8:9]
	global_store_dwordx4 v[20:21], v[16:19], off nt
	s_waitcnt lgkmcnt(0)
	v_mul_f32_e32 v4, v4, v184
	v_mul_f32_e32 v5, v5, v185
	v_cvt_pk_bf16_f32 v4, v4, v5
	s_waitcnt lgkmcnt(0)
	v_mul_f32_e32 v5, v6, v186
	v_mul_f32_e32 v6, v7, v187
	v_cvt_pk_bf16_f32 v5, v5, v6
	s_waitcnt lgkmcnt(0)
	v_mul_f32_e32 v0, v0, v188
	v_mul_f32_e32 v1, v1, v189
	v_cvt_pk_bf16_f32 v6, v0, v1
	s_waitcnt lgkmcnt(0)
	v_mul_f32_e32 v0, v2, v190
	v_mul_f32_e32 v1, v3, v191
	v_cvt_pk_bf16_f32 v7, v0, v1
	v_add_u32_e32 v0, 56, v24
	v_ashrrev_i32_e32 v1, 31, v0
	v_mul_lo_u32 v2, s56, v1
	v_mul_lo_u32 v3, s57, v0
	v_mad_u64_u32 v[0:1], s[6:7], s56, v0, 0
	v_add3_u32 v1, v1, v2, v3
	v_lshl_add_u64 v[0:1], v[0:1], 1, s[60:61]
	v_lshl_add_u64 v[0:1], v[0:1], 0, s[4:5]
	v_lshl_add_u64 v[0:1], v[0:1], 0, v[8:9]
	global_store_dwordx4 v[0:1], v[4:7], off nt
	s_waitcnt lgkmcnt(0)
	s_cbranch_scc0 .Lcvp10_ret

; __device__ __forceinline__ void conv_load(const ConvItem& ci, int lane, float (&v)[64]) {
;     const bool okc = ci.srcc >= 0 && (ci.srcc + lane) < ci.ncols;
;     const float* base = ci.W + (okc ? ci.srcc + lane : 0);
;     const int kmax = ci.Ksrc - 1;
; #pragma unroll
;     for (int i = 0; i < 64; ++i) { const int k = ci.k0 + i, kk = k < kmax ? k : kmax; v[i] = __builtin_nontemporal_load(base + (size_t)kk * ci.ldw); }
; #pragma unroll
;     for (int i = 0; i < 64; ++i) v[i] = (okc && (ci.k0 + i) < ci.Ksrc) ? v[i] : 0.f;
; }
.Lcvp11_30:
	s_cmp_lt_i32 s58, s76
	s_cselect_b64 s[4:5], -1, 0
	s_and_b64 s[4:5], vcc, s[4:5]
	s_cmp_lt_i32 s64, s76
	s_waitcnt vmcnt(62)
	v_cndmask_b32_e64 v21, 0, v21, s[4:5]
	s_cselect_b64 s[4:5], -1, 0
	s_and_b64 s[4:5], vcc, s[4:5]
	s_cmp_lt_i32 s65, s76
	v_cndmask_b32_e64 v20, 0, v20, s[4:5]
	s_cselect_b64 s[4:5], -1, 0
	s_and_b64 s[4:5], vcc, s[4:5]
	s_cmp_lt_i32 s78, s76
	s_waitcnt vmcnt(61)
	v_cndmask_b32_e64 v19, 0, v19, s[4:5]
	s_cselect_b64 s[4:5], -1, 0
	s_and_b64 s[4:5], vcc, s[4:5]
	s_cmp_lt_i32 s79, s76
	s_waitcnt vmcnt(60)
	v_cndmask_b32_e64 v18, 0, v18, s[4:5]
	s_cselect_b64 s[4:5], -1, 0
	s_and_b64 s[4:5], vcc, s[4:5]
	s_cmp_lt_i32 s80, s76
	s_waitcnt vmcnt(59)
	v_cndmask_b32_e64 v17, 0, v17, s[4:5]
	s_cselect_b64 s[4:5], -1, 0
	s_and_b64 s[4:5], vcc, s[4:5]
	s_cmp_lt_i32 s81, s76
	s_waitcnt vmcnt(58)
	v_cndmask_b32_e64 v16, 0, v16, s[4:5]
	s_cselect_b64 s[4:5], -1, 0
	s_and_b64 s[4:5], vcc, s[4:5]
	s_cmp_lt_i32 s82, s76
	s_waitcnt vmcnt(57)
	v_cndmask_b32_e64 v15, 0, v15, s[4:5]
	s_cselect_b64 s[4:5], -1, 0
	s_and_b64 s[4:5], vcc, s[4:5]
	s_cmp_lt_i32 s83, s76
	s_waitcnt vmcnt(56)
	v_cndmask_b32_e64 v8, 0, v8, s[4:5]
	s_cselect_b64 s[4:5], -1, 0
	s_and_b64 s[4:5], vcc, s[4:5]
	s_cmp_lt_i32 s85, s76
	s_waitcnt vmcnt(55)
	v_cndmask_b32_e64 v29, 0, v29, s[4:5]
	s_cselect_b64 s[4:5], -1, 0
	s_and_b64 s[4:5], vcc, s[4:5]
	s_cmp_lt_i32 s86, s76
	s_waitcnt vmcnt(54)
	v_cndmask_b32_e64 v28, 0, v28, s[4:5]
	s_cselect_b64 s[4:5], -1, 0
	s_and_b64 s[4:5], vcc, s[4:5]
	s_cmp_lt_i32 s87, s76
	s_waitcnt vmcnt(53)
	v_cndmask_b32_e64 v27, 0, v27, s[4:5]
	s_cselect_b64 s[4:5], -1, 0
	s_and_b64 s[4:5], vcc, s[4:5]
	s_cmp_lt_i32 s88, s76
	s_waitcnt vmcnt(52)
	v_cndmask_b32_e64 v26, 0, v26, s[4:5]
	s_cselect_b64 s[4:5], -1, 0
	s_and_b64 s[4:5], vcc, s[4:5]
	s_cmp_lt_i32 s89, s76
	s_waitcnt vmcnt(51)
	v_cndmask_b32_e64 v25, 0, v25, s[4:5]
	s_cselect_b64 s[4:5], -1, 0
	s_and_b64 s[4:5], vcc, s[4:5]
	s_cmp_lt_i32 s90, s76
	s_waitcnt vmcnt(50)
	v_cndmask_b32_e64 v24, 0, v24, s[4:5]
	s_cselect_b64 s[4:5], -1, 0
	s_and_b64 s[4:5], vcc, s[4:5]
	s_cmp_lt_i32 s92, s76
	s_waitcnt vmcnt(49)
	v_cndmask_b32_e64 v23, 0, v23, s[4:5]
	s_cselect_b64 s[4:5], -1, 0
	s_and_b64 s[4:5], vcc, s[4:5]
	s_cmp_lt_i32 s93, s76
	s_waitcnt vmcnt(48)
	v_cndmask_b32_e64 v22, 0, v22, s[4:5]
	s_cselect_b64 s[4:5], -1, 0
	s_and_b64 s[4:5], vcc, s[4:5]
	s_cmp_lt_i32 s94, s76
	s_waitcnt vmcnt(47)
	v_cndmask_b32_e64 v37, 0, v37, s[4:5]
	s_cselect_b64 s[4:5], -1, 0
	s_and_b64 s[4:5], vcc, s[4:5]
	s_cmp_lt_i32 s95, s76
	s_waitcnt vmcnt(46)
	v_cndmask_b32_e64 v36, 0, v36, s[4:5]
	s_cselect_b64 s[4:5], -1, 0
	s_and_b64 s[4:5], vcc, s[4:5]
	s_cmp_lt_i32 s50, s76
	s_waitcnt vmcnt(45)
	v_cndmask_b32_e64 v35, 0, v35, s[4:5]
	s_cselect_b64 s[4:5], -1, 0
	s_and_b64 s[4:5], vcc, s[4:5]
	s_cmp_lt_i32 s51, s76
	s_waitcnt vmcnt(44)
	v_cndmask_b32_e64 v34, 0, v34, s[4:5]
	s_cselect_b64 s[4:5], -1, 0
	s_and_b64 s[4:5], vcc, s[4:5]
	s_cmp_lt_i32 s52, s76
	s_waitcnt vmcnt(43)
	v_cndmask_b32_e64 v33, 0, v33, s[4:5]
	s_cselect_b64 s[4:5], -1, 0
	s_and_b64 s[4:5], vcc, s[4:5]
	s_cmp_lt_i32 s53, s76
	s_waitcnt vmcnt(42)
	v_cndmask_b32_e64 v32, 0, v32, s[4:5]
	s_cselect_b64 s[4:5], -1, 0
	s_and_b64 s[4:5], vcc, s[4:5]
	s_cmp_lt_i32 s6, s76
	s_waitcnt vmcnt(41)
	v_cndmask_b32_e64 v31, 0, v31, s[4:5]
	s_cselect_b64 s[4:5], -1, 0
	s_and_b64 s[4:5], vcc, s[4:5]
	s_cmp_lt_i32 s7, s76
	s_waitcnt vmcnt(40)
	v_cndmask_b32_e64 v30, 0, v30, s[4:5]
	s_cselect_b64 s[4:5], -1, 0
	s_and_b64 s[4:5], vcc, s[4:5]
	s_cmp_lt_i32 s8, s76
	s_waitcnt vmcnt(39)
	v_cndmask_b32_e64 v45, 0, v45, s[4:5]
	s_cselect_b64 s[4:5], -1, 0
	s_and_b64 s[4:5], vcc, s[4:5]
	s_cmp_lt_i32 s9, s76
	s_waitcnt vmcnt(38)
	v_cndmask_b32_e64 v44, 0, v44, s[4:5]
	s_cselect_b64 s[4:5], -1, 0
	s_and_b64 s[4:5], vcc, s[4:5]
	s_cmp_lt_i32 s10, s76
	s_waitcnt vmcnt(37)
	v_cndmask_b32_e64 v43, 0, v43, s[4:5]
	s_cselect_b64 s[4:5], -1, 0
	s_and_b64 s[4:5], vcc, s[4:5]
	s_cmp_lt_i32 s11, s76
	s_waitcnt vmcnt(36)
	v_cndmask_b32_e64 v42, 0, v42, s[4:5]
	s_cselect_b64 s[4:5], -1, 0
	s_and_b64 s[4:5], vcc, s[4:5]
	s_cmp_lt_i32 s14, s76
	s_waitcnt vmcnt(35)
	v_cndmask_b32_e64 v41, 0, v41, s[4:5]
	s_cselect_b64 s[4:5], -1, 0
	s_and_b64 s[4:5], vcc, s[4:5]
	s_cmp_lt_i32 s15, s76
	s_waitcnt vmcnt(34)
	v_cndmask_b32_e64 v40, 0, v40, s[4:5]
	s_cselect_b64 s[4:5], -1, 0
	s_and_b64 s[4:5], vcc, s[4:5]
	s_cmp_lt_i32 s16, s76
	s_waitcnt vmcnt(33)
	v_cndmask_b32_e64 v39, 0, v39, s[4:5]
	s_cselect_b64 s[4:5], -1, 0
	s_and_b64 s[4:5], vcc, s[4:5]
	s_cmp_lt_i32 s17, s76
	s_waitcnt vmcnt(32)
	v_cndmask_b32_e64 v38, 0, v38, s[4:5]
	s_cselect_b64 s[4:5], -1, 0
	s_and_b64 s[4:5], vcc, s[4:5]
	s_cmp_lt_i32 s12, s76
	s_waitcnt vmcnt(31)
	v_cndmask_b32_e64 v53, 0, v53, s[4:5]
	s_cselect_b64 s[4:5], -1, 0
	s_and_b64 s[4:5], vcc, s[4:5]
	s_cmp_lt_i32 s13, s76
	s_waitcnt vmcnt(30)
	v_cndmask_b32_e64 v52, 0, v52, s[4:5]
	s_cselect_b64 s[4:5], -1, 0
	s_and_b64 s[4:5], vcc, s[4:5]
	s_cmp_lt_i32 s20, s76
	s_waitcnt vmcnt(29)
	v_cndmask_b32_e64 v51, 0, v51, s[4:5]
	s_cselect_b64 s[4:5], -1, 0
	s_and_b64 s[4:5], vcc, s[4:5]
	s_cmp_lt_i32 s21, s76
	s_waitcnt vmcnt(28)
	v_cndmask_b32_e64 v50, 0, v50, s[4:5]
	s_cselect_b64 s[4:5], -1, 0
	s_and_b64 s[4:5], vcc, s[4:5]
	s_cmp_lt_i32 s24, s76
	s_waitcnt vmcnt(27)
	v_cndmask_b32_e64 v49, 0, v49, s[4:5]
	s_cselect_b64 s[4:5], -1, 0
	s_and_b64 s[4:5], vcc, s[4:5]
	s_cmp_lt_i32 s25, s76
	s_waitcnt vmcnt(26)
	v_cndmask_b32_e64 v48, 0, v48, s[4:5]
	s_cselect_b64 s[4:5], -1, 0
	s_and_b64 s[4:5], vcc, s[4:5]
	s_cmp_lt_i32 s26, s76
	s_waitcnt vmcnt(25)
	v_cndmask_b32_e64 v47, 0, v47, s[4:5]
	s_cselect_b64 s[4:5], -1, 0
	s_and_b64 s[4:5], vcc, s[4:5]
	s_cmp_lt_i32 s27, s76
	s_waitcnt vmcnt(24)
; #define LAS __attribute__((address_space(3)))
; #define LDS_WAIT() asm volatile("s_waitcnt lgkmcnt(0)" ::: "memory")
; __device__ __forceinline__ void conv_load(const ConvItem& ci, int lane, float (&v)[64]) {
;     ...
;     for (int i = 0; i < 64; ++i) { const int k = ci.k0 + i, kk = k < kmax ? k : kmax; v[i] = __builtin_nontemporal_load(base + (size_t)kk * ci.ldw); }
; #pragma unroll
;     for (int i = 0; i < 64; ++i) v[i] = (okc && (ci.k0 + i) < ci.Ksrc) ? v[i] : 0.f;
; }
; __device__ __forceinline__ void conv_store(const ConvItem& ci, LAS float* scr, int lane, const float (&v)[64]) {
;     const int c = lane & 7;
;     f32x4 s0 = {1.f, 1.f, 1.f, 1.f}, s1 = s0;
;     if (ci.ks) { const int kb = ci.k0 + 8 * c < ci.Ksrc - 8 ? ci.k0 + 8 * c : ci.Ksrc - 8; s0 = *(const f32x4*)(ci.ks + kb); s1 = *(const f32x4*)(ci.ks + kb + 4); }
; #pragma unroll
;     for (int i = 0; i < 64; ++i) scr[i * 65 + lane] = v[i];
;     LDS_WAIT(); asm volatile("" ::: "memory");
	v_cndmask_b32_e64 v46, 0, v46, s[4:5]
	s_cselect_b64 s[4:5], -1, 0
	s_and_b64 s[4:5], vcc, s[4:5]
	s_cmp_lt_i32 s18, s76
	s_waitcnt vmcnt(23)
	v_cndmask_b32_e64 v61, 0, v61, s[4:5]
	s_cselect_b64 s[4:5], -1, 0
	s_and_b64 s[4:5], vcc, s[4:5]
	s_cmp_lt_i32 s19, s76
	s_waitcnt vmcnt(22)
	v_cndmask_b32_e64 v60, 0, v60, s[4:5]
	s_cselect_b64 s[4:5], -1, 0
	s_and_b64 s[4:5], vcc, s[4:5]
	s_cmp_lt_i32 s28, s76
	s_waitcnt vmcnt(21)
	v_cndmask_b32_e64 v59, 0, v59, s[4:5]
	s_cselect_b64 s[4:5], -1, 0
	s_and_b64 s[4:5], vcc, s[4:5]
	s_cmp_lt_i32 s29, s76
	s_waitcnt vmcnt(20)
	v_cndmask_b32_e64 v58, 0, v58, s[4:5]
	s_cselect_b64 s[4:5], -1, 0
	s_and_b64 s[4:5], vcc, s[4:5]
	s_cmp_lt_i32 s22, s76
	s_waitcnt vmcnt(19)
	v_cndmask_b32_e64 v57, 0, v57, s[4:5]
	s_cselect_b64 s[4:5], -1, 0
	s_and_b64 s[4:5], vcc, s[4:5]
	s_cmp_lt_i32 s23, s76
	s_waitcnt vmcnt(18)
	v_cndmask_b32_e64 v56, 0, v56, s[4:5]
	s_cselect_b64 s[4:5], -1, 0
	s_and_b64 s[4:5], vcc, s[4:5]
	s_cmp_lt_i32 s30, s76
	s_waitcnt vmcnt(17)
	v_cndmask_b32_e64 v55, 0, v55, s[4:5]
	s_cselect_b64 s[4:5], -1, 0
	s_and_b64 s[4:5], vcc, s[4:5]
	s_cmp_lt_i32 s31, s76
	s_waitcnt vmcnt(16)
	v_cndmask_b32_e64 v54, 0, v54, s[4:5]
	s_cselect_b64 s[4:5], -1, 0
	s_and_b64 s[4:5], vcc, s[4:5]
	s_cmp_lt_i32 s36, s76
	s_waitcnt vmcnt(15)
	v_cndmask_b32_e64 v70, 0, v70, s[4:5]
	s_cselect_b64 s[4:5], -1, 0
	s_and_b64 s[4:5], vcc, s[4:5]
	s_cmp_lt_i32 s37, s76
	s_waitcnt vmcnt(14)
	v_cndmask_b32_e64 v69, 0, v69, s[4:5]
	s_cselect_b64 s[4:5], -1, 0
	s_and_b64 s[4:5], vcc, s[4:5]
	s_cmp_lt_i32 s38, s76
	s_waitcnt vmcnt(13)
	v_cndmask_b32_e64 v68, 0, v68, s[4:5]
	s_cselect_b64 s[4:5], -1, 0
	s_and_b64 s[4:5], vcc, s[4:5]
	s_cmp_lt_i32 s39, s76
	s_waitcnt vmcnt(12)
	v_cndmask_b32_e64 v67, 0, v67, s[4:5]
	s_cselect_b64 s[4:5], -1, 0
	s_and_b64 s[4:5], vcc, s[4:5]
	s_cmp_lt_i32 s34, s76
	s_waitcnt vmcnt(11)
	v_cndmask_b32_e64 v66, 0, v66, s[4:5]
	s_cselect_b64 s[4:5], -1, 0
	s_and_b64 s[4:5], vcc, s[4:5]
	s_cmp_lt_i32 s35, s76
	s_waitcnt vmcnt(10)
	v_cndmask_b32_e64 v64, 0, v64, s[4:5]
	s_cselect_b64 s[4:5], -1, 0
	s_and_b64 s[4:5], vcc, s[4:5]
	s_cmp_lt_i32 s42, s76
	s_waitcnt vmcnt(9)
	v_cndmask_b32_e64 v63, 0, v63, s[4:5]
	s_cselect_b64 s[4:5], -1, 0
	s_and_b64 s[4:5], vcc, s[4:5]
	s_cmp_lt_i32 s43, s76
	s_waitcnt vmcnt(8)
	v_cndmask_b32_e64 v62, 0, v62, s[4:5]
	s_cselect_b64 s[4:5], -1, 0
	s_and_b64 s[4:5], vcc, s[4:5]
	s_cmp_lt_i32 s54, s76
	s_waitcnt vmcnt(7)
	v_cndmask_b32_e64 v65, 0, v65, s[4:5]
	s_cselect_b64 s[4:5], -1, 0
	s_and_b64 s[4:5], vcc, s[4:5]
	s_cmp_lt_i32 s55, s76
	s_waitcnt vmcnt(6)
	v_cndmask_b32_e64 v74, 0, v74, s[4:5]
	s_cselect_b64 s[4:5], -1, 0
	s_and_b64 s[4:5], vcc, s[4:5]
	s_cmp_lt_i32 s46, s76
	ds_write2_b32 v12, v21, v20 offset1:65
	ds_write2_b32 v12, v19, v18 offset0:130 offset1:195
	v_add_u32_e32 v18, 0x400, v12
	s_waitcnt vmcnt(5)
	v_cndmask_b32_e64 v73, 0, v73, s[4:5]
	s_cselect_b64 s[4:5], -1, 0
	ds_write2_b32 v18, v17, v16 offset0:4 offset1:69
	ds_write2_b32 v18, v15, v8 offset0:134 offset1:199
	v_add_u32_e32 v8, 0x800, v12
	s_and_b64 s[4:5], vcc, s[4:5]
	ds_write2_b32 v8, v29, v28 offset0:8 offset1:73
	ds_write2_b32 v8, v27, v26 offset0:138 offset1:203
	v_add_u32_e32 v8, 0xc00, v12
	s_cmp_lt_i32 s47, s76
	ds_write2_b32 v8, v25, v24 offset0:12 offset1:77
	ds_write2_b32 v8, v23, v22 offset0:142 offset1:207
	v_add_u32_e32 v8, 0x1000, v12
	s_waitcnt vmcnt(4)
	v_cndmask_b32_e64 v72, 0, v72, s[4:5]
	s_cselect_b64 s[4:5], -1, 0
	ds_write2_b32 v8, v37, v36 offset0:16 offset1:81
	ds_write2_b32 v8, v35, v34 offset0:146 offset1:211
	v_add_u32_e32 v8, 0x1400, v12
	s_and_b64 s[4:5], vcc, s[4:5]
	ds_write2_b32 v8, v33, v32 offset0:20 offset1:85
	ds_write2_b32 v8, v31, v30 offset0:150 offset1:215
	v_add_u32_e32 v8, 0x1800, v12
	s_cmp_lt_i32 s48, s76
	ds_write2_b32 v8, v45, v44 offset0:24 offset1:89
	ds_write2_b32 v8, v43, v42 offset0:154 offset1:219
	v_add_u32_e32 v8, 0x1c00, v12
	s_waitcnt vmcnt(3)
	v_cndmask_b32_e64 v71, 0, v71, s[4:5]
	s_cselect_b64 s[4:5], -1, 0
	ds_write2_b32 v8, v41, v40 offset0:28 offset1:93
	ds_write2_b32 v8, v39, v38 offset0:158 offset1:223
	v_add_u32_e32 v8, 0x2000, v12
	s_and_b64 s[4:5], vcc, s[4:5]
	ds_write2_b32 v8, v53, v52 offset0:32 offset1:97
	ds_write2_b32 v8, v51, v50 offset0:162 offset1:227
	v_add_u32_e32 v8, 0x2400, v12
	s_cmp_lt_i32 s49, s76
	ds_write2_b32 v8, v49, v48 offset0:36 offset1:101
	ds_write2_b32 v8, v47, v46 offset0:166 offset1:231
	v_add_u32_e32 v8, 0x2800, v12
	s_waitcnt vmcnt(2)
	v_cndmask_b32_e64 v77, 0, v77, s[4:5]
	s_cselect_b64 s[4:5], -1, 0
	ds_write2_b32 v8, v61, v60 offset0:40 offset1:105
	ds_write2_b32 v8, v59, v58 offset0:170 offset1:235
	v_add_u32_e32 v8, 0x2c00, v12
	s_and_b64 s[4:5], vcc, s[4:5]
	ds_write2_b32 v8, v57, v56 offset0:44 offset1:109
	ds_write2_b32 v8, v55, v54 offset0:174 offset1:239
	v_add_u32_e32 v8, 0x3000, v12
	s_cmp_lt_i32 s44, s76
	ds_write2_b32 v8, v70, v69 offset0:48 offset1:113
	ds_write2_b32 v8, v68, v67 offset0:178 offset1:243
	v_add_u32_e32 v8, 0x3400, v12
	s_waitcnt vmcnt(1)
	v_cndmask_b32_e64 v76, 0, v76, s[4:5]
	s_cselect_b64 s[4:5], -1, 0
	ds_write2_b32 v8, v66, v64 offset0:52 offset1:117
	ds_write2_b32 v8, v63, v62 offset0:182 offset1:247
	v_add_u32_e32 v8, 0x3800, v12
	s_and_b64 vcc, vcc, s[4:5]
	ds_write2_b32 v8, v65, v74 offset0:56 offset1:121
	ds_write2_b32 v8, v73, v72 offset0:186 offset1:251
	v_add_u32_e32 v8, 0x3c00, v12
	s_waitcnt vmcnt(0)
	v_cndmask_b32_e32 v75, 0, v75, vcc
	ds_write2_b32 v8, v71, v77 offset0:60 offset1:125
	ds_write2_b32 v8, v76, v75 offset0:190 offset1:255
	s_waitcnt lgkmcnt(0)
; __device__ __forceinline__ unsigned cvt_pk_bf16(float lo, float hi) { unsigned r; asm volatile("v_cvt_pk_bf16_f32 %0, %1, %2" : "=v"(r) : "v"(lo), "v"(hi)); return r; }
; #define LAS __attribute__((address_space(3)))
; #define LDS_WAIT() asm volatile("s_waitcnt lgkmcnt(0)" ::: "memory")
; __device__ __forceinline__ void conv_store(const ConvItem& ci, LAS float* scr, int lane, const float (&v)[64]) {
;     ...
;     LDS_WAIT(); asm volatile("" ::: "memory");
; #pragma unroll
;     for (int j = 0; j < 8; ++j) { const int n = (lane >> 3) + 8 * j; const LAS float* s = scr + (8 * c) * 65 + n;
;         v4u o; o.x = cvt_pk_bf16(s[0 * 65] * s0[0], s[1 * 65] * s0[1]); o.y = cvt_pk_bf16(s[2 * 65] * s0[2], s[3 * 65] * s0[3]); o.z = cvt_pk_bf16(s[4 * 65] * s1[0], s[5 * 65] * s1[1]); o.w = cvt_pk_bf16(s[6 * 65] * s1[2], s[7 * 65] * s1[3]);
;         *(v4u*)(ci.dst + (size_t)(ci.drow0 + n) * ci.ldd + ci.k0 + 8 * c) = o; }
	v_add_u32_e32 v192, 0x400, v14
	ds_read2_b32 v[128:129], v14 offset1:65
	ds_read2_b32 v[130:131], v14 offset0:130 offset1:195
	ds_read2_b32 v[132:133], v192 offset0:4 offset1:69
	ds_read2_b32 v[134:135], v192 offset0:134 offset1:199
	ds_read2_b32 v[136:137], v14 offset0:8 offset1:73
	ds_read2_b32 v[138:139], v14 offset0:138 offset1:203
	ds_read2_b32 v[140:141], v192 offset0:12 offset1:77
	ds_read2_b32 v[142:143], v192 offset0:142 offset1:207
	ds_read2_b32 v[144:145], v14 offset0:16 offset1:81
	ds_read2_b32 v[146:147], v14 offset0:146 offset1:211
	ds_read2_b32 v[148:149], v192 offset0:20 offset1:85
	ds_read2_b32 v[150:151], v192 offset0:150 offset1:215
	ds_read2_b32 v[152:153], v14 offset0:24 offset1:89
	ds_read2_b32 v[154:155], v14 offset0:154 offset1:219
	ds_read2_b32 v[156:157], v192 offset0:28 offset1:93
	ds_read2_b32 v[158:159], v192 offset0:158 offset1:223
	ds_read2_b32 v[160:161], v14 offset0:32 offset1:97
	ds_read2_b32 v[162:163], v14 offset0:162 offset1:227
	ds_read2_b32 v[164:165], v192 offset0:36 offset1:101
	ds_read2_b32 v[166:167], v192 offset0:166 offset1:231
	ds_read2_b32 v[168:169], v14 offset0:40 offset1:105
	ds_read2_b32 v[170:171], v14 offset0:170 offset1:235
	ds_read2_b32 v[172:173], v192 offset0:44 offset1:109
	ds_read2_b32 v[174:175], v192 offset0:174 offset1:239
	ds_read2_b32 v[176:177], v14 offset0:48 offset1:113
	ds_read2_b32 v[178:179], v14 offset0:178 offset1:243
	ds_read2_b32 v[180:181], v192 offset0:52 offset1:117
	ds_read2_b32 v[182:183], v192 offset0:182 offset1:247
	ds_read2_b32 v[184:185], v14 offset0:56 offset1:121
	ds_read2_b32 v[186:187], v14 offset0:186 offset1:251
	ds_read2_b32 v[188:189], v192 offset0:60 offset1:125
	ds_read2_b32 v[190:191], v192 offset0:190 offset1:255
	s_waitcnt lgkmcnt(0)
	v_add_u32_e32 v24, s59, v13
	v_mul_lo_u32 v22, s57, v24
	s_ashr_i32 s59, s58, 31
	v_readlane_b32 s76, v254, 31
	s_waitcnt lgkmcnt(0)
	v_mul_f32_e32 v8, v4, v128
	v_mul_f32_e32 v15, v5, v129
	v_cvt_pk_bf16_f32 v16, v8, v15
	s_add_i32 s3, s3, s33
	s_add_i32 s66, s66, s67
	s_add_i32 s68, s68, s69
	s_add_i32 s70, s70, s71
	s_waitcnt lgkmcnt(0)
	v_mul_f32_e32 v15, v7, v131
	v_mul_f32_e32 v8, v6, v130
	v_cvt_pk_bf16_f32 v17, v8, v15
	v_add_u32_e32 v15, 0x400, v14
	s_add_i32 s72, s72, s73
	s_add_i32 s74, s74, s75
	v_readlane_b32 s78, v254, 33
	v_readlane_b32 s79, v254, 34
	s_waitcnt lgkmcnt(0)
	v_mul_f32_e32 v8, v0, v132
	v_mul_f32_e32 v18, v1, v133
	v_cvt_pk_bf16_f32 v18, v8, v18
	v_readlane_b32 s80, v255, 21
	v_readlane_b32 s77, v254, 32
	s_movk_i32 s78, 0x1580
	v_readlane_b32 s82, v255, 23
	s_waitcnt lgkmcnt(0)
	v_mul_f32_e32 v8, v2, v134
	v_mul_f32_e32 v19, v3, v135
	v_cvt_pk_bf16_f32 v19, v8, v19
	v_ashrrev_i32_e32 v8, 31, v24
	v_mul_lo_u32 v8, s56, v8
	v_mad_u64_u32 v[20:21], s[4:5], s56, v24, 0
	v_add3_u32 v21, v21, v8, v22
	v_lshl_add_u64 v[20:21], v[20:21], 1, s[60:61]
	s_lshl_b64 s[4:5], s[58:59], 1
	v_lshl_add_u64 v[20:21], v[20:21], 0, s[4:5]
	v_lshlrev_b32_e32 v8, 1, v10
	v_lshl_add_u64 v[20:21], v[20:21], 0, v[8:9]
	global_store_dwordx4 v[20:21], v[16:19], off nt
	s_cmpk_lt_i32 s3, 26496
	v_readlane_b32 s83, v255, 24
	s_waitcnt lgkmcnt(0)
	v_mul_f32_e32 v16, v4, v136
	v_mul_f32_e32 v17, v5, v137
	v_cvt_pk_bf16_f32 v16, v16, v17
	s_mov_b32 s79, 0x3f22f983
	s_mov_b32 s85, 0xbfc90fda
	s_brev_b32 s86, 1
	s_movk_i32 s87, 0x1f8
	s_waitcnt lgkmcnt(0)
	v_mul_f32_e32 v17, v6, v138
	v_mul_f32_e32 v18, v7, v139
	v_cvt_pk_bf16_f32 v17, v17, v18
	s_mov_b64 s[88:89], 0x80
	s_mov_b64 s[92:93], 0x4000
	s_mov_b64 s[94:95], 0x4800
	v_readlane_b32 s81, v255, 22
	s_waitcnt lgkmcnt(0)
	v_mul_f32_e32 v18, v0, v140
	v_mul_f32_e32 v19, v1, v141
	v_cvt_pk_bf16_f32 v18, v18, v19
	s_waitcnt lgkmcnt(0)
	v_mul_f32_e32 v19, v2, v142
	v_mul_f32_e32 v20, v3, v143
	v_cvt_pk_bf16_f32 v19, v19, v20
	v_add_u32_e32 v20, 8, v24
	v_ashrrev_i32_e32 v21, 31, v20
	v_mul_lo_u32 v22, s56, v21
	v_mul_lo_u32 v23, s57, v20
	v_mad_u64_u32 v[20:21], s[6:7], s56, v20, 0
	v_add3_u32 v21, v21, v22, v23
	v_lshl_add_u64 v[20:21], v[20:21], 1, s[60:61]
	v_lshl_add_u64 v[20:21], v[20:21], 0, s[4:5]
	v_lshl_add_u64 v[20:21], v[20:21], 0, v[8:9]
	global_store_dwordx4 v[20:21], v[16:19], off nt
	s_waitcnt lgkmcnt(0)
	s_nop 0
	v_mul_f32_e32 v16, v4, v144
	v_mul_f32_e32 v17, v5, v145
	v_cvt_pk_bf16_f32 v16, v16, v17
	s_waitcnt lgkmcnt(0)
	v_mul_f32_e32 v17, v6, v146
	v_mul_f32_e32 v18, v7, v147
	v_cvt_pk_bf16_f32 v17, v17, v18
	s_waitcnt lgkmcnt(0)
	v_mul_f32_e32 v18, v0, v148
	v_mul_f32_e32 v19, v1, v149
	v_cvt_pk_bf16_f32 v18, v18, v19
	s_waitcnt lgkmcnt(0)
; __device__ __forceinline__ unsigned cvt_pk_bf16(float lo, float hi) { unsigned r; asm volatile("v_cvt_pk_bf16_f32 %0, %1, %2" : "=v"(r) : "v"(lo), "v"(hi)); return r; }
; #define LAS __attribute__((address_space(3)))
; #define LDS_WAIT() asm volatile("s_waitcnt lgkmcnt(0)" ::: "memory")
; __device__ __forceinline__ void conv_store(const ConvItem& ci, LAS float* scr, int lane, const float (&v)[64]) {
;     ...
;     for (int j = 0; j < 8; ++j) { const int n = (lane >> 3) + 8 * j; const LAS float* s = scr + (8 * c) * 65 + n;
;         v4u o; o.x = cvt_pk_bf16(s[0 * 65] * s0[0], s[1 * 65] * s0[1]); o.y = cvt_pk_bf16(s[2 * 65] * s0[2], s[3 * 65] * s0[3]); o.z = cvt_pk_bf16(s[4 * 65] * s1[0], s[5 * 65] * s1[1]); o.w = cvt_pk_bf16(s[6 * 65] * s1[2], s[7 * 65] * s1[3]);
;         *(v4u*)(ci.dst + (size_t)(ci.drow0 + n) * ci.ldd + ci.k0 + 8 * c) = o; }
;     LDS_WAIT(); asm volatile("" ::: "memory");
; }
	v_mul_f32_e32 v19, v2, v150
	v_mul_f32_e32 v20, v3, v151
	v_cvt_pk_bf16_f32 v19, v19, v20
	v_add_u32_e32 v20, 16, v24
	v_ashrrev_i32_e32 v21, 31, v20
	v_mul_lo_u32 v22, s56, v21
	v_mul_lo_u32 v23, s57, v20
	v_mad_u64_u32 v[20:21], s[6:7], s56, v20, 0
	v_add3_u32 v21, v21, v22, v23
	v_lshl_add_u64 v[20:21], v[20:21], 1, s[60:61]
	v_lshl_add_u64 v[20:21], v[20:21], 0, s[4:5]
	v_lshl_add_u64 v[20:21], v[20:21], 0, v[8:9]
	global_store_dwordx4 v[20:21], v[16:19], off nt
	s_waitcnt lgkmcnt(0)
	s_nop 0
	v_mul_f32_e32 v16, v4, v152
	v_mul_f32_e32 v17, v5, v153
	v_cvt_pk_bf16_f32 v16, v16, v17
	s_waitcnt lgkmcnt(0)
	v_mul_f32_e32 v17, v6, v154
	v_mul_f32_e32 v18, v7, v155
	v_cvt_pk_bf16_f32 v17, v17, v18
	s_waitcnt lgkmcnt(0)
	v_mul_f32_e32 v18, v0, v156
	v_mul_f32_e32 v19, v1, v157
	v_cvt_pk_bf16_f32 v18, v18, v19
	s_waitcnt lgkmcnt(0)
	v_mul_f32_e32 v19, v2, v158
	v_mul_f32_e32 v20, v3, v159
	v_cvt_pk_bf16_f32 v19, v19, v20
	v_add_u32_e32 v20, 24, v24
	v_ashrrev_i32_e32 v21, 31, v20
	v_mul_lo_u32 v22, s56, v21
	v_mul_lo_u32 v23, s57, v20
	v_mad_u64_u32 v[20:21], s[6:7], s56, v20, 0
	v_add3_u32 v21, v21, v22, v23
	v_lshl_add_u64 v[20:21], v[20:21], 1, s[60:61]
	v_lshl_add_u64 v[20:21], v[20:21], 0, s[4:5]
	v_lshl_add_u64 v[20:21], v[20:21], 0, v[8:9]
	global_store_dwordx4 v[20:21], v[16:19], off nt
	s_waitcnt lgkmcnt(0)
	s_nop 0
	v_mul_f32_e32 v16, v4, v160
	v_mul_f32_e32 v17, v5, v161
	v_cvt_pk_bf16_f32 v16, v16, v17
	s_waitcnt lgkmcnt(0)
	v_mul_f32_e32 v17, v6, v162
	v_mul_f32_e32 v18, v7, v163
	v_cvt_pk_bf16_f32 v17, v17, v18
	s_waitcnt lgkmcnt(0)
	v_mul_f32_e32 v18, v0, v164
	v_mul_f32_e32 v19, v1, v165
	v_cvt_pk_bf16_f32 v18, v18, v19
	s_waitcnt lgkmcnt(0)
	v_mul_f32_e32 v19, v2, v166
	v_mul_f32_e32 v20, v3, v167
	v_cvt_pk_bf16_f32 v19, v19, v20
	v_add_u32_e32 v20, 32, v24
	v_ashrrev_i32_e32 v21, 31, v20
	v_mul_lo_u32 v22, s56, v21
	v_mul_lo_u32 v23, s57, v20
	v_mad_u64_u32 v[20:21], s[6:7], s56, v20, 0
	v_add3_u32 v21, v21, v22, v23
	v_lshl_add_u64 v[20:21], v[20:21], 1, s[60:61]
	v_lshl_add_u64 v[20:21], v[20:21], 0, s[4:5]
	v_lshl_add_u64 v[20:21], v[20:21], 0, v[8:9]
	global_store_dwordx4 v[20:21], v[16:19], off nt
	s_waitcnt lgkmcnt(0)
	s_nop 0
	v_mul_f32_e32 v16, v4, v168
	v_mul_f32_e32 v17, v5, v169
	v_cvt_pk_bf16_f32 v16, v16, v17
	s_waitcnt lgkmcnt(0)
	v_mul_f32_e32 v17, v6, v170
	v_mul_f32_e32 v18, v7, v171
	v_cvt_pk_bf16_f32 v17, v17, v18
	s_waitcnt lgkmcnt(0)
	v_mul_f32_e32 v18, v0, v172
	v_mul_f32_e32 v19, v1, v173
	v_cvt_pk_bf16_f32 v18, v18, v19
	s_waitcnt lgkmcnt(0)
	v_mul_f32_e32 v19, v2, v174
	v_mul_f32_e32 v20, v3, v175
	v_cvt_pk_bf16_f32 v19, v19, v20
	v_add_u32_e32 v20, 40, v24
	v_ashrrev_i32_e32 v21, 31, v20
	v_mul_lo_u32 v22, s56, v21
	v_mul_lo_u32 v23, s57, v20
	v_mad_u64_u32 v[20:21], s[6:7], s56, v20, 0
	v_add3_u32 v21, v21, v22, v23
	v_lshl_add_u64 v[20:21], v[20:21], 1, s[60:61]
	v_lshl_add_u64 v[20:21], v[20:21], 0, s[4:5]
	v_lshl_add_u64 v[20:21], v[20:21], 0, v[8:9]
	global_store_dwordx4 v[20:21], v[16:19], off nt
	s_waitcnt lgkmcnt(0)
	s_nop 0
	v_mul_f32_e32 v16, v4, v176
	v_mul_f32_e32 v17, v5, v177
	v_cvt_pk_bf16_f32 v16, v16, v17
	s_waitcnt lgkmcnt(0)
	v_mul_f32_e32 v17, v6, v178
	v_mul_f32_e32 v18, v7, v179
	v_cvt_pk_bf16_f32 v17, v17, v18
	s_waitcnt lgkmcnt(0)
	v_mul_f32_e32 v18, v0, v180
	v_mul_f32_e32 v19, v1, v181
	v_cvt_pk_bf16_f32 v18, v18, v19
	s_waitcnt lgkmcnt(0)
	v_mul_f32_e32 v19, v2, v182
	v_mul_f32_e32 v20, v3, v183
	v_cvt_pk_bf16_f32 v19, v19, v20
	v_add_u32_e32 v20, 48, v24
	v_ashrrev_i32_e32 v21, 31, v20
	v_mul_lo_u32 v22, s56, v21
	v_mul_lo_u32 v23, s57, v20
	v_mad_u64_u32 v[20:21], s[6:7], s56, v20, 0
	v_add3_u32 v21, v21, v22, v23
	v_lshl_add_u64 v[20:21], v[20:21], 1, s[60:61]
	v_lshl_add_u64 v[20:21], v[20:21], 0, s[4:5]
	v_lshl_add_u64 v[20:21], v[20:21], 0, v[8:9]
	global_store_dwordx4 v[20:21], v[16:19], off nt
	s_waitcnt lgkmcnt(0)
	v_mul_f32_e32 v4, v4, v184
	v_mul_f32_e32 v5, v5, v185
	v_cvt_pk_bf16_f32 v4, v4, v5
	s_waitcnt lgkmcnt(0)
	v_mul_f32_e32 v5, v6, v186
	v_mul_f32_e32 v6, v7, v187
	v_cvt_pk_bf16_f32 v5, v5, v6
	s_waitcnt lgkmcnt(0)
	v_mul_f32_e32 v0, v0, v188
	v_mul_f32_e32 v1, v1, v189
	v_cvt_pk_bf16_f32 v6, v0, v1
	s_waitcnt lgkmcnt(0)
	v_mul_f32_e32 v0, v2, v190
	v_mul_f32_e32 v1, v3, v191
	v_cvt_pk_bf16_f32 v7, v0, v1
	v_add_u32_e32 v0, 56, v24
	v_ashrrev_i32_e32 v1, 31, v0
	v_mul_lo_u32 v2, s56, v1
	v_mul_lo_u32 v3, s57, v0
	v_mad_u64_u32 v[0:1], s[6:7], s56, v0, 0
	v_add3_u32 v1, v1, v2, v3
	v_lshl_add_u64 v[0:1], v[0:1], 1, s[60:61]
	v_lshl_add_u64 v[0:1], v[0:1], 0, s[4:5]
	v_lshl_add_u64 v[0:1], v[0:1], 0, v[8:9]
	global_store_dwordx4 v[0:1], v[4:7], off nt
	s_waitcnt lgkmcnt(0)
	s_cbranch_scc0 .Lcvp11_ret

; __device__ __forceinline__ void conv_load(const ConvItem& ci, int lane, float (&v)[64]) {
;     const bool okc = ci.srcc >= 0 && (ci.srcc + lane) < ci.ncols;
;     const float* base = ci.W + (okc ? ci.srcc + lane : 0);
;     const int kmax = ci.Ksrc - 1;
; #pragma unroll
;     for (int i = 0; i < 64; ++i) { const int k = ci.k0 + i, kk = k < kmax ? k : kmax; v[i] = __builtin_nontemporal_load(base + (size_t)kk * ci.ldw); }
; #pragma unroll
;     for (int i = 0; i < 64; ++i) v[i] = (okc && (ci.k0 + i) < ci.Ksrc) ? v[i] : 0.f;
; }
.Lcvp30_30:
	s_cmp_lt_i32 s58, s76
	s_cselect_b64 s[4:5], -1, 0
	s_and_b64 s[4:5], vcc, s[4:5]
	s_cmp_lt_i32 s64, s76
	s_waitcnt vmcnt(62)
	v_cndmask_b32_e64 v21, 0, v21, s[4:5]
	s_cselect_b64 s[4:5], -1, 0
	s_and_b64 s[4:5], vcc, s[4:5]
	s_cmp_lt_i32 s65, s76
	v_cndmask_b32_e64 v20, 0, v20, s[4:5]
	s_cselect_b64 s[4:5], -1, 0
	s_and_b64 s[4:5], vcc, s[4:5]
	s_cmp_lt_i32 s78, s76
	s_waitcnt vmcnt(61)
	v_cndmask_b32_e64 v19, 0, v19, s[4:5]
	s_cselect_b64 s[4:5], -1, 0
	s_and_b64 s[4:5], vcc, s[4:5]
	s_cmp_lt_i32 s79, s76
	s_waitcnt vmcnt(60)
	v_cndmask_b32_e64 v18, 0, v18, s[4:5]
	s_cselect_b64 s[4:5], -1, 0
	s_and_b64 s[4:5], vcc, s[4:5]
	s_cmp_lt_i32 s80, s76
	s_waitcnt vmcnt(59)
	v_cndmask_b32_e64 v17, 0, v17, s[4:5]
	s_cselect_b64 s[4:5], -1, 0
	s_and_b64 s[4:5], vcc, s[4:5]
	s_cmp_lt_i32 s81, s76
	s_waitcnt vmcnt(58)
	v_cndmask_b32_e64 v16, 0, v16, s[4:5]
	s_cselect_b64 s[4:5], -1, 0
	s_and_b64 s[4:5], vcc, s[4:5]
	s_cmp_lt_i32 s82, s76
	s_waitcnt vmcnt(57)
	v_cndmask_b32_e64 v15, 0, v15, s[4:5]
	s_cselect_b64 s[4:5], -1, 0
	s_and_b64 s[4:5], vcc, s[4:5]
	s_cmp_lt_i32 s83, s76
	s_waitcnt vmcnt(56)
	v_cndmask_b32_e64 v8, 0, v8, s[4:5]
	s_cselect_b64 s[4:5], -1, 0
	s_and_b64 s[4:5], vcc, s[4:5]
	s_cmp_lt_i32 s85, s76
	s_waitcnt vmcnt(55)
	v_cndmask_b32_e64 v29, 0, v29, s[4:5]
	s_cselect_b64 s[4:5], -1, 0
	s_and_b64 s[4:5], vcc, s[4:5]
	s_cmp_lt_i32 s86, s76
	s_waitcnt vmcnt(54)
	v_cndmask_b32_e64 v28, 0, v28, s[4:5]
	s_cselect_b64 s[4:5], -1, 0
	s_and_b64 s[4:5], vcc, s[4:5]
	s_cmp_lt_i32 s87, s76
	s_waitcnt vmcnt(53)
	v_cndmask_b32_e64 v27, 0, v27, s[4:5]
	s_cselect_b64 s[4:5], -1, 0
	s_and_b64 s[4:5], vcc, s[4:5]
	s_cmp_lt_i32 s88, s76
	s_waitcnt vmcnt(52)
	v_cndmask_b32_e64 v26, 0, v26, s[4:5]
	s_cselect_b64 s[4:5], -1, 0
	s_and_b64 s[4:5], vcc, s[4:5]
	s_cmp_lt_i32 s89, s76
	s_waitcnt vmcnt(51)
	v_cndmask_b32_e64 v25, 0, v25, s[4:5]
	s_cselect_b64 s[4:5], -1, 0
	s_and_b64 s[4:5], vcc, s[4:5]
	s_cmp_lt_i32 s90, s76
	s_waitcnt vmcnt(50)
	v_cndmask_b32_e64 v24, 0, v24, s[4:5]
	s_cselect_b64 s[4:5], -1, 0
	s_and_b64 s[4:5], vcc, s[4:5]
	s_cmp_lt_i32 s92, s76
	s_waitcnt vmcnt(49)
	v_cndmask_b32_e64 v23, 0, v23, s[4:5]
	s_cselect_b64 s[4:5], -1, 0
	s_and_b64 s[4:5], vcc, s[4:5]
	s_cmp_lt_i32 s93, s76
	s_waitcnt vmcnt(48)
	v_cndmask_b32_e64 v22, 0, v22, s[4:5]
	s_cselect_b64 s[4:5], -1, 0
	s_and_b64 s[4:5], vcc, s[4:5]
	s_cmp_lt_i32 s94, s76
	s_waitcnt vmcnt(47)
	v_cndmask_b32_e64 v37, 0, v37, s[4:5]
	s_cselect_b64 s[4:5], -1, 0
	s_and_b64 s[4:5], vcc, s[4:5]
	s_cmp_lt_i32 s95, s76
	s_waitcnt vmcnt(46)
	v_cndmask_b32_e64 v36, 0, v36, s[4:5]
	s_cselect_b64 s[4:5], -1, 0
	s_and_b64 s[4:5], vcc, s[4:5]
	s_cmp_lt_i32 s50, s76
	s_waitcnt vmcnt(45)
	v_cndmask_b32_e64 v35, 0, v35, s[4:5]
	s_cselect_b64 s[4:5], -1, 0
	s_and_b64 s[4:5], vcc, s[4:5]
	s_cmp_lt_i32 s51, s76
	s_waitcnt vmcnt(44)
	v_cndmask_b32_e64 v34, 0, v34, s[4:5]
	s_cselect_b64 s[4:5], -1, 0
	s_and_b64 s[4:5], vcc, s[4:5]
	s_cmp_lt_i32 s52, s76
	s_waitcnt vmcnt(43)
	v_cndmask_b32_e64 v33, 0, v33, s[4:5]
	s_cselect_b64 s[4:5], -1, 0
	s_and_b64 s[4:5], vcc, s[4:5]
	s_cmp_lt_i32 s53, s76
	s_waitcnt vmcnt(42)
	v_cndmask_b32_e64 v32, 0, v32, s[4:5]
	s_cselect_b64 s[4:5], -1, 0
	s_and_b64 s[4:5], vcc, s[4:5]
	s_cmp_lt_i32 s6, s76
	s_waitcnt vmcnt(41)
	v_cndmask_b32_e64 v31, 0, v31, s[4:5]
	s_cselect_b64 s[4:5], -1, 0
	s_and_b64 s[4:5], vcc, s[4:5]
	s_cmp_lt_i32 s7, s76
	s_waitcnt vmcnt(40)
	v_cndmask_b32_e64 v30, 0, v30, s[4:5]
	s_cselect_b64 s[4:5], -1, 0
	s_and_b64 s[4:5], vcc, s[4:5]
	s_cmp_lt_i32 s8, s76
	s_waitcnt vmcnt(39)
	v_cndmask_b32_e64 v45, 0, v45, s[4:5]
	s_cselect_b64 s[4:5], -1, 0
	s_and_b64 s[4:5], vcc, s[4:5]
	s_cmp_lt_i32 s9, s76
	s_waitcnt vmcnt(38)
	v_cndmask_b32_e64 v44, 0, v44, s[4:5]
	s_cselect_b64 s[4:5], -1, 0
	s_and_b64 s[4:5], vcc, s[4:5]
	s_cmp_lt_i32 s10, s76
	s_waitcnt vmcnt(37)
	v_cndmask_b32_e64 v43, 0, v43, s[4:5]
	s_cselect_b64 s[4:5], -1, 0
	s_and_b64 s[4:5], vcc, s[4:5]
	s_cmp_lt_i32 s11, s76
	s_waitcnt vmcnt(36)
	v_cndmask_b32_e64 v42, 0, v42, s[4:5]
	s_cselect_b64 s[4:5], -1, 0
	s_and_b64 s[4:5], vcc, s[4:5]
	s_cmp_lt_i32 s14, s76
	s_waitcnt vmcnt(35)
	v_cndmask_b32_e64 v41, 0, v41, s[4:5]
	s_cselect_b64 s[4:5], -1, 0
	s_and_b64 s[4:5], vcc, s[4:5]
	s_cmp_lt_i32 s15, s76
	s_waitcnt vmcnt(34)
	v_cndmask_b32_e64 v40, 0, v40, s[4:5]
	s_cselect_b64 s[4:5], -1, 0
	s_and_b64 s[4:5], vcc, s[4:5]
	s_cmp_lt_i32 s16, s76
	s_waitcnt vmcnt(33)
	v_cndmask_b32_e64 v39, 0, v39, s[4:5]
	s_cselect_b64 s[4:5], -1, 0
	s_and_b64 s[4:5], vcc, s[4:5]
	s_cmp_lt_i32 s17, s76
	s_waitcnt vmcnt(32)
	v_cndmask_b32_e64 v38, 0, v38, s[4:5]
	s_cselect_b64 s[4:5], -1, 0
	s_and_b64 s[4:5], vcc, s[4:5]
	s_cmp_lt_i32 s12, s76
	s_waitcnt vmcnt(31)
	v_cndmask_b32_e64 v53, 0, v53, s[4:5]
	s_cselect_b64 s[4:5], -1, 0
	s_and_b64 s[4:5], vcc, s[4:5]
	s_cmp_lt_i32 s13, s76
	s_waitcnt vmcnt(30)
	v_cndmask_b32_e64 v52, 0, v52, s[4:5]
	s_cselect_b64 s[4:5], -1, 0
	s_and_b64 s[4:5], vcc, s[4:5]
	s_cmp_lt_i32 s20, s76
	s_waitcnt vmcnt(29)
	v_cndmask_b32_e64 v51, 0, v51, s[4:5]
	s_cselect_b64 s[4:5], -1, 0
	s_and_b64 s[4:5], vcc, s[4:5]
	s_cmp_lt_i32 s21, s76
	s_waitcnt vmcnt(28)
	v_cndmask_b32_e64 v50, 0, v50, s[4:5]
	s_cselect_b64 s[4:5], -1, 0
	s_and_b64 s[4:5], vcc, s[4:5]
	s_cmp_lt_i32 s24, s76
	s_waitcnt vmcnt(27)
	v_cndmask_b32_e64 v49, 0, v49, s[4:5]
	s_cselect_b64 s[4:5], -1, 0
	s_and_b64 s[4:5], vcc, s[4:5]
	s_cmp_lt_i32 s25, s76
	s_waitcnt vmcnt(26)
	v_cndmask_b32_e64 v48, 0, v48, s[4:5]
	s_cselect_b64 s[4:5], -1, 0
	s_and_b64 s[4:5], vcc, s[4:5]
	s_cmp_lt_i32 s26, s76
	s_waitcnt vmcnt(25)
	v_cndmask_b32_e64 v47, 0, v47, s[4:5]
	s_cselect_b64 s[4:5], -1, 0
	s_and_b64 s[4:5], vcc, s[4:5]
	s_cmp_lt_i32 s27, s76
	s_waitcnt vmcnt(24)
; #define LAS __attribute__((address_space(3)))
; #define LDS_WAIT() asm volatile("s_waitcnt lgkmcnt(0)" ::: "memory")
; __device__ __forceinline__ void conv_load(const ConvItem& ci, int lane, float (&v)[64]) {
;     ...
;     for (int i = 0; i < 64; ++i) { const int k = ci.k0 + i, kk = k < kmax ? k : kmax; v[i] = __builtin_nontemporal_load(base + (size_t)kk * ci.ldw); }
; #pragma unroll
;     for (int i = 0; i < 64; ++i) v[i] = (okc && (ci.k0 + i) < ci.Ksrc) ? v[i] : 0.f;
; }
; __device__ __forceinline__ void conv_store(const ConvItem& ci, LAS float* scr, int lane, const float (&v)[64]) {
;     const int c = lane & 7;
;     f32x4 s0 = {1.f, 1.f, 1.f, 1.f}, s1 = s0;
;     if (ci.ks) { const int kb = ci.k0 + 8 * c < ci.Ksrc - 8 ? ci.k0 + 8 * c : ci.Ksrc - 8; s0 = *(const f32x4*)(ci.ks + kb); s1 = *(const f32x4*)(ci.ks + kb + 4); }
; #pragma unroll
;     for (int i = 0; i < 64; ++i) scr[i * 65 + lane] = v[i];
;     LDS_WAIT(); asm volatile("" ::: "memory");
	v_cndmask_b32_e64 v46, 0, v46, s[4:5]
	s_cselect_b64 s[4:5], -1, 0
	s_and_b64 s[4:5], vcc, s[4:5]
	s_cmp_lt_i32 s18, s76
	s_waitcnt vmcnt(23)
	v_cndmask_b32_e64 v61, 0, v61, s[4:5]
	s_cselect_b64 s[4:5], -1, 0
	s_and_b64 s[4:5], vcc, s[4:5]
	s_cmp_lt_i32 s19, s76
	s_waitcnt vmcnt(22)
	v_cndmask_b32_e64 v60, 0, v60, s[4:5]
	s_cselect_b64 s[4:5], -1, 0
	s_and_b64 s[4:5], vcc, s[4:5]
	s_cmp_lt_i32 s28, s76
	s_waitcnt vmcnt(21)
	v_cndmask_b32_e64 v59, 0, v59, s[4:5]
	s_cselect_b64 s[4:5], -1, 0
	s_and_b64 s[4:5], vcc, s[4:5]
	s_cmp_lt_i32 s29, s76
	s_waitcnt vmcnt(20)
	v_cndmask_b32_e64 v58, 0, v58, s[4:5]
	s_cselect_b64 s[4:5], -1, 0
	s_and_b64 s[4:5], vcc, s[4:5]
	s_cmp_lt_i32 s22, s76
	s_waitcnt vmcnt(19)
	v_cndmask_b32_e64 v57, 0, v57, s[4:5]
	s_cselect_b64 s[4:5], -1, 0
	s_and_b64 s[4:5], vcc, s[4:5]
	s_cmp_lt_i32 s23, s76
	s_waitcnt vmcnt(18)
	v_cndmask_b32_e64 v56, 0, v56, s[4:5]
	s_cselect_b64 s[4:5], -1, 0
	s_and_b64 s[4:5], vcc, s[4:5]
	s_cmp_lt_i32 s30, s76
	s_waitcnt vmcnt(17)
	v_cndmask_b32_e64 v55, 0, v55, s[4:5]
	s_cselect_b64 s[4:5], -1, 0
	s_and_b64 s[4:5], vcc, s[4:5]
	s_cmp_lt_i32 s31, s76
	s_waitcnt vmcnt(16)
	v_cndmask_b32_e64 v54, 0, v54, s[4:5]
	s_cselect_b64 s[4:5], -1, 0
	s_and_b64 s[4:5], vcc, s[4:5]
	s_cmp_lt_i32 s36, s76
	s_waitcnt vmcnt(15)
	v_cndmask_b32_e64 v70, 0, v70, s[4:5]
	s_cselect_b64 s[4:5], -1, 0
	s_and_b64 s[4:5], vcc, s[4:5]
	s_cmp_lt_i32 s37, s76
	s_waitcnt vmcnt(14)
	v_cndmask_b32_e64 v69, 0, v69, s[4:5]
	s_cselect_b64 s[4:5], -1, 0
	s_and_b64 s[4:5], vcc, s[4:5]
	s_cmp_lt_i32 s38, s76
	s_waitcnt vmcnt(13)
	v_cndmask_b32_e64 v68, 0, v68, s[4:5]
	s_cselect_b64 s[4:5], -1, 0
	s_and_b64 s[4:5], vcc, s[4:5]
	s_cmp_lt_i32 s39, s76
	s_waitcnt vmcnt(12)
	v_cndmask_b32_e64 v67, 0, v67, s[4:5]
	s_cselect_b64 s[4:5], -1, 0
	s_and_b64 s[4:5], vcc, s[4:5]
	s_cmp_lt_i32 s34, s76
	s_waitcnt vmcnt(11)
	v_cndmask_b32_e64 v66, 0, v66, s[4:5]
	s_cselect_b64 s[4:5], -1, 0
	s_and_b64 s[4:5], vcc, s[4:5]
	s_cmp_lt_i32 s35, s76
	s_waitcnt vmcnt(10)
	v_cndmask_b32_e64 v64, 0, v64, s[4:5]
	s_cselect_b64 s[4:5], -1, 0
	s_and_b64 s[4:5], vcc, s[4:5]
	s_cmp_lt_i32 s42, s76
	s_waitcnt vmcnt(9)
	v_cndmask_b32_e64 v63, 0, v63, s[4:5]
	s_cselect_b64 s[4:5], -1, 0
	s_and_b64 s[4:5], vcc, s[4:5]
	s_cmp_lt_i32 s43, s76
	s_waitcnt vmcnt(8)
	v_cndmask_b32_e64 v62, 0, v62, s[4:5]
	s_cselect_b64 s[4:5], -1, 0
	s_and_b64 s[4:5], vcc, s[4:5]
	s_cmp_lt_i32 s54, s76
	s_waitcnt vmcnt(7)
	v_cndmask_b32_e64 v65, 0, v65, s[4:5]
	s_cselect_b64 s[4:5], -1, 0
	s_and_b64 s[4:5], vcc, s[4:5]
	s_cmp_lt_i32 s55, s76
	s_waitcnt vmcnt(6)
	v_cndmask_b32_e64 v74, 0, v74, s[4:5]
	s_cselect_b64 s[4:5], -1, 0
	s_and_b64 s[4:5], vcc, s[4:5]
	s_cmp_lt_i32 s46, s76
	ds_write2_b32 v12, v21, v20 offset1:65
	ds_write2_b32 v12, v19, v18 offset0:130 offset1:195
	v_add_u32_e32 v18, 0x400, v12
	s_waitcnt vmcnt(5)
	v_cndmask_b32_e64 v73, 0, v73, s[4:5]
	s_cselect_b64 s[4:5], -1, 0
	ds_write2_b32 v18, v17, v16 offset0:4 offset1:69
	ds_write2_b32 v18, v15, v8 offset0:134 offset1:199
	v_add_u32_e32 v8, 0x800, v12
	s_and_b64 s[4:5], vcc, s[4:5]
	ds_write2_b32 v8, v29, v28 offset0:8 offset1:73
	ds_write2_b32 v8, v27, v26 offset0:138 offset1:203
	v_add_u32_e32 v8, 0xc00, v12
	s_cmp_lt_i32 s47, s76
	ds_write2_b32 v8, v25, v24 offset0:12 offset1:77
	ds_write2_b32 v8, v23, v22 offset0:142 offset1:207
	v_add_u32_e32 v8, 0x1000, v12
	s_waitcnt vmcnt(4)
	v_cndmask_b32_e64 v72, 0, v72, s[4:5]
	s_cselect_b64 s[4:5], -1, 0
	ds_write2_b32 v8, v37, v36 offset0:16 offset1:81
	ds_write2_b32 v8, v35, v34 offset0:146 offset1:211
	v_add_u32_e32 v8, 0x1400, v12
	s_and_b64 s[4:5], vcc, s[4:5]
	ds_write2_b32 v8, v33, v32 offset0:20 offset1:85
	ds_write2_b32 v8, v31, v30 offset0:150 offset1:215
	v_add_u32_e32 v8, 0x1800, v12
	s_cmp_lt_i32 s48, s76
	ds_write2_b32 v8, v45, v44 offset0:24 offset1:89
	ds_write2_b32 v8, v43, v42 offset0:154 offset1:219
	v_add_u32_e32 v8, 0x1c00, v12
	s_waitcnt vmcnt(3)
	v_cndmask_b32_e64 v71, 0, v71, s[4:5]
	s_cselect_b64 s[4:5], -1, 0
	ds_write2_b32 v8, v41, v40 offset0:28 offset1:93
	ds_write2_b32 v8, v39, v38 offset0:158 offset1:223
	v_add_u32_e32 v8, 0x2000, v12
	s_and_b64 s[4:5], vcc, s[4:5]
	ds_write2_b32 v8, v53, v52 offset0:32 offset1:97
	ds_write2_b32 v8, v51, v50 offset0:162 offset1:227
	v_add_u32_e32 v8, 0x2400, v12
	s_cmp_lt_i32 s49, s76
	ds_write2_b32 v8, v49, v48 offset0:36 offset1:101
	ds_write2_b32 v8, v47, v46 offset0:166 offset1:231
	v_add_u32_e32 v8, 0x2800, v12
	s_waitcnt vmcnt(2)
	v_cndmask_b32_e64 v77, 0, v77, s[4:5]
	s_cselect_b64 s[4:5], -1, 0
	ds_write2_b32 v8, v61, v60 offset0:40 offset1:105
	ds_write2_b32 v8, v59, v58 offset0:170 offset1:235
	v_add_u32_e32 v8, 0x2c00, v12
	s_and_b64 s[4:5], vcc, s[4:5]
	ds_write2_b32 v8, v57, v56 offset0:44 offset1:109
	ds_write2_b32 v8, v55, v54 offset0:174 offset1:239
	v_add_u32_e32 v8, 0x3000, v12
	s_cmp_lt_i32 s44, s76
	ds_write2_b32 v8, v70, v69 offset0:48 offset1:113
	ds_write2_b32 v8, v68, v67 offset0:178 offset1:243
	v_add_u32_e32 v8, 0x3400, v12
	s_waitcnt vmcnt(1)
	v_cndmask_b32_e64 v76, 0, v76, s[4:5]
	s_cselect_b64 s[4:5], -1, 0
	ds_write2_b32 v8, v66, v64 offset0:52 offset1:117
	ds_write2_b32 v8, v63, v62 offset0:182 offset1:247
	v_add_u32_e32 v8, 0x3800, v12
	s_and_b64 vcc, vcc, s[4:5]
	ds_write2_b32 v8, v65, v74 offset0:56 offset1:121
	ds_write2_b32 v8, v73, v72 offset0:186 offset1:251
	v_add_u32_e32 v8, 0x3c00, v12
	s_waitcnt vmcnt(0)
	v_cndmask_b32_e32 v75, 0, v75, vcc
	ds_write2_b32 v8, v71, v77 offset0:60 offset1:125
	ds_write2_b32 v8, v76, v75 offset0:190 offset1:255
	s_waitcnt lgkmcnt(0)
; __device__ __forceinline__ unsigned cvt_pk_bf16(float lo, float hi) { unsigned r; asm volatile("v_cvt_pk_bf16_f32 %0, %1, %2" : "=v"(r) : "v"(lo), "v"(hi)); return r; }
; #define LAS __attribute__((address_space(3)))
; #define LDS_WAIT() asm volatile("s_waitcnt lgkmcnt(0)" ::: "memory")
; __device__ __forceinline__ void conv_store(const ConvItem& ci, LAS float* scr, int lane, const float (&v)[64]) {
;     ...
;     LDS_WAIT(); asm volatile("" ::: "memory");
; #pragma unroll
;     for (int j = 0; j < 8; ++j) { const int n = (lane >> 3) + 8 * j; const LAS float* s = scr + (8 * c) * 65 + n;
;         v4u o; o.x = cvt_pk_bf16(s[0 * 65] * s0[0], s[1 * 65] * s0[1]); o.y = cvt_pk_bf16(s[2 * 65] * s0[2], s[3 * 65] * s0[3]); o.z = cvt_pk_bf16(s[4 * 65] * s1[0], s[5 * 65] * s1[1]); o.w = cvt_pk_bf16(s[6 * 65] * s1[2], s[7 * 65] * s1[3]);
;         *(v4u*)(ci.dst + (size_t)(ci.drow0 + n) * ci.ldd + ci.k0 + 8 * c) = o; }
	v_add_u32_e32 v192, 0x400, v14
	ds_read2_b32 v[128:129], v14 offset1:65
	ds_read2_b32 v[130:131], v14 offset0:130 offset1:195
	ds_read2_b32 v[132:133], v192 offset0:4 offset1:69
	ds_read2_b32 v[134:135], v192 offset0:134 offset1:199
	ds_read2_b32 v[136:137], v14 offset0:8 offset1:73
	ds_read2_b32 v[138:139], v14 offset0:138 offset1:203
	ds_read2_b32 v[140:141], v192 offset0:12 offset1:77
	ds_read2_b32 v[142:143], v192 offset0:142 offset1:207
	ds_read2_b32 v[144:145], v14 offset0:16 offset1:81
	ds_read2_b32 v[146:147], v14 offset0:146 offset1:211
	ds_read2_b32 v[148:149], v192 offset0:20 offset1:85
	ds_read2_b32 v[150:151], v192 offset0:150 offset1:215
	ds_read2_b32 v[152:153], v14 offset0:24 offset1:89
	ds_read2_b32 v[154:155], v14 offset0:154 offset1:219
	ds_read2_b32 v[156:157], v192 offset0:28 offset1:93
	ds_read2_b32 v[158:159], v192 offset0:158 offset1:223
	ds_read2_b32 v[160:161], v14 offset0:32 offset1:97
	ds_read2_b32 v[162:163], v14 offset0:162 offset1:227
	ds_read2_b32 v[164:165], v192 offset0:36 offset1:101
	ds_read2_b32 v[166:167], v192 offset0:166 offset1:231
	ds_read2_b32 v[168:169], v14 offset0:40 offset1:105
	ds_read2_b32 v[170:171], v14 offset0:170 offset1:235
	ds_read2_b32 v[172:173], v192 offset0:44 offset1:109
	ds_read2_b32 v[174:175], v192 offset0:174 offset1:239
	ds_read2_b32 v[176:177], v14 offset0:48 offset1:113
	ds_read2_b32 v[178:179], v14 offset0:178 offset1:243
	ds_read2_b32 v[180:181], v192 offset0:52 offset1:117
	ds_read2_b32 v[182:183], v192 offset0:182 offset1:247
	ds_read2_b32 v[184:185], v14 offset0:56 offset1:121
	ds_read2_b32 v[186:187], v14 offset0:186 offset1:251
	ds_read2_b32 v[188:189], v192 offset0:60 offset1:125
	ds_read2_b32 v[190:191], v192 offset0:190 offset1:255
	s_waitcnt lgkmcnt(0)
	v_add_u32_e32 v24, s59, v13
	v_mul_lo_u32 v22, s57, v24
	s_ashr_i32 s59, s58, 31
	v_readlane_b32 s76, v254, 31
	s_waitcnt lgkmcnt(0)
	v_mul_f32_e32 v8, v4, v128
	v_mul_f32_e32 v15, v5, v129
	v_cvt_pk_bf16_f32 v16, v8, v15
	s_add_i32 s3, s3, s33
	s_add_i32 s66, s66, s67
	s_add_i32 s68, s68, s69
	s_add_i32 s70, s70, s71
	s_waitcnt lgkmcnt(0)
	v_mul_f32_e32 v15, v7, v131
	v_mul_f32_e32 v8, v6, v130
	v_cvt_pk_bf16_f32 v17, v8, v15
	v_add_u32_e32 v15, 0x400, v14
	s_add_i32 s72, s72, s73
	s_add_i32 s74, s74, s75
	v_readlane_b32 s78, v254, 33
	v_readlane_b32 s79, v254, 34
	s_waitcnt lgkmcnt(0)
	v_mul_f32_e32 v8, v0, v132
	v_mul_f32_e32 v18, v1, v133
	v_cvt_pk_bf16_f32 v18, v8, v18
	v_readlane_b32 s80, v255, 21
	v_readlane_b32 s77, v254, 32
	s_movk_i32 s78, 0x1580
	v_readlane_b32 s82, v255, 23
	s_waitcnt lgkmcnt(0)
	v_mul_f32_e32 v8, v2, v134
	v_mul_f32_e32 v19, v3, v135
	v_cvt_pk_bf16_f32 v19, v8, v19
	v_ashrrev_i32_e32 v8, 31, v24
	v_mul_lo_u32 v8, s56, v8
	v_mad_u64_u32 v[20:21], s[4:5], s56, v24, 0
	v_add3_u32 v21, v21, v8, v22
	v_lshl_add_u64 v[20:21], v[20:21], 1, s[60:61]
	s_lshl_b64 s[4:5], s[58:59], 1
	v_lshl_add_u64 v[20:21], v[20:21], 0, s[4:5]
	v_lshlrev_b32_e32 v8, 1, v10
	v_lshl_add_u64 v[20:21], v[20:21], 0, v[8:9]
	global_store_dwordx4 v[20:21], v[16:19], off nt
	s_cmpk_lt_i32 s3, 21440
	v_readlane_b32 s83, v255, 24
	s_waitcnt lgkmcnt(0)
	v_mul_f32_e32 v16, v4, v136
	v_mul_f32_e32 v17, v5, v137
	v_cvt_pk_bf16_f32 v16, v16, v17
	s_mov_b32 s79, 0x3f22f983
	s_mov_b32 s85, 0xbfc90fda
	s_brev_b32 s86, 1
	s_movk_i32 s87, 0x1f8
	s_waitcnt lgkmcnt(0)
	v_mul_f32_e32 v17, v6, v138
	v_mul_f32_e32 v18, v7, v139
	v_cvt_pk_bf16_f32 v17, v17, v18
	s_mov_b64 s[88:89], 0x80
	s_mov_b64 s[92:93], 0x4000
	s_mov_b64 s[94:95], 0x4800
	v_readlane_b32 s81, v255, 22
	s_waitcnt lgkmcnt(0)
	v_mul_f32_e32 v18, v0, v140
	v_mul_f32_e32 v19, v1, v141
	v_cvt_pk_bf16_f32 v18, v18, v19
	s_waitcnt lgkmcnt(0)
	v_mul_f32_e32 v19, v2, v142
	v_mul_f32_e32 v20, v3, v143
	v_cvt_pk_bf16_f32 v19, v19, v20
	v_add_u32_e32 v20, 8, v24
	v_ashrrev_i32_e32 v21, 31, v20
	v_mul_lo_u32 v22, s56, v21
	v_mul_lo_u32 v23, s57, v20
	v_mad_u64_u32 v[20:21], s[6:7], s56, v20, 0
	v_add3_u32 v21, v21, v22, v23
	v_lshl_add_u64 v[20:21], v[20:21], 1, s[60:61]
	v_lshl_add_u64 v[20:21], v[20:21], 0, s[4:5]
	v_lshl_add_u64 v[20:21], v[20:21], 0, v[8:9]
	global_store_dwordx4 v[20:21], v[16:19], off nt
	s_waitcnt lgkmcnt(0)
	s_nop 0
	v_mul_f32_e32 v16, v4, v144
	v_mul_f32_e32 v17, v5, v145
	v_cvt_pk_bf16_f32 v16, v16, v17
	s_waitcnt lgkmcnt(0)
	v_mul_f32_e32 v17, v6, v146
	v_mul_f32_e32 v18, v7, v147
	v_cvt_pk_bf16_f32 v17, v17, v18
	s_waitcnt lgkmcnt(0)
	v_mul_f32_e32 v18, v0, v148
	v_mul_f32_e32 v19, v1, v149
	v_cvt_pk_bf16_f32 v18, v18, v19
	s_waitcnt lgkmcnt(0)
; __device__ __forceinline__ unsigned cvt_pk_bf16(float lo, float hi) { unsigned r; asm volatile("v_cvt_pk_bf16_f32 %0, %1, %2" : "=v"(r) : "v"(lo), "v"(hi)); return r; }
; #define LAS __attribute__((address_space(3)))
; #define LDS_WAIT() asm volatile("s_waitcnt lgkmcnt(0)" ::: "memory")
; __device__ __forceinline__ void conv_store(const ConvItem& ci, LAS float* scr, int lane, const float (&v)[64]) {
;     ...
;     for (int j = 0; j < 8; ++j) { const int n = (lane >> 3) + 8 * j; const LAS float* s = scr + (8 * c) * 65 + n;
;         v4u o; o.x = cvt_pk_bf16(s[0 * 65] * s0[0], s[1 * 65] * s0[1]); o.y = cvt_pk_bf16(s[2 * 65] * s0[2], s[3 * 65] * s0[3]); o.z = cvt_pk_bf16(s[4 * 65] * s1[0], s[5 * 65] * s1[1]); o.w = cvt_pk_bf16(s[6 * 65] * s1[2], s[7 * 65] * s1[3]);
;         *(v4u*)(ci.dst + (size_t)(ci.drow0 + n) * ci.ldd + ci.k0 + 8 * c) = o; }
;     LDS_WAIT(); asm volatile("" ::: "memory");
; }
	v_mul_f32_e32 v19, v2, v150
	v_mul_f32_e32 v20, v3, v151
	v_cvt_pk_bf16_f32 v19, v19, v20
	v_add_u32_e32 v20, 16, v24
	v_ashrrev_i32_e32 v21, 31, v20
	v_mul_lo_u32 v22, s56, v21
	v_mul_lo_u32 v23, s57, v20
	v_mad_u64_u32 v[20:21], s[6:7], s56, v20, 0
	v_add3_u32 v21, v21, v22, v23
	v_lshl_add_u64 v[20:21], v[20:21], 1, s[60:61]
	v_lshl_add_u64 v[20:21], v[20:21], 0, s[4:5]
	v_lshl_add_u64 v[20:21], v[20:21], 0, v[8:9]
	global_store_dwordx4 v[20:21], v[16:19], off nt
	s_waitcnt lgkmcnt(0)
	s_nop 0
	v_mul_f32_e32 v16, v4, v152
	v_mul_f32_e32 v17, v5, v153
	v_cvt_pk_bf16_f32 v16, v16, v17
	s_waitcnt lgkmcnt(0)
	v_mul_f32_e32 v17, v6, v154
	v_mul_f32_e32 v18, v7, v155
	v_cvt_pk_bf16_f32 v17, v17, v18
	s_waitcnt lgkmcnt(0)
	v_mul_f32_e32 v18, v0, v156
	v_mul_f32_e32 v19, v1, v157
	v_cvt_pk_bf16_f32 v18, v18, v19
	s_waitcnt lgkmcnt(0)
	v_mul_f32_e32 v19, v2, v158
	v_mul_f32_e32 v20, v3, v159
	v_cvt_pk_bf16_f32 v19, v19, v20
	v_add_u32_e32 v20, 24, v24
	v_ashrrev_i32_e32 v21, 31, v20
	v_mul_lo_u32 v22, s56, v21
	v_mul_lo_u32 v23, s57, v20
	v_mad_u64_u32 v[20:21], s[6:7], s56, v20, 0
	v_add3_u32 v21, v21, v22, v23
	v_lshl_add_u64 v[20:21], v[20:21], 1, s[60:61]
	v_lshl_add_u64 v[20:21], v[20:21], 0, s[4:5]
	v_lshl_add_u64 v[20:21], v[20:21], 0, v[8:9]
	global_store_dwordx4 v[20:21], v[16:19], off nt
	s_waitcnt lgkmcnt(0)
	s_nop 0
	v_mul_f32_e32 v16, v4, v160
	v_mul_f32_e32 v17, v5, v161
	v_cvt_pk_bf16_f32 v16, v16, v17
	s_waitcnt lgkmcnt(0)
	v_mul_f32_e32 v17, v6, v162
	v_mul_f32_e32 v18, v7, v163
	v_cvt_pk_bf16_f32 v17, v17, v18
	s_waitcnt lgkmcnt(0)
	v_mul_f32_e32 v18, v0, v164
	v_mul_f32_e32 v19, v1, v165
	v_cvt_pk_bf16_f32 v18, v18, v19
	s_waitcnt lgkmcnt(0)
	v_mul_f32_e32 v19, v2, v166
	v_mul_f32_e32 v20, v3, v167
	v_cvt_pk_bf16_f32 v19, v19, v20
	v_add_u32_e32 v20, 32, v24
	v_ashrrev_i32_e32 v21, 31, v20
	v_mul_lo_u32 v22, s56, v21
	v_mul_lo_u32 v23, s57, v20
	v_mad_u64_u32 v[20:21], s[6:7], s56, v20, 0
	v_add3_u32 v21, v21, v22, v23
	v_lshl_add_u64 v[20:21], v[20:21], 1, s[60:61]
	v_lshl_add_u64 v[20:21], v[20:21], 0, s[4:5]
	v_lshl_add_u64 v[20:21], v[20:21], 0, v[8:9]
	global_store_dwordx4 v[20:21], v[16:19], off nt
	s_waitcnt lgkmcnt(0)
	s_nop 0
	v_mul_f32_e32 v16, v4, v168
	v_mul_f32_e32 v17, v5, v169
	v_cvt_pk_bf16_f32 v16, v16, v17
	s_waitcnt lgkmcnt(0)
	v_mul_f32_e32 v17, v6, v170
	v_mul_f32_e32 v18, v7, v171
	v_cvt_pk_bf16_f32 v17, v17, v18
	s_waitcnt lgkmcnt(0)
	v_mul_f32_e32 v18, v0, v172
	v_mul_f32_e32 v19, v1, v173
	v_cvt_pk_bf16_f32 v18, v18, v19
	s_waitcnt lgkmcnt(0)
	v_mul_f32_e32 v19, v2, v174
	v_mul_f32_e32 v20, v3, v175
	v_cvt_pk_bf16_f32 v19, v19, v20
	v_add_u32_e32 v20, 40, v24
	v_ashrrev_i32_e32 v21, 31, v20
	v_mul_lo_u32 v22, s56, v21
	v_mul_lo_u32 v23, s57, v20
	v_mad_u64_u32 v[20:21], s[6:7], s56, v20, 0
	v_add3_u32 v21, v21, v22, v23
	v_lshl_add_u64 v[20:21], v[20:21], 1, s[60:61]
	v_lshl_add_u64 v[20:21], v[20:21], 0, s[4:5]
	v_lshl_add_u64 v[20:21], v[20:21], 0, v[8:9]
	global_store_dwordx4 v[20:21], v[16:19], off nt
	s_waitcnt lgkmcnt(0)
	s_nop 0
	v_mul_f32_e32 v16, v4, v176
	v_mul_f32_e32 v17, v5, v177
	v_cvt_pk_bf16_f32 v16, v16, v17
	s_waitcnt lgkmcnt(0)
	v_mul_f32_e32 v17, v6, v178
	v_mul_f32_e32 v18, v7, v179
	v_cvt_pk_bf16_f32 v17, v17, v18
	s_waitcnt lgkmcnt(0)
	v_mul_f32_e32 v18, v0, v180
	v_mul_f32_e32 v19, v1, v181
	v_cvt_pk_bf16_f32 v18, v18, v19
	s_waitcnt lgkmcnt(0)
	v_mul_f32_e32 v19, v2, v182
	v_mul_f32_e32 v20, v3, v183
	v_cvt_pk_bf16_f32 v19, v19, v20
	v_add_u32_e32 v20, 48, v24
	v_ashrrev_i32_e32 v21, 31, v20
	v_mul_lo_u32 v22, s56, v21
	v_mul_lo_u32 v23, s57, v20
	v_mad_u64_u32 v[20:21], s[6:7], s56, v20, 0
	v_add3_u32 v21, v21, v22, v23
	v_lshl_add_u64 v[20:21], v[20:21], 1, s[60:61]
	v_lshl_add_u64 v[20:21], v[20:21], 0, s[4:5]
	v_lshl_add_u64 v[20:21], v[20:21], 0, v[8:9]
	global_store_dwordx4 v[20:21], v[16:19], off nt
	s_waitcnt lgkmcnt(0)
	v_mul_f32_e32 v4, v4, v184
	v_mul_f32_e32 v5, v5, v185
	v_cvt_pk_bf16_f32 v4, v4, v5
	s_waitcnt lgkmcnt(0)
	v_mul_f32_e32 v5, v6, v186
	v_mul_f32_e32 v6, v7, v187
	v_cvt_pk_bf16_f32 v5, v5, v6
	s_waitcnt lgkmcnt(0)
	v_mul_f32_e32 v0, v0, v188
	v_mul_f32_e32 v1, v1, v189
	v_cvt_pk_bf16_f32 v6, v0, v1
	s_waitcnt lgkmcnt(0)
	v_mul_f32_e32 v0, v2, v190
	v_mul_f32_e32 v1, v3, v191
	v_cvt_pk_bf16_f32 v7, v0, v1
	v_add_u32_e32 v0, 56, v24
	v_ashrrev_i32_e32 v1, 31, v0
	v_mul_lo_u32 v2, s56, v1
	v_mul_lo_u32 v3, s57, v0
	v_mad_u64_u32 v[0:1], s[6:7], s56, v0, 0
	v_add3_u32 v1, v1, v2, v3
	v_lshl_add_u64 v[0:1], v[0:1], 1, s[60:61]
	v_lshl_add_u64 v[0:1], v[0:1], 0, s[4:5]
	v_lshl_add_u64 v[0:1], v[0:1], 0, v[8:9]
	global_store_dwordx4 v[0:1], v[4:7], off nt
	s_waitcnt lgkmcnt(0)
	s_cbranch_scc0 .Lcvp30_ret

; __device__ __forceinline__ void conv_load(const ConvItem& ci, int lane, float (&v)[64]) {
;     const bool okc = ci.srcc >= 0 && (ci.srcc + lane) < ci.ncols;
;     const float* base = ci.W + (okc ? ci.srcc + lane : 0);
;     const int kmax = ci.Ksrc - 1;
; #pragma unroll
;     for (int i = 0; i < 64; ++i) { const int k = ci.k0 + i, kk = k < kmax ? k : kmax; v[i] = __builtin_nontemporal_load(base + (size_t)kk * ci.ldw); }
; #pragma unroll
;     for (int i = 0; i < 64; ++i) v[i] = (okc && (ci.k0 + i) < ci.Ksrc) ? v[i] : 0.f;
; }
.Lcvp31_30:
	s_cmp_lt_i32 s58, s76
	s_cselect_b64 s[4:5], -1, 0
	s_and_b64 s[4:5], vcc, s[4:5]
	s_cmp_lt_i32 s64, s76
	s_waitcnt vmcnt(62)
	v_cndmask_b32_e64 v21, 0, v21, s[4:5]
	s_cselect_b64 s[4:5], -1, 0
	s_and_b64 s[4:5], vcc, s[4:5]
	s_cmp_lt_i32 s65, s76
	v_cndmask_b32_e64 v20, 0, v20, s[4:5]
	s_cselect_b64 s[4:5], -1, 0
	s_and_b64 s[4:5], vcc, s[4:5]
	s_cmp_lt_i32 s78, s76
	s_waitcnt vmcnt(61)
	v_cndmask_b32_e64 v19, 0, v19, s[4:5]
	s_cselect_b64 s[4:5], -1, 0
	s_and_b64 s[4:5], vcc, s[4:5]
	s_cmp_lt_i32 s79, s76
	s_waitcnt vmcnt(60)
	v_cndmask_b32_e64 v18, 0, v18, s[4:5]
	s_cselect_b64 s[4:5], -1, 0
	s_and_b64 s[4:5], vcc, s[4:5]
	s_cmp_lt_i32 s80, s76
	s_waitcnt vmcnt(59)
	v_cndmask_b32_e64 v17, 0, v17, s[4:5]
	s_cselect_b64 s[4:5], -1, 0
	s_and_b64 s[4:5], vcc, s[4:5]
	s_cmp_lt_i32 s81, s76
	s_waitcnt vmcnt(58)
	v_cndmask_b32_e64 v16, 0, v16, s[4:5]
	s_cselect_b64 s[4:5], -1, 0
	s_and_b64 s[4:5], vcc, s[4:5]
	s_cmp_lt_i32 s82, s76
	s_waitcnt vmcnt(57)
	v_cndmask_b32_e64 v15, 0, v15, s[4:5]
	s_cselect_b64 s[4:5], -1, 0
	s_and_b64 s[4:5], vcc, s[4:5]
	s_cmp_lt_i32 s83, s76
	s_waitcnt vmcnt(56)
	v_cndmask_b32_e64 v8, 0, v8, s[4:5]
	s_cselect_b64 s[4:5], -1, 0
	s_and_b64 s[4:5], vcc, s[4:5]
	s_cmp_lt_i32 s85, s76
	s_waitcnt vmcnt(55)
	v_cndmask_b32_e64 v29, 0, v29, s[4:5]
	s_cselect_b64 s[4:5], -1, 0
	s_and_b64 s[4:5], vcc, s[4:5]
	s_cmp_lt_i32 s86, s76
	s_waitcnt vmcnt(54)
	v_cndmask_b32_e64 v28, 0, v28, s[4:5]
	s_cselect_b64 s[4:5], -1, 0
	s_and_b64 s[4:5], vcc, s[4:5]
	s_cmp_lt_i32 s87, s76
	s_waitcnt vmcnt(53)
	v_cndmask_b32_e64 v27, 0, v27, s[4:5]
	s_cselect_b64 s[4:5], -1, 0
	s_and_b64 s[4:5], vcc, s[4:5]
	s_cmp_lt_i32 s88, s76
	s_waitcnt vmcnt(52)
	v_cndmask_b32_e64 v26, 0, v26, s[4:5]
	s_cselect_b64 s[4:5], -1, 0
	s_and_b64 s[4:5], vcc, s[4:5]
	s_cmp_lt_i32 s89, s76
	s_waitcnt vmcnt(51)
	v_cndmask_b32_e64 v25, 0, v25, s[4:5]
	s_cselect_b64 s[4:5], -1, 0
	s_and_b64 s[4:5], vcc, s[4:5]
	s_cmp_lt_i32 s90, s76
	s_waitcnt vmcnt(50)
	v_cndmask_b32_e64 v24, 0, v24, s[4:5]
	s_cselect_b64 s[4:5], -1, 0
	s_and_b64 s[4:5], vcc, s[4:5]
	s_cmp_lt_i32 s92, s76
	s_waitcnt vmcnt(49)
	v_cndmask_b32_e64 v23, 0, v23, s[4:5]
	s_cselect_b64 s[4:5], -1, 0
	s_and_b64 s[4:5], vcc, s[4:5]
	s_cmp_lt_i32 s93, s76
	s_waitcnt vmcnt(48)
	v_cndmask_b32_e64 v22, 0, v22, s[4:5]
	s_cselect_b64 s[4:5], -1, 0
	s_and_b64 s[4:5], vcc, s[4:5]
	s_cmp_lt_i32 s94, s76
	s_waitcnt vmcnt(47)
	v_cndmask_b32_e64 v37, 0, v37, s[4:5]
	s_cselect_b64 s[4:5], -1, 0
	s_and_b64 s[4:5], vcc, s[4:5]
	s_cmp_lt_i32 s95, s76
	s_waitcnt vmcnt(46)
	v_cndmask_b32_e64 v36, 0, v36, s[4:5]
	s_cselect_b64 s[4:5], -1, 0
	s_and_b64 s[4:5], vcc, s[4:5]
	s_cmp_lt_i32 s50, s76
	s_waitcnt vmcnt(45)
	v_cndmask_b32_e64 v35, 0, v35, s[4:5]
	s_cselect_b64 s[4:5], -1, 0
	s_and_b64 s[4:5], vcc, s[4:5]
	s_cmp_lt_i32 s51, s76
	s_waitcnt vmcnt(44)
	v_cndmask_b32_e64 v34, 0, v34, s[4:5]
	s_cselect_b64 s[4:5], -1, 0
	s_and_b64 s[4:5], vcc, s[4:5]
	s_cmp_lt_i32 s52, s76
	s_waitcnt vmcnt(43)
	v_cndmask_b32_e64 v33, 0, v33, s[4:5]
	s_cselect_b64 s[4:5], -1, 0
	s_and_b64 s[4:5], vcc, s[4:5]
	s_cmp_lt_i32 s53, s76
	s_waitcnt vmcnt(42)
	v_cndmask_b32_e64 v32, 0, v32, s[4:5]
	s_cselect_b64 s[4:5], -1, 0
	s_and_b64 s[4:5], vcc, s[4:5]
	s_cmp_lt_i32 s6, s76
	s_waitcnt vmcnt(41)
	v_cndmask_b32_e64 v31, 0, v31, s[4:5]
	s_cselect_b64 s[4:5], -1, 0
	s_and_b64 s[4:5], vcc, s[4:5]
	s_cmp_lt_i32 s7, s76
	s_waitcnt vmcnt(40)
	v_cndmask_b32_e64 v30, 0, v30, s[4:5]
	s_cselect_b64 s[4:5], -1, 0
	s_and_b64 s[4:5], vcc, s[4:5]
	s_cmp_lt_i32 s8, s76
	s_waitcnt vmcnt(39)
	v_cndmask_b32_e64 v45, 0, v45, s[4:5]
	s_cselect_b64 s[4:5], -1, 0
	s_and_b64 s[4:5], vcc, s[4:5]
	s_cmp_lt_i32 s9, s76
	s_waitcnt vmcnt(38)
	v_cndmask_b32_e64 v44, 0, v44, s[4:5]
	s_cselect_b64 s[4:5], -1, 0
	s_and_b64 s[4:5], vcc, s[4:5]
	s_cmp_lt_i32 s10, s76
	s_waitcnt vmcnt(37)
	v_cndmask_b32_e64 v43, 0, v43, s[4:5]
	s_cselect_b64 s[4:5], -1, 0
	s_and_b64 s[4:5], vcc, s[4:5]
	s_cmp_lt_i32 s11, s76
	s_waitcnt vmcnt(36)
	v_cndmask_b32_e64 v42, 0, v42, s[4:5]
	s_cselect_b64 s[4:5], -1, 0
	s_and_b64 s[4:5], vcc, s[4:5]
	s_cmp_lt_i32 s14, s76
	s_waitcnt vmcnt(35)
	v_cndmask_b32_e64 v41, 0, v41, s[4:5]
	s_cselect_b64 s[4:5], -1, 0
	s_and_b64 s[4:5], vcc, s[4:5]
	s_cmp_lt_i32 s15, s76
	s_waitcnt vmcnt(34)
	v_cndmask_b32_e64 v40, 0, v40, s[4:5]
	s_cselect_b64 s[4:5], -1, 0
	s_and_b64 s[4:5], vcc, s[4:5]
	s_cmp_lt_i32 s16, s76
	s_waitcnt vmcnt(33)
	v_cndmask_b32_e64 v39, 0, v39, s[4:5]
	s_cselect_b64 s[4:5], -1, 0
	s_and_b64 s[4:5], vcc, s[4:5]
	s_cmp_lt_i32 s17, s76
	s_waitcnt vmcnt(32)
	v_cndmask_b32_e64 v38, 0, v38, s[4:5]
	s_cselect_b64 s[4:5], -1, 0
	s_and_b64 s[4:5], vcc, s[4:5]
	s_cmp_lt_i32 s12, s76
	s_waitcnt vmcnt(31)
	v_cndmask_b32_e64 v53, 0, v53, s[4:5]
	s_cselect_b64 s[4:5], -1, 0
	s_and_b64 s[4:5], vcc, s[4:5]
	s_cmp_lt_i32 s13, s76
	s_waitcnt vmcnt(30)
	v_cndmask_b32_e64 v52, 0, v52, s[4:5]
	s_cselect_b64 s[4:5], -1, 0
	s_and_b64 s[4:5], vcc, s[4:5]
	s_cmp_lt_i32 s20, s76
	s_waitcnt vmcnt(29)
	v_cndmask_b32_e64 v51, 0, v51, s[4:5]
	s_cselect_b64 s[4:5], -1, 0
	s_and_b64 s[4:5], vcc, s[4:5]
	s_cmp_lt_i32 s21, s76
	s_waitcnt vmcnt(28)
	v_cndmask_b32_e64 v50, 0, v50, s[4:5]
	s_cselect_b64 s[4:5], -1, 0
	s_and_b64 s[4:5], vcc, s[4:5]
	s_cmp_lt_i32 s24, s76
	s_waitcnt vmcnt(27)
	v_cndmask_b32_e64 v49, 0, v49, s[4:5]
	s_cselect_b64 s[4:5], -1, 0
	s_and_b64 s[4:5], vcc, s[4:5]
	s_cmp_lt_i32 s25, s76
	s_waitcnt vmcnt(26)
	v_cndmask_b32_e64 v48, 0, v48, s[4:5]
	s_cselect_b64 s[4:5], -1, 0
	s_and_b64 s[4:5], vcc, s[4:5]
	s_cmp_lt_i32 s26, s76
	s_waitcnt vmcnt(25)
	v_cndmask_b32_e64 v47, 0, v47, s[4:5]
	s_cselect_b64 s[4:5], -1, 0
	s_and_b64 s[4:5], vcc, s[4:5]
	s_cmp_lt_i32 s27, s76
	s_waitcnt vmcnt(24)
; #define LAS __attribute__((address_space(3)))
; #define LDS_WAIT() asm volatile("s_waitcnt lgkmcnt(0)" ::: "memory")
; __device__ __forceinline__ void conv_load(const ConvItem& ci, int lane, float (&v)[64]) {
;     ...
;     for (int i = 0; i < 64; ++i) { const int k = ci.k0 + i, kk = k < kmax ? k : kmax; v[i] = __builtin_nontemporal_load(base + (size_t)kk * ci.ldw); }
; #pragma unroll
;     for (int i = 0; i < 64; ++i) v[i] = (okc && (ci.k0 + i) < ci.Ksrc) ? v[i] : 0.f;
; }
; __device__ __forceinline__ void conv_store(const ConvItem& ci, LAS float* scr, int lane, const float (&v)[64]) {
;     const int c = lane & 7;
;     f32x4 s0 = {1.f, 1.f, 1.f, 1.f}, s1 = s0;
;     if (ci.ks) { const int kb = ci.k0 + 8 * c < ci.Ksrc - 8 ? ci.k0 + 8 * c : ci.Ksrc - 8; s0 = *(const f32x4*)(ci.ks + kb); s1 = *(const f32x4*)(ci.ks + kb + 4); }
; #pragma unroll
;     for (int i = 0; i < 64; ++i) scr[i * 65 + lane] = v[i];
;     LDS_WAIT(); asm volatile("" ::: "memory");
	v_cndmask_b32_e64 v46, 0, v46, s[4:5]
	s_cselect_b64 s[4:5], -1, 0
	s_and_b64 s[4:5], vcc, s[4:5]
	s_cmp_lt_i32 s18, s76
	s_waitcnt vmcnt(23)
	v_cndmask_b32_e64 v61, 0, v61, s[4:5]
	s_cselect_b64 s[4:5], -1, 0
	s_and_b64 s[4:5], vcc, s[4:5]
	s_cmp_lt_i32 s19, s76
	s_waitcnt vmcnt(22)
	v_cndmask_b32_e64 v60, 0, v60, s[4:5]
	s_cselect_b64 s[4:5], -1, 0
	s_and_b64 s[4:5], vcc, s[4:5]
	s_cmp_lt_i32 s28, s76
	s_waitcnt vmcnt(21)
	v_cndmask_b32_e64 v59, 0, v59, s[4:5]
	s_cselect_b64 s[4:5], -1, 0
	s_and_b64 s[4:5], vcc, s[4:5]
	s_cmp_lt_i32 s29, s76
	s_waitcnt vmcnt(20)
	v_cndmask_b32_e64 v58, 0, v58, s[4:5]
	s_cselect_b64 s[4:5], -1, 0
	s_and_b64 s[4:5], vcc, s[4:5]
	s_cmp_lt_i32 s22, s76
	s_waitcnt vmcnt(19)
	v_cndmask_b32_e64 v57, 0, v57, s[4:5]
	s_cselect_b64 s[4:5], -1, 0
	s_and_b64 s[4:5], vcc, s[4:5]
	s_cmp_lt_i32 s23, s76
	s_waitcnt vmcnt(18)
	v_cndmask_b32_e64 v56, 0, v56, s[4:5]
	s_cselect_b64 s[4:5], -1, 0
	s_and_b64 s[4:5], vcc, s[4:5]
	s_cmp_lt_i32 s30, s76
	s_waitcnt vmcnt(17)
	v_cndmask_b32_e64 v55, 0, v55, s[4:5]
	s_cselect_b64 s[4:5], -1, 0
	s_and_b64 s[4:5], vcc, s[4:5]
	s_cmp_lt_i32 s31, s76
	s_waitcnt vmcnt(16)
	v_cndmask_b32_e64 v54, 0, v54, s[4:5]
	s_cselect_b64 s[4:5], -1, 0
	s_and_b64 s[4:5], vcc, s[4:5]
	s_cmp_lt_i32 s36, s76
	s_waitcnt vmcnt(15)
	v_cndmask_b32_e64 v70, 0, v70, s[4:5]
	s_cselect_b64 s[4:5], -1, 0
	s_and_b64 s[4:5], vcc, s[4:5]
	s_cmp_lt_i32 s37, s76
	s_waitcnt vmcnt(14)
	v_cndmask_b32_e64 v69, 0, v69, s[4:5]
	s_cselect_b64 s[4:5], -1, 0
	s_and_b64 s[4:5], vcc, s[4:5]
	s_cmp_lt_i32 s38, s76
	s_waitcnt vmcnt(13)
	v_cndmask_b32_e64 v68, 0, v68, s[4:5]
	s_cselect_b64 s[4:5], -1, 0
	s_and_b64 s[4:5], vcc, s[4:5]
	s_cmp_lt_i32 s39, s76
	s_waitcnt vmcnt(12)
	v_cndmask_b32_e64 v67, 0, v67, s[4:5]
	s_cselect_b64 s[4:5], -1, 0
	s_and_b64 s[4:5], vcc, s[4:5]
	s_cmp_lt_i32 s34, s76
	s_waitcnt vmcnt(11)
	v_cndmask_b32_e64 v66, 0, v66, s[4:5]
	s_cselect_b64 s[4:5], -1, 0
	s_and_b64 s[4:5], vcc, s[4:5]
	s_cmp_lt_i32 s35, s76
	s_waitcnt vmcnt(10)
	v_cndmask_b32_e64 v64, 0, v64, s[4:5]
	s_cselect_b64 s[4:5], -1, 0
	s_and_b64 s[4:5], vcc, s[4:5]
	s_cmp_lt_i32 s42, s76
	s_waitcnt vmcnt(9)
	v_cndmask_b32_e64 v63, 0, v63, s[4:5]
	s_cselect_b64 s[4:5], -1, 0
	s_and_b64 s[4:5], vcc, s[4:5]
	s_cmp_lt_i32 s43, s76
	s_waitcnt vmcnt(8)
	v_cndmask_b32_e64 v62, 0, v62, s[4:5]
	s_cselect_b64 s[4:5], -1, 0
	s_and_b64 s[4:5], vcc, s[4:5]
	s_cmp_lt_i32 s54, s76
	s_waitcnt vmcnt(7)
	v_cndmask_b32_e64 v65, 0, v65, s[4:5]
	s_cselect_b64 s[4:5], -1, 0
	s_and_b64 s[4:5], vcc, s[4:5]
	s_cmp_lt_i32 s55, s76
	s_waitcnt vmcnt(6)
	v_cndmask_b32_e64 v74, 0, v74, s[4:5]
	s_cselect_b64 s[4:5], -1, 0
	s_and_b64 s[4:5], vcc, s[4:5]
	s_cmp_lt_i32 s46, s76
	ds_write2_b32 v12, v21, v20 offset1:65
	ds_write2_b32 v12, v19, v18 offset0:130 offset1:195
	v_add_u32_e32 v18, 0x400, v12
	s_waitcnt vmcnt(5)
	v_cndmask_b32_e64 v73, 0, v73, s[4:5]
	s_cselect_b64 s[4:5], -1, 0
	ds_write2_b32 v18, v17, v16 offset0:4 offset1:69
	ds_write2_b32 v18, v15, v8 offset0:134 offset1:199
	v_add_u32_e32 v8, 0x800, v12
	s_and_b64 s[4:5], vcc, s[4:5]
	ds_write2_b32 v8, v29, v28 offset0:8 offset1:73
	ds_write2_b32 v8, v27, v26 offset0:138 offset1:203
	v_add_u32_e32 v8, 0xc00, v12
	s_cmp_lt_i32 s47, s76
	ds_write2_b32 v8, v25, v24 offset0:12 offset1:77
	ds_write2_b32 v8, v23, v22 offset0:142 offset1:207
	v_add_u32_e32 v8, 0x1000, v12
	s_waitcnt vmcnt(4)
	v_cndmask_b32_e64 v72, 0, v72, s[4:5]
	s_cselect_b64 s[4:5], -1, 0
	ds_write2_b32 v8, v37, v36 offset0:16 offset1:81
	ds_write2_b32 v8, v35, v34 offset0:146 offset1:211
	v_add_u32_e32 v8, 0x1400, v12
	s_and_b64 s[4:5], vcc, s[4:5]
	ds_write2_b32 v8, v33, v32 offset0:20 offset1:85
	ds_write2_b32 v8, v31, v30 offset0:150 offset1:215
	v_add_u32_e32 v8, 0x1800, v12
	s_cmp_lt_i32 s48, s76
	ds_write2_b32 v8, v45, v44 offset0:24 offset1:89
	ds_write2_b32 v8, v43, v42 offset0:154 offset1:219
	v_add_u32_e32 v8, 0x1c00, v12
	s_waitcnt vmcnt(3)
	v_cndmask_b32_e64 v71, 0, v71, s[4:5]
	s_cselect_b64 s[4:5], -1, 0
	ds_write2_b32 v8, v41, v40 offset0:28 offset1:93
	ds_write2_b32 v8, v39, v38 offset0:158 offset1:223
	v_add_u32_e32 v8, 0x2000, v12
	s_and_b64 s[4:5], vcc, s[4:5]
	ds_write2_b32 v8, v53, v52 offset0:32 offset1:97
	ds_write2_b32 v8, v51, v50 offset0:162 offset1:227
	v_add_u32_e32 v8, 0x2400, v12
	s_cmp_lt_i32 s49, s76
	ds_write2_b32 v8, v49, v48 offset0:36 offset1:101
	ds_write2_b32 v8, v47, v46 offset0:166 offset1:231
	v_add_u32_e32 v8, 0x2800, v12
	s_waitcnt vmcnt(2)
	v_cndmask_b32_e64 v77, 0, v77, s[4:5]
	s_cselect_b64 s[4:5], -1, 0
	ds_write2_b32 v8, v61, v60 offset0:40 offset1:105
	ds_write2_b32 v8, v59, v58 offset0:170 offset1:235
	v_add_u32_e32 v8, 0x2c00, v12
	s_and_b64 s[4:5], vcc, s[4:5]
	ds_write2_b32 v8, v57, v56 offset0:44 offset1:109
	ds_write2_b32 v8, v55, v54 offset0:174 offset1:239
	v_add_u32_e32 v8, 0x3000, v12
	s_cmp_lt_i32 s44, s76
	ds_write2_b32 v8, v70, v69 offset0:48 offset1:113
	ds_write2_b32 v8, v68, v67 offset0:178 offset1:243
	v_add_u32_e32 v8, 0x3400, v12
	s_waitcnt vmcnt(1)
	v_cndmask_b32_e64 v76, 0, v76, s[4:5]
	s_cselect_b64 s[4:5], -1, 0
	ds_write2_b32 v8, v66, v64 offset0:52 offset1:117
	ds_write2_b32 v8, v63, v62 offset0:182 offset1:247
	v_add_u32_e32 v8, 0x3800, v12
	s_and_b64 vcc, vcc, s[4:5]
	ds_write2_b32 v8, v65, v74 offset0:56 offset1:121
	ds_write2_b32 v8, v73, v72 offset0:186 offset1:251
	v_add_u32_e32 v8, 0x3c00, v12
	s_waitcnt vmcnt(0)
	v_cndmask_b32_e32 v75, 0, v75, vcc
	ds_write2_b32 v8, v71, v77 offset0:60 offset1:125
	ds_write2_b32 v8, v76, v75 offset0:190 offset1:255
	s_waitcnt lgkmcnt(0)
; __device__ __forceinline__ unsigned cvt_pk_bf16(float lo, float hi) { unsigned r; asm volatile("v_cvt_pk_bf16_f32 %0, %1, %2" : "=v"(r) : "v"(lo), "v"(hi)); return r; }
; #define LAS __attribute__((address_space(3)))
; #define LDS_WAIT() asm volatile("s_waitcnt lgkmcnt(0)" ::: "memory")
; __device__ __forceinline__ void conv_store(const ConvItem& ci, LAS float* scr, int lane, const float (&v)[64]) {
;     ...
;     LDS_WAIT(); asm volatile("" ::: "memory");
; #pragma unroll
;     for (int j = 0; j < 8; ++j) { const int n = (lane >> 3) + 8 * j; const LAS float* s = scr + (8 * c) * 65 + n;
;         v4u o; o.x = cvt_pk_bf16(s[0 * 65] * s0[0], s[1 * 65] * s0[1]); o.y = cvt_pk_bf16(s[2 * 65] * s0[2], s[3 * 65] * s0[3]); o.z = cvt_pk_bf16(s[4 * 65] * s1[0], s[5 * 65] * s1[1]); o.w = cvt_pk_bf16(s[6 * 65] * s1[2], s[7 * 65] * s1[3]);
;         *(v4u*)(ci.dst + (size_t)(ci.drow0 + n) * ci.ldd + ci.k0 + 8 * c) = o; }
	v_add_u32_e32 v192, 0x400, v14
	ds_read2_b32 v[128:129], v14 offset1:65
	ds_read2_b32 v[130:131], v14 offset0:130 offset1:195
	ds_read2_b32 v[132:133], v192 offset0:4 offset1:69
	ds_read2_b32 v[134:135], v192 offset0:134 offset1:199
	ds_read2_b32 v[136:137], v14 offset0:8 offset1:73
	ds_read2_b32 v[138:139], v14 offset0:138 offset1:203
	ds_read2_b32 v[140:141], v192 offset0:12 offset1:77
	ds_read2_b32 v[142:143], v192 offset0:142 offset1:207
	ds_read2_b32 v[144:145], v14 offset0:16 offset1:81
	ds_read2_b32 v[146:147], v14 offset0:146 offset1:211
	ds_read2_b32 v[148:149], v192 offset0:20 offset1:85
	ds_read2_b32 v[150:151], v192 offset0:150 offset1:215
	ds_read2_b32 v[152:153], v14 offset0:24 offset1:89
	ds_read2_b32 v[154:155], v14 offset0:154 offset1:219
	ds_read2_b32 v[156:157], v192 offset0:28 offset1:93
	ds_read2_b32 v[158:159], v192 offset0:158 offset1:223
	ds_read2_b32 v[160:161], v14 offset0:32 offset1:97
	ds_read2_b32 v[162:163], v14 offset0:162 offset1:227
	ds_read2_b32 v[164:165], v192 offset0:36 offset1:101
	ds_read2_b32 v[166:167], v192 offset0:166 offset1:231
	ds_read2_b32 v[168:169], v14 offset0:40 offset1:105
	ds_read2_b32 v[170:171], v14 offset0:170 offset1:235
	ds_read2_b32 v[172:173], v192 offset0:44 offset1:109
	ds_read2_b32 v[174:175], v192 offset0:174 offset1:239
	ds_read2_b32 v[176:177], v14 offset0:48 offset1:113
	ds_read2_b32 v[178:179], v14 offset0:178 offset1:243
	ds_read2_b32 v[180:181], v192 offset0:52 offset1:117
	ds_read2_b32 v[182:183], v192 offset0:182 offset1:247
	ds_read2_b32 v[184:185], v14 offset0:56 offset1:121
	ds_read2_b32 v[186:187], v14 offset0:186 offset1:251
	ds_read2_b32 v[188:189], v192 offset0:60 offset1:125
	ds_read2_b32 v[190:191], v192 offset0:190 offset1:255
	s_waitcnt lgkmcnt(0)
	v_add_u32_e32 v24, s59, v13
	v_mul_lo_u32 v22, s57, v24
	s_ashr_i32 s59, s58, 31
	v_readlane_b32 s76, v254, 31
	s_waitcnt lgkmcnt(0)
	v_mul_f32_e32 v8, v4, v128
	v_mul_f32_e32 v15, v5, v129
	v_cvt_pk_bf16_f32 v16, v8, v15
	s_add_i32 s3, s3, s33
	s_add_i32 s66, s66, s67
	s_add_i32 s68, s68, s69
	s_add_i32 s70, s70, s71
	s_waitcnt lgkmcnt(0)
	v_mul_f32_e32 v15, v7, v131
	v_mul_f32_e32 v8, v6, v130
	v_cvt_pk_bf16_f32 v17, v8, v15
	v_add_u32_e32 v15, 0x400, v14
	s_add_i32 s72, s72, s73
	s_add_i32 s74, s74, s75
	v_readlane_b32 s78, v254, 33
	v_readlane_b32 s79, v254, 34
	s_waitcnt lgkmcnt(0)
	v_mul_f32_e32 v8, v0, v132
	v_mul_f32_e32 v18, v1, v133
	v_cvt_pk_bf16_f32 v18, v8, v18
	v_readlane_b32 s80, v255, 21
	v_readlane_b32 s77, v254, 32
	s_movk_i32 s78, 0x1580
	v_readlane_b32 s82, v255, 23
	s_waitcnt lgkmcnt(0)
	v_mul_f32_e32 v8, v2, v134
	v_mul_f32_e32 v19, v3, v135
	v_cvt_pk_bf16_f32 v19, v8, v19
	v_ashrrev_i32_e32 v8, 31, v24
	v_mul_lo_u32 v8, s56, v8
	v_mad_u64_u32 v[20:21], s[4:5], s56, v24, 0
	v_add3_u32 v21, v21, v8, v22
	v_lshl_add_u64 v[20:21], v[20:21], 1, s[60:61]
	s_lshl_b64 s[4:5], s[58:59], 1
	v_lshl_add_u64 v[20:21], v[20:21], 0, s[4:5]
	v_lshlrev_b32_e32 v8, 1, v10
	v_lshl_add_u64 v[20:21], v[20:21], 0, v[8:9]
	global_store_dwordx4 v[20:21], v[16:19], off nt
	s_cmpk_lt_i32 s3, 25216
	v_readlane_b32 s83, v255, 24
	s_waitcnt lgkmcnt(0)
	v_mul_f32_e32 v16, v4, v136
	v_mul_f32_e32 v17, v5, v137
	v_cvt_pk_bf16_f32 v16, v16, v17
	s_mov_b32 s79, 0x3f22f983
	s_mov_b32 s85, 0xbfc90fda
	s_brev_b32 s86, 1
	s_movk_i32 s87, 0x1f8
	s_waitcnt lgkmcnt(0)
	v_mul_f32_e32 v17, v6, v138
	v_mul_f32_e32 v18, v7, v139
	v_cvt_pk_bf16_f32 v17, v17, v18
	s_mov_b64 s[88:89], 0x80
	s_mov_b64 s[92:93], 0x4000
	s_mov_b64 s[94:95], 0x4800
	v_readlane_b32 s81, v255, 22
	s_waitcnt lgkmcnt(0)
	v_mul_f32_e32 v18, v0, v140
	v_mul_f32_e32 v19, v1, v141
	v_cvt_pk_bf16_f32 v18, v18, v19
	s_waitcnt lgkmcnt(0)
	v_mul_f32_e32 v19, v2, v142
	v_mul_f32_e32 v20, v3, v143
	v_cvt_pk_bf16_f32 v19, v19, v20
	v_add_u32_e32 v20, 8, v24
	v_ashrrev_i32_e32 v21, 31, v20
	v_mul_lo_u32 v22, s56, v21
	v_mul_lo_u32 v23, s57, v20
	v_mad_u64_u32 v[20:21], s[6:7], s56, v20, 0
	v_add3_u32 v21, v21, v22, v23
	v_lshl_add_u64 v[20:21], v[20:21], 1, s[60:61]
	v_lshl_add_u64 v[20:21], v[20:21], 0, s[4:5]
	v_lshl_add_u64 v[20:21], v[20:21], 0, v[8:9]
	global_store_dwordx4 v[20:21], v[16:19], off nt
	s_waitcnt lgkmcnt(0)
	s_nop 0
	v_mul_f32_e32 v16, v4, v144
	v_mul_f32_e32 v17, v5, v145
	v_cvt_pk_bf16_f32 v16, v16, v17
	s_waitcnt lgkmcnt(0)
	v_mul_f32_e32 v17, v6, v146
	v_mul_f32_e32 v18, v7, v147
	v_cvt_pk_bf16_f32 v17, v17, v18
	s_waitcnt lgkmcnt(0)
	v_mul_f32_e32 v18, v0, v148
	v_mul_f32_e32 v19, v1, v149
	v_cvt_pk_bf16_f32 v18, v18, v19
	s_waitcnt lgkmcnt(0)
; __device__ __forceinline__ unsigned cvt_pk_bf16(float lo, float hi) { unsigned r; asm volatile("v_cvt_pk_bf16_f32 %0, %1, %2" : "=v"(r) : "v"(lo), "v"(hi)); return r; }
; #define LAS __attribute__((address_space(3)))
; #define LDS_WAIT() asm volatile("s_waitcnt lgkmcnt(0)" ::: "memory")
; __device__ __forceinline__ void conv_store(const ConvItem& ci, LAS float* scr, int lane, const float (&v)[64]) {
;     ...
;     for (int j = 0; j < 8; ++j) { const int n = (lane >> 3) + 8 * j; const LAS float* s = scr + (8 * c) * 65 + n;
;         v4u o; o.x = cvt_pk_bf16(s[0 * 65] * s0[0], s[1 * 65] * s0[1]); o.y = cvt_pk_bf16(s[2 * 65] * s0[2], s[3 * 65] * s0[3]); o.z = cvt_pk_bf16(s[4 * 65] * s1[0], s[5 * 65] * s1[1]); o.w = cvt_pk_bf16(s[6 * 65] * s1[2], s[7 * 65] * s1[3]);
;         *(v4u*)(ci.dst + (size_t)(ci.drow0 + n) * ci.ldd + ci.k0 + 8 * c) = o; }
;     LDS_WAIT(); asm volatile("" ::: "memory");
; }
	v_mul_f32_e32 v19, v2, v150
	v_mul_f32_e32 v20, v3, v151
	v_cvt_pk_bf16_f32 v19, v19, v20
	v_add_u32_e32 v20, 16, v24
	v_ashrrev_i32_e32 v21, 31, v20
	v_mul_lo_u32 v22, s56, v21
	v_mul_lo_u32 v23, s57, v20
	v_mad_u64_u32 v[20:21], s[6:7], s56, v20, 0
	v_add3_u32 v21, v21, v22, v23
	v_lshl_add_u64 v[20:21], v[20:21], 1, s[60:61]
	v_lshl_add_u64 v[20:21], v[20:21], 0, s[4:5]
	v_lshl_add_u64 v[20:21], v[20:21], 0, v[8:9]
	global_store_dwordx4 v[20:21], v[16:19], off nt
	s_waitcnt lgkmcnt(0)
	s_nop 0
	v_mul_f32_e32 v16, v4, v152
	v_mul_f32_e32 v17, v5, v153
	v_cvt_pk_bf16_f32 v16, v16, v17
	s_waitcnt lgkmcnt(0)
	v_mul_f32_e32 v17, v6, v154
	v_mul_f32_e32 v18, v7, v155
	v_cvt_pk_bf16_f32 v17, v17, v18
	s_waitcnt lgkmcnt(0)
	v_mul_f32_e32 v18, v0, v156
	v_mul_f32_e32 v19, v1, v157
	v_cvt_pk_bf16_f32 v18, v18, v19
	s_waitcnt lgkmcnt(0)
	v_mul_f32_e32 v19, v2, v158
	v_mul_f32_e32 v20, v3, v159
	v_cvt_pk_bf16_f32 v19, v19, v20
	v_add_u32_e32 v20, 24, v24
	v_ashrrev_i32_e32 v21, 31, v20
	v_mul_lo_u32 v22, s56, v21
	v_mul_lo_u32 v23, s57, v20
	v_mad_u64_u32 v[20:21], s[6:7], s56, v20, 0
	v_add3_u32 v21, v21, v22, v23
	v_lshl_add_u64 v[20:21], v[20:21], 1, s[60:61]
	v_lshl_add_u64 v[20:21], v[20:21], 0, s[4:5]
	v_lshl_add_u64 v[20:21], v[20:21], 0, v[8:9]
	global_store_dwordx4 v[20:21], v[16:19], off nt
	s_waitcnt lgkmcnt(0)
	s_nop 0
	v_mul_f32_e32 v16, v4, v160
	v_mul_f32_e32 v17, v5, v161
	v_cvt_pk_bf16_f32 v16, v16, v17
	s_waitcnt lgkmcnt(0)
	v_mul_f32_e32 v17, v6, v162
	v_mul_f32_e32 v18, v7, v163
	v_cvt_pk_bf16_f32 v17, v17, v18
	s_waitcnt lgkmcnt(0)
	v_mul_f32_e32 v18, v0, v164
	v_mul_f32_e32 v19, v1, v165
	v_cvt_pk_bf16_f32 v18, v18, v19
	s_waitcnt lgkmcnt(0)
	v_mul_f32_e32 v19, v2, v166
	v_mul_f32_e32 v20, v3, v167
	v_cvt_pk_bf16_f32 v19, v19, v20
	v_add_u32_e32 v20, 32, v24
	v_ashrrev_i32_e32 v21, 31, v20
	v_mul_lo_u32 v22, s56, v21
	v_mul_lo_u32 v23, s57, v20
	v_mad_u64_u32 v[20:21], s[6:7], s56, v20, 0
	v_add3_u32 v21, v21, v22, v23
	v_lshl_add_u64 v[20:21], v[20:21], 1, s[60:61]
	v_lshl_add_u64 v[20:21], v[20:21], 0, s[4:5]
	v_lshl_add_u64 v[20:21], v[20:21], 0, v[8:9]
	global_store_dwordx4 v[20:21], v[16:19], off nt
	s_waitcnt lgkmcnt(0)
	s_nop 0
	v_mul_f32_e32 v16, v4, v168
	v_mul_f32_e32 v17, v5, v169
	v_cvt_pk_bf16_f32 v16, v16, v17
	s_waitcnt lgkmcnt(0)
	v_mul_f32_e32 v17, v6, v170
	v_mul_f32_e32 v18, v7, v171
	v_cvt_pk_bf16_f32 v17, v17, v18
	s_waitcnt lgkmcnt(0)
	v_mul_f32_e32 v18, v0, v172
	v_mul_f32_e32 v19, v1, v173
	v_cvt_pk_bf16_f32 v18, v18, v19
	s_waitcnt lgkmcnt(0)
	v_mul_f32_e32 v19, v2, v174
	v_mul_f32_e32 v20, v3, v175
	v_cvt_pk_bf16_f32 v19, v19, v20
	v_add_u32_e32 v20, 40, v24
	v_ashrrev_i32_e32 v21, 31, v20
	v_mul_lo_u32 v22, s56, v21
	v_mul_lo_u32 v23, s57, v20
	v_mad_u64_u32 v[20:21], s[6:7], s56, v20, 0
	v_add3_u32 v21, v21, v22, v23
	v_lshl_add_u64 v[20:21], v[20:21], 1, s[60:61]
	v_lshl_add_u64 v[20:21], v[20:21], 0, s[4:5]
	v_lshl_add_u64 v[20:21], v[20:21], 0, v[8:9]
	global_store_dwordx4 v[20:21], v[16:19], off nt
	s_waitcnt lgkmcnt(0)
	s_nop 0
	v_mul_f32_e32 v16, v4, v176
	v_mul_f32_e32 v17, v5, v177
	v_cvt_pk_bf16_f32 v16, v16, v17
	s_waitcnt lgkmcnt(0)
	v_mul_f32_e32 v17, v6, v178
	v_mul_f32_e32 v18, v7, v179
	v_cvt_pk_bf16_f32 v17, v17, v18
	s_waitcnt lgkmcnt(0)
	v_mul_f32_e32 v18, v0, v180
	v_mul_f32_e32 v19, v1, v181
	v_cvt_pk_bf16_f32 v18, v18, v19
	s_waitcnt lgkmcnt(0)
	v_mul_f32_e32 v19, v2, v182
	v_mul_f32_e32 v20, v3, v183
	v_cvt_pk_bf16_f32 v19, v19, v20
	v_add_u32_e32 v20, 48, v24
	v_ashrrev_i32_e32 v21, 31, v20
	v_mul_lo_u32 v22, s56, v21
	v_mul_lo_u32 v23, s57, v20
	v_mad_u64_u32 v[20:21], s[6:7], s56, v20, 0
	v_add3_u32 v21, v21, v22, v23
	v_lshl_add_u64 v[20:21], v[20:21], 1, s[60:61]
	v_lshl_add_u64 v[20:21], v[20:21], 0, s[4:5]
	v_lshl_add_u64 v[20:21], v[20:21], 0, v[8:9]
	global_store_dwordx4 v[20:21], v[16:19], off nt
	s_waitcnt lgkmcnt(0)
	v_mul_f32_e32 v4, v4, v184
	v_mul_f32_e32 v5, v5, v185
	v_cvt_pk_bf16_f32 v4, v4, v5
	s_waitcnt lgkmcnt(0)
	v_mul_f32_e32 v5, v6, v186
	v_mul_f32_e32 v6, v7, v187
	v_cvt_pk_bf16_f32 v5, v5, v6
	s_waitcnt lgkmcnt(0)
	v_mul_f32_e32 v0, v0, v188
	v_mul_f32_e32 v1, v1, v189
	v_cvt_pk_bf16_f32 v6, v0, v1
	s_waitcnt lgkmcnt(0)
	v_mul_f32_e32 v0, v2, v190
	v_mul_f32_e32 v1, v3, v191
	v_cvt_pk_bf16_f32 v7, v0, v1
	v_add_u32_e32 v0, 56, v24
	v_ashrrev_i32_e32 v1, 31, v0
	v_mul_lo_u32 v2, s56, v1
	v_mul_lo_u32 v3, s57, v0
	v_mad_u64_u32 v[0:1], s[6:7], s56, v0, 0
	v_add3_u32 v1, v1, v2, v3
	v_lshl_add_u64 v[0:1], v[0:1], 1, s[60:61]
	v_lshl_add_u64 v[0:1], v[0:1], 0, s[4:5]
	v_lshl_add_u64 v[0:1], v[0:1], 0, v[8:9]
	global_store_dwordx4 v[0:1], v[4:7], off nt
	s_waitcnt lgkmcnt(0)
	s_cbranch_scc0 .Lcvp31_ret

; __device__ __forceinline__ void conv_load(const ConvItem& ci, int lane, float (&v)[64]) {
;     const bool okc = ci.srcc >= 0 && (ci.srcc + lane) < ci.ncols;
;     const float* base = ci.W + (okc ? ci.srcc + lane : 0);
;     const int kmax = ci.Ksrc - 1;
; #pragma unroll
;     for (int i = 0; i < 64; ++i) { const int k = ci.k0 + i, kk = k < kmax ? k : kmax; v[i] = __builtin_nontemporal_load(base + (size_t)kk * ci.ldw); }
; #pragma unroll
;     for (int i = 0; i < 64; ++i) v[i] = (okc && (ci.k0 + i) < ci.Ksrc) ? v[i] : 0.f;
; }
.Lcvp130_30:
	s_cmp_lt_i32 s58, s76
	s_cselect_b64 s[4:5], -1, 0
	s_and_b64 s[4:5], vcc, s[4:5]
	s_cmp_lt_i32 s64, s76
	s_waitcnt vmcnt(62)
	v_cndmask_b32_e64 v21, 0, v21, s[4:5]
	s_cselect_b64 s[4:5], -1, 0
	s_and_b64 s[4:5], vcc, s[4:5]
	s_cmp_lt_i32 s65, s76
	v_cndmask_b32_e64 v20, 0, v20, s[4:5]
	s_cselect_b64 s[4:5], -1, 0
	s_and_b64 s[4:5], vcc, s[4:5]
	s_cmp_lt_i32 s78, s76
	s_waitcnt vmcnt(61)
	v_cndmask_b32_e64 v19, 0, v19, s[4:5]
	s_cselect_b64 s[4:5], -1, 0
	s_and_b64 s[4:5], vcc, s[4:5]
	s_cmp_lt_i32 s79, s76
	s_waitcnt vmcnt(60)
	v_cndmask_b32_e64 v18, 0, v18, s[4:5]
	s_cselect_b64 s[4:5], -1, 0
	s_and_b64 s[4:5], vcc, s[4:5]
	s_cmp_lt_i32 s80, s76
	s_waitcnt vmcnt(59)
	v_cndmask_b32_e64 v17, 0, v17, s[4:5]
	s_cselect_b64 s[4:5], -1, 0
	s_and_b64 s[4:5], vcc, s[4:5]
	s_cmp_lt_i32 s81, s76
	s_waitcnt vmcnt(58)
	v_cndmask_b32_e64 v16, 0, v16, s[4:5]
	s_cselect_b64 s[4:5], -1, 0
	s_and_b64 s[4:5], vcc, s[4:5]
	s_cmp_lt_i32 s82, s76
	s_waitcnt vmcnt(57)
	v_cndmask_b32_e64 v15, 0, v15, s[4:5]
	s_cselect_b64 s[4:5], -1, 0
	s_and_b64 s[4:5], vcc, s[4:5]
	s_cmp_lt_i32 s83, s76
	s_waitcnt vmcnt(56)
	v_cndmask_b32_e64 v8, 0, v8, s[4:5]
	s_cselect_b64 s[4:5], -1, 0
	s_and_b64 s[4:5], vcc, s[4:5]
	s_cmp_lt_i32 s85, s76
	s_waitcnt vmcnt(55)
	v_cndmask_b32_e64 v29, 0, v29, s[4:5]
	s_cselect_b64 s[4:5], -1, 0
	s_and_b64 s[4:5], vcc, s[4:5]
	s_cmp_lt_i32 s86, s76
	s_waitcnt vmcnt(54)
	v_cndmask_b32_e64 v28, 0, v28, s[4:5]
	s_cselect_b64 s[4:5], -1, 0
	s_and_b64 s[4:5], vcc, s[4:5]
	s_cmp_lt_i32 s87, s76
	s_waitcnt vmcnt(53)
	v_cndmask_b32_e64 v27, 0, v27, s[4:5]
	s_cselect_b64 s[4:5], -1, 0
	s_and_b64 s[4:5], vcc, s[4:5]
	s_cmp_lt_i32 s88, s76
	s_waitcnt vmcnt(52)
	v_cndmask_b32_e64 v26, 0, v26, s[4:5]
	s_cselect_b64 s[4:5], -1, 0
	s_and_b64 s[4:5], vcc, s[4:5]
	s_cmp_lt_i32 s89, s76
	s_waitcnt vmcnt(51)
	v_cndmask_b32_e64 v25, 0, v25, s[4:5]
	s_cselect_b64 s[4:5], -1, 0
	s_and_b64 s[4:5], vcc, s[4:5]
	s_cmp_lt_i32 s90, s76
	s_waitcnt vmcnt(50)
	v_cndmask_b32_e64 v24, 0, v24, s[4:5]
	s_cselect_b64 s[4:5], -1, 0
	s_and_b64 s[4:5], vcc, s[4:5]
	s_cmp_lt_i32 s92, s76
	s_waitcnt vmcnt(49)
	v_cndmask_b32_e64 v23, 0, v23, s[4:5]
	s_cselect_b64 s[4:5], -1, 0
	s_and_b64 s[4:5], vcc, s[4:5]
	s_cmp_lt_i32 s93, s76
	s_waitcnt vmcnt(48)
	v_cndmask_b32_e64 v22, 0, v22, s[4:5]
	s_cselect_b64 s[4:5], -1, 0
	s_and_b64 s[4:5], vcc, s[4:5]
	s_cmp_lt_i32 s94, s76
	s_waitcnt vmcnt(47)
	v_cndmask_b32_e64 v37, 0, v37, s[4:5]
	s_cselect_b64 s[4:5], -1, 0
	s_and_b64 s[4:5], vcc, s[4:5]
	s_cmp_lt_i32 s95, s76
	s_waitcnt vmcnt(46)
	v_cndmask_b32_e64 v36, 0, v36, s[4:5]
	s_cselect_b64 s[4:5], -1, 0
	s_and_b64 s[4:5], vcc, s[4:5]
	s_cmp_lt_i32 s50, s76
	s_waitcnt vmcnt(45)
	v_cndmask_b32_e64 v35, 0, v35, s[4:5]
	s_cselect_b64 s[4:5], -1, 0
	s_and_b64 s[4:5], vcc, s[4:5]
	s_cmp_lt_i32 s51, s76
	s_waitcnt vmcnt(44)
	v_cndmask_b32_e64 v34, 0, v34, s[4:5]
	s_cselect_b64 s[4:5], -1, 0
	s_and_b64 s[4:5], vcc, s[4:5]
	s_cmp_lt_i32 s52, s76
	s_waitcnt vmcnt(43)
	v_cndmask_b32_e64 v33, 0, v33, s[4:5]
	s_cselect_b64 s[4:5], -1, 0
	s_and_b64 s[4:5], vcc, s[4:5]
	s_cmp_lt_i32 s53, s76
	s_waitcnt vmcnt(42)
	v_cndmask_b32_e64 v32, 0, v32, s[4:5]
	s_cselect_b64 s[4:5], -1, 0
	s_and_b64 s[4:5], vcc, s[4:5]
	s_cmp_lt_i32 s6, s76
	s_waitcnt vmcnt(41)
	v_cndmask_b32_e64 v31, 0, v31, s[4:5]
	s_cselect_b64 s[4:5], -1, 0
	s_and_b64 s[4:5], vcc, s[4:5]
	s_cmp_lt_i32 s7, s76
	s_waitcnt vmcnt(40)
	v_cndmask_b32_e64 v30, 0, v30, s[4:5]
	s_cselect_b64 s[4:5], -1, 0
	s_and_b64 s[4:5], vcc, s[4:5]
	s_cmp_lt_i32 s8, s76
	s_waitcnt vmcnt(39)
	v_cndmask_b32_e64 v45, 0, v45, s[4:5]
	s_cselect_b64 s[4:5], -1, 0
	s_and_b64 s[4:5], vcc, s[4:5]
	s_cmp_lt_i32 s9, s76
	s_waitcnt vmcnt(38)
	v_cndmask_b32_e64 v44, 0, v44, s[4:5]
	s_cselect_b64 s[4:5], -1, 0
	s_and_b64 s[4:5], vcc, s[4:5]
	s_cmp_lt_i32 s10, s76
	s_waitcnt vmcnt(37)
	v_cndmask_b32_e64 v43, 0, v43, s[4:5]
	s_cselect_b64 s[4:5], -1, 0
	s_and_b64 s[4:5], vcc, s[4:5]
	s_cmp_lt_i32 s11, s76
	s_waitcnt vmcnt(36)
	v_cndmask_b32_e64 v42, 0, v42, s[4:5]
	s_cselect_b64 s[4:5], -1, 0
	s_and_b64 s[4:5], vcc, s[4:5]
	s_cmp_lt_i32 s14, s76
	s_waitcnt vmcnt(35)
	v_cndmask_b32_e64 v41, 0, v41, s[4:5]
	s_cselect_b64 s[4:5], -1, 0
	s_and_b64 s[4:5], vcc, s[4:5]
	s_cmp_lt_i32 s15, s76
	s_waitcnt vmcnt(34)
	v_cndmask_b32_e64 v40, 0, v40, s[4:5]
	s_cselect_b64 s[4:5], -1, 0
	s_and_b64 s[4:5], vcc, s[4:5]
	s_cmp_lt_i32 s16, s76
	s_waitcnt vmcnt(33)
	v_cndmask_b32_e64 v39, 0, v39, s[4:5]
	s_cselect_b64 s[4:5], -1, 0
	s_and_b64 s[4:5], vcc, s[4:5]
	s_cmp_lt_i32 s17, s76
	s_waitcnt vmcnt(32)
	v_cndmask_b32_e64 v38, 0, v38, s[4:5]
	s_cselect_b64 s[4:5], -1, 0
	s_and_b64 s[4:5], vcc, s[4:5]
	s_cmp_lt_i32 s12, s76
	s_waitcnt vmcnt(31)
	v_cndmask_b32_e64 v53, 0, v53, s[4:5]
	s_cselect_b64 s[4:5], -1, 0
	s_and_b64 s[4:5], vcc, s[4:5]
	s_cmp_lt_i32 s13, s76
	s_waitcnt vmcnt(30)
	v_cndmask_b32_e64 v52, 0, v52, s[4:5]
	s_cselect_b64 s[4:5], -1, 0
	s_and_b64 s[4:5], vcc, s[4:5]
	s_cmp_lt_i32 s20, s76
	s_waitcnt vmcnt(29)
	v_cndmask_b32_e64 v51, 0, v51, s[4:5]
	s_cselect_b64 s[4:5], -1, 0
	s_and_b64 s[4:5], vcc, s[4:5]
	s_cmp_lt_i32 s21, s76
	s_waitcnt vmcnt(28)
	v_cndmask_b32_e64 v50, 0, v50, s[4:5]
	s_cselect_b64 s[4:5], -1, 0
	s_and_b64 s[4:5], vcc, s[4:5]
	s_cmp_lt_i32 s24, s76
	s_waitcnt vmcnt(27)
	v_cndmask_b32_e64 v49, 0, v49, s[4:5]
	s_cselect_b64 s[4:5], -1, 0
	s_and_b64 s[4:5], vcc, s[4:5]
	s_cmp_lt_i32 s25, s76
	s_waitcnt vmcnt(26)
	v_cndmask_b32_e64 v48, 0, v48, s[4:5]
	s_cselect_b64 s[4:5], -1, 0
	s_and_b64 s[4:5], vcc, s[4:5]
	s_cmp_lt_i32 s26, s76
	s_waitcnt vmcnt(25)
	v_cndmask_b32_e64 v47, 0, v47, s[4:5]
	s_cselect_b64 s[4:5], -1, 0
	s_and_b64 s[4:5], vcc, s[4:5]
	s_cmp_lt_i32 s27, s76
	s_waitcnt vmcnt(24)
; #define LAS __attribute__((address_space(3)))
; #define LDS_WAIT() asm volatile("s_waitcnt lgkmcnt(0)" ::: "memory")
; __device__ __forceinline__ void conv_load(const ConvItem& ci, int lane, float (&v)[64]) {
;     ...
;     for (int i = 0; i < 64; ++i) { const int k = ci.k0 + i, kk = k < kmax ? k : kmax; v[i] = __builtin_nontemporal_load(base + (size_t)kk * ci.ldw); }
; #pragma unroll
;     for (int i = 0; i < 64; ++i) v[i] = (okc && (ci.k0 + i) < ci.Ksrc) ? v[i] : 0.f;
; }
; __device__ __forceinline__ void conv_store(const ConvItem& ci, LAS float* scr, int lane, const float (&v)[64]) {
;     const int c = lane & 7;
;     f32x4 s0 = {1.f, 1.f, 1.f, 1.f}, s1 = s0;
;     if (ci.ks) { const int kb = ci.k0 + 8 * c < ci.Ksrc - 8 ? ci.k0 + 8 * c : ci.Ksrc - 8; s0 = *(const f32x4*)(ci.ks + kb); s1 = *(const f32x4*)(ci.ks + kb + 4); }
; #pragma unroll
;     for (int i = 0; i < 64; ++i) scr[i * 65 + lane] = v[i];
;     LDS_WAIT(); asm volatile("" ::: "memory");
	v_cndmask_b32_e64 v46, 0, v46, s[4:5]
	s_cselect_b64 s[4:5], -1, 0
	s_and_b64 s[4:5], vcc, s[4:5]
	s_cmp_lt_i32 s18, s76
	s_waitcnt vmcnt(23)
	v_cndmask_b32_e64 v61, 0, v61, s[4:5]
	s_cselect_b64 s[4:5], -1, 0
	s_and_b64 s[4:5], vcc, s[4:5]
	s_cmp_lt_i32 s19, s76
	s_waitcnt vmcnt(22)
	v_cndmask_b32_e64 v60, 0, v60, s[4:5]
	s_cselect_b64 s[4:5], -1, 0
	s_and_b64 s[4:5], vcc, s[4:5]
	s_cmp_lt_i32 s28, s76
	s_waitcnt vmcnt(21)
	v_cndmask_b32_e64 v59, 0, v59, s[4:5]
	s_cselect_b64 s[4:5], -1, 0
	s_and_b64 s[4:5], vcc, s[4:5]
	s_cmp_lt_i32 s29, s76
	s_waitcnt vmcnt(20)
	v_cndmask_b32_e64 v58, 0, v58, s[4:5]
	s_cselect_b64 s[4:5], -1, 0
	s_and_b64 s[4:5], vcc, s[4:5]
	s_cmp_lt_i32 s22, s76
	s_waitcnt vmcnt(19)
	v_cndmask_b32_e64 v57, 0, v57, s[4:5]
	s_cselect_b64 s[4:5], -1, 0
	s_and_b64 s[4:5], vcc, s[4:5]
	s_cmp_lt_i32 s23, s76
	s_waitcnt vmcnt(18)
	v_cndmask_b32_e64 v56, 0, v56, s[4:5]
	s_cselect_b64 s[4:5], -1, 0
	s_and_b64 s[4:5], vcc, s[4:5]
	s_cmp_lt_i32 s30, s76
	s_waitcnt vmcnt(17)
	v_cndmask_b32_e64 v55, 0, v55, s[4:5]
	s_cselect_b64 s[4:5], -1, 0
	s_and_b64 s[4:5], vcc, s[4:5]
	s_cmp_lt_i32 s31, s76
	s_waitcnt vmcnt(16)
	v_cndmask_b32_e64 v54, 0, v54, s[4:5]
	s_cselect_b64 s[4:5], -1, 0
	s_and_b64 s[4:5], vcc, s[4:5]
	s_cmp_lt_i32 s36, s76
	s_waitcnt vmcnt(15)
	v_cndmask_b32_e64 v70, 0, v70, s[4:5]
	s_cselect_b64 s[4:5], -1, 0
	s_and_b64 s[4:5], vcc, s[4:5]
	s_cmp_lt_i32 s37, s76
	s_waitcnt vmcnt(14)
	v_cndmask_b32_e64 v69, 0, v69, s[4:5]
	s_cselect_b64 s[4:5], -1, 0
	s_and_b64 s[4:5], vcc, s[4:5]
	s_cmp_lt_i32 s38, s76
	s_waitcnt vmcnt(13)
	v_cndmask_b32_e64 v68, 0, v68, s[4:5]
	s_cselect_b64 s[4:5], -1, 0
	s_and_b64 s[4:5], vcc, s[4:5]
	s_cmp_lt_i32 s39, s76
	s_waitcnt vmcnt(12)
	v_cndmask_b32_e64 v67, 0, v67, s[4:5]
	s_cselect_b64 s[4:5], -1, 0
	s_and_b64 s[4:5], vcc, s[4:5]
	s_cmp_lt_i32 s34, s76
	s_waitcnt vmcnt(11)
	v_cndmask_b32_e64 v66, 0, v66, s[4:5]
	s_cselect_b64 s[4:5], -1, 0
	s_and_b64 s[4:5], vcc, s[4:5]
	s_cmp_lt_i32 s35, s76
	s_waitcnt vmcnt(10)
	v_cndmask_b32_e64 v64, 0, v64, s[4:5]
	s_cselect_b64 s[4:5], -1, 0
	s_and_b64 s[4:5], vcc, s[4:5]
	s_cmp_lt_i32 s42, s76
	s_waitcnt vmcnt(9)
	v_cndmask_b32_e64 v63, 0, v63, s[4:5]
	s_cselect_b64 s[4:5], -1, 0
	s_and_b64 s[4:5], vcc, s[4:5]
	s_cmp_lt_i32 s43, s76
	s_waitcnt vmcnt(8)
	v_cndmask_b32_e64 v62, 0, v62, s[4:5]
	s_cselect_b64 s[4:5], -1, 0
	s_and_b64 s[4:5], vcc, s[4:5]
	s_cmp_lt_i32 s54, s76
	s_waitcnt vmcnt(7)
	v_cndmask_b32_e64 v65, 0, v65, s[4:5]
	s_cselect_b64 s[4:5], -1, 0
	s_and_b64 s[4:5], vcc, s[4:5]
	s_cmp_lt_i32 s55, s76
	s_waitcnt vmcnt(6)
	v_cndmask_b32_e64 v74, 0, v74, s[4:5]
	s_cselect_b64 s[4:5], -1, 0
	s_and_b64 s[4:5], vcc, s[4:5]
	s_cmp_lt_i32 s46, s76
	ds_write2_b32 v12, v21, v20 offset1:65
	ds_write2_b32 v12, v19, v18 offset0:130 offset1:195
	v_add_u32_e32 v18, 0x400, v12
	s_waitcnt vmcnt(5)
	v_cndmask_b32_e64 v73, 0, v73, s[4:5]
	s_cselect_b64 s[4:5], -1, 0
	ds_write2_b32 v18, v17, v16 offset0:4 offset1:69
	ds_write2_b32 v18, v15, v8 offset0:134 offset1:199
	v_add_u32_e32 v8, 0x800, v12
	s_and_b64 s[4:5], vcc, s[4:5]
	ds_write2_b32 v8, v29, v28 offset0:8 offset1:73
	ds_write2_b32 v8, v27, v26 offset0:138 offset1:203
	v_add_u32_e32 v8, 0xc00, v12
	s_cmp_lt_i32 s47, s76
	ds_write2_b32 v8, v25, v24 offset0:12 offset1:77
	ds_write2_b32 v8, v23, v22 offset0:142 offset1:207
	v_add_u32_e32 v8, 0x1000, v12
	s_waitcnt vmcnt(4)
	v_cndmask_b32_e64 v72, 0, v72, s[4:5]
	s_cselect_b64 s[4:5], -1, 0
	ds_write2_b32 v8, v37, v36 offset0:16 offset1:81
	ds_write2_b32 v8, v35, v34 offset0:146 offset1:211
	v_add_u32_e32 v8, 0x1400, v12
	s_and_b64 s[4:5], vcc, s[4:5]
	ds_write2_b32 v8, v33, v32 offset0:20 offset1:85
	ds_write2_b32 v8, v31, v30 offset0:150 offset1:215
	v_add_u32_e32 v8, 0x1800, v12
	s_cmp_lt_i32 s48, s76
	ds_write2_b32 v8, v45, v44 offset0:24 offset1:89
	ds_write2_b32 v8, v43, v42 offset0:154 offset1:219
	v_add_u32_e32 v8, 0x1c00, v12
	s_waitcnt vmcnt(3)
	v_cndmask_b32_e64 v71, 0, v71, s[4:5]
	s_cselect_b64 s[4:5], -1, 0
	ds_write2_b32 v8, v41, v40 offset0:28 offset1:93
	ds_write2_b32 v8, v39, v38 offset0:158 offset1:223
	v_add_u32_e32 v8, 0x2000, v12
	s_and_b64 s[4:5], vcc, s[4:5]
	ds_write2_b32 v8, v53, v52 offset0:32 offset1:97
	ds_write2_b32 v8, v51, v50 offset0:162 offset1:227
	v_add_u32_e32 v8, 0x2400, v12
	s_cmp_lt_i32 s49, s76
	ds_write2_b32 v8, v49, v48 offset0:36 offset1:101
	ds_write2_b32 v8, v47, v46 offset0:166 offset1:231
	v_add_u32_e32 v8, 0x2800, v12
	s_waitcnt vmcnt(2)
	v_cndmask_b32_e64 v77, 0, v77, s[4:5]
	s_cselect_b64 s[4:5], -1, 0
	ds_write2_b32 v8, v61, v60 offset0:40 offset1:105
	ds_write2_b32 v8, v59, v58 offset0:170 offset1:235
	v_add_u32_e32 v8, 0x2c00, v12
	s_and_b64 s[4:5], vcc, s[4:5]
	ds_write2_b32 v8, v57, v56 offset0:44 offset1:109
	ds_write2_b32 v8, v55, v54 offset0:174 offset1:239
	v_add_u32_e32 v8, 0x3000, v12
	s_cmp_lt_i32 s44, s76
	ds_write2_b32 v8, v70, v69 offset0:48 offset1:113
	ds_write2_b32 v8, v68, v67 offset0:178 offset1:243
	v_add_u32_e32 v8, 0x3400, v12
	s_waitcnt vmcnt(1)
	v_cndmask_b32_e64 v76, 0, v76, s[4:5]
	s_cselect_b64 s[4:5], -1, 0
	ds_write2_b32 v8, v66, v64 offset0:52 offset1:117
	ds_write2_b32 v8, v63, v62 offset0:182 offset1:247
	v_add_u32_e32 v8, 0x3800, v12
	s_and_b64 vcc, vcc, s[4:5]
	ds_write2_b32 v8, v65, v74 offset0:56 offset1:121
	ds_write2_b32 v8, v73, v72 offset0:186 offset1:251
	v_add_u32_e32 v8, 0x3c00, v12
	s_waitcnt vmcnt(0)
	v_cndmask_b32_e32 v75, 0, v75, vcc
	ds_write2_b32 v8, v71, v77 offset0:60 offset1:125
	ds_write2_b32 v8, v76, v75 offset0:190 offset1:255
	s_waitcnt lgkmcnt(0)
; __device__ __forceinline__ unsigned cvt_pk_bf16(float lo, float hi) { unsigned r; asm volatile("v_cvt_pk_bf16_f32 %0, %1, %2" : "=v"(r) : "v"(lo), "v"(hi)); return r; }
; #define LAS __attribute__((address_space(3)))
; #define LDS_WAIT() asm volatile("s_waitcnt lgkmcnt(0)" ::: "memory")
; __device__ __forceinline__ void conv_store(const ConvItem& ci, LAS float* scr, int lane, const float (&v)[64]) {
;     ...
;     LDS_WAIT(); asm volatile("" ::: "memory");
; #pragma unroll
;     for (int j = 0; j < 8; ++j) { const int n = (lane >> 3) + 8 * j; const LAS float* s = scr + (8 * c) * 65 + n;
;         v4u o; o.x = cvt_pk_bf16(s[0 * 65] * s0[0], s[1 * 65] * s0[1]); o.y = cvt_pk_bf16(s[2 * 65] * s0[2], s[3 * 65] * s0[3]); o.z = cvt_pk_bf16(s[4 * 65] * s1[0], s[5 * 65] * s1[1]); o.w = cvt_pk_bf16(s[6 * 65] * s1[2], s[7 * 65] * s1[3]);
;         *(v4u*)(ci.dst + (size_t)(ci.drow0 + n) * ci.ldd + ci.k0 + 8 * c) = o; }
	v_add_u32_e32 v192, 0x400, v14
	ds_read2_b32 v[128:129], v14 offset1:65
	ds_read2_b32 v[130:131], v14 offset0:130 offset1:195
	ds_read2_b32 v[132:133], v192 offset0:4 offset1:69
	ds_read2_b32 v[134:135], v192 offset0:134 offset1:199
	ds_read2_b32 v[136:137], v14 offset0:8 offset1:73
	ds_read2_b32 v[138:139], v14 offset0:138 offset1:203
	ds_read2_b32 v[140:141], v192 offset0:12 offset1:77
	ds_read2_b32 v[142:143], v192 offset0:142 offset1:207
	ds_read2_b32 v[144:145], v14 offset0:16 offset1:81
	ds_read2_b32 v[146:147], v14 offset0:146 offset1:211
	ds_read2_b32 v[148:149], v192 offset0:20 offset1:85
	ds_read2_b32 v[150:151], v192 offset0:150 offset1:215
	ds_read2_b32 v[152:153], v14 offset0:24 offset1:89
	ds_read2_b32 v[154:155], v14 offset0:154 offset1:219
	ds_read2_b32 v[156:157], v192 offset0:28 offset1:93
	ds_read2_b32 v[158:159], v192 offset0:158 offset1:223
	ds_read2_b32 v[160:161], v14 offset0:32 offset1:97
	ds_read2_b32 v[162:163], v14 offset0:162 offset1:227
	ds_read2_b32 v[164:165], v192 offset0:36 offset1:101
	ds_read2_b32 v[166:167], v192 offset0:166 offset1:231
	ds_read2_b32 v[168:169], v14 offset0:40 offset1:105
	ds_read2_b32 v[170:171], v14 offset0:170 offset1:235
	ds_read2_b32 v[172:173], v192 offset0:44 offset1:109
	ds_read2_b32 v[174:175], v192 offset0:174 offset1:239
	ds_read2_b32 v[176:177], v14 offset0:48 offset1:113
	ds_read2_b32 v[178:179], v14 offset0:178 offset1:243
	ds_read2_b32 v[180:181], v192 offset0:52 offset1:117
	ds_read2_b32 v[182:183], v192 offset0:182 offset1:247
	ds_read2_b32 v[184:185], v14 offset0:56 offset1:121
	ds_read2_b32 v[186:187], v14 offset0:186 offset1:251
	ds_read2_b32 v[188:189], v192 offset0:60 offset1:125
	ds_read2_b32 v[190:191], v192 offset0:190 offset1:255
	s_waitcnt lgkmcnt(0)
	v_add_u32_e32 v24, s59, v13
	v_mul_lo_u32 v22, s57, v24
	s_ashr_i32 s59, s58, 31
	v_readlane_b32 s76, v254, 31
	s_waitcnt lgkmcnt(0)
	v_mul_f32_e32 v8, v4, v128
	v_mul_f32_e32 v15, v5, v129
	v_cvt_pk_bf16_f32 v16, v8, v15
	s_add_i32 s3, s3, s33
	s_add_i32 s66, s66, s67
	s_add_i32 s68, s68, s69
	s_add_i32 s70, s70, s71
	s_waitcnt lgkmcnt(0)
	v_mul_f32_e32 v15, v7, v131
	v_mul_f32_e32 v8, v6, v130
	v_cvt_pk_bf16_f32 v17, v8, v15
	v_add_u32_e32 v15, 0x400, v14
	s_add_i32 s72, s72, s73
	s_add_i32 s74, s74, s75
	v_readlane_b32 s78, v254, 33
	v_readlane_b32 s79, v254, 34
	s_waitcnt lgkmcnt(0)
	v_mul_f32_e32 v8, v0, v132
	v_mul_f32_e32 v18, v1, v133
	v_cvt_pk_bf16_f32 v18, v8, v18
	v_readlane_b32 s80, v255, 21
	v_readlane_b32 s77, v254, 32
	s_movk_i32 s78, 0x1580
	v_readlane_b32 s82, v255, 23
	s_waitcnt lgkmcnt(0)
	v_mul_f32_e32 v8, v2, v134
	v_mul_f32_e32 v19, v3, v135
	v_cvt_pk_bf16_f32 v19, v8, v19
	v_ashrrev_i32_e32 v8, 31, v24
	v_mul_lo_u32 v8, s56, v8
	v_mad_u64_u32 v[20:21], s[4:5], s56, v24, 0
	v_add3_u32 v21, v21, v8, v22
	v_lshl_add_u64 v[20:21], v[20:21], 1, s[60:61]
	s_lshl_b64 s[4:5], s[58:59], 1
	v_lshl_add_u64 v[20:21], v[20:21], 0, s[4:5]
	v_lshlrev_b32_e32 v8, 1, v10
	v_lshl_add_u64 v[20:21], v[20:21], 0, v[8:9]
	global_store_dwordx4 v[20:21], v[16:19], off nt
	s_cmpk_lt_i32 s3, 18688
	v_readlane_b32 s83, v255, 24
	s_waitcnt lgkmcnt(0)
	v_mul_f32_e32 v16, v4, v136
	v_mul_f32_e32 v17, v5, v137
	v_cvt_pk_bf16_f32 v16, v16, v17
	s_mov_b32 s79, 0x3f22f983
	s_mov_b32 s85, 0xbfc90fda
	s_brev_b32 s86, 1
	s_movk_i32 s87, 0x1f8
	s_waitcnt lgkmcnt(0)
	v_mul_f32_e32 v17, v6, v138
	v_mul_f32_e32 v18, v7, v139
	v_cvt_pk_bf16_f32 v17, v17, v18
	s_mov_b64 s[88:89], 0x80
	s_mov_b64 s[92:93], 0x4000
	s_mov_b64 s[94:95], 0x4800
	v_readlane_b32 s81, v255, 22
	s_waitcnt lgkmcnt(0)
	v_mul_f32_e32 v18, v0, v140
	v_mul_f32_e32 v19, v1, v141
	v_cvt_pk_bf16_f32 v18, v18, v19
	s_waitcnt lgkmcnt(0)
	v_mul_f32_e32 v19, v2, v142
	v_mul_f32_e32 v20, v3, v143
	v_cvt_pk_bf16_f32 v19, v19, v20
	v_add_u32_e32 v20, 8, v24
	v_ashrrev_i32_e32 v21, 31, v20
	v_mul_lo_u32 v22, s56, v21
	v_mul_lo_u32 v23, s57, v20
	v_mad_u64_u32 v[20:21], s[6:7], s56, v20, 0
	v_add3_u32 v21, v21, v22, v23
	v_lshl_add_u64 v[20:21], v[20:21], 1, s[60:61]
	v_lshl_add_u64 v[20:21], v[20:21], 0, s[4:5]
	v_lshl_add_u64 v[20:21], v[20:21], 0, v[8:9]
	global_store_dwordx4 v[20:21], v[16:19], off nt
	s_waitcnt lgkmcnt(0)
	s_nop 0
	v_mul_f32_e32 v16, v4, v144
	v_mul_f32_e32 v17, v5, v145
	v_cvt_pk_bf16_f32 v16, v16, v17
	s_waitcnt lgkmcnt(0)
	v_mul_f32_e32 v17, v6, v146
	v_mul_f32_e32 v18, v7, v147
	v_cvt_pk_bf16_f32 v17, v17, v18
	s_waitcnt lgkmcnt(0)
	v_mul_f32_e32 v18, v0, v148
	v_mul_f32_e32 v19, v1, v149
	v_cvt_pk_bf16_f32 v18, v18, v19
	s_waitcnt lgkmcnt(0)
; __device__ __forceinline__ unsigned cvt_pk_bf16(float lo, float hi) { unsigned r; asm volatile("v_cvt_pk_bf16_f32 %0, %1, %2" : "=v"(r) : "v"(lo), "v"(hi)); return r; }
; #define LAS __attribute__((address_space(3)))
; #define LDS_WAIT() asm volatile("s_waitcnt lgkmcnt(0)" ::: "memory")
; __device__ __forceinline__ void conv_store(const ConvItem& ci, LAS float* scr, int lane, const float (&v)[64]) {
;     ...
;     for (int j = 0; j < 8; ++j) { const int n = (lane >> 3) + 8 * j; const LAS float* s = scr + (8 * c) * 65 + n;
;         v4u o; o.x = cvt_pk_bf16(s[0 * 65] * s0[0], s[1 * 65] * s0[1]); o.y = cvt_pk_bf16(s[2 * 65] * s0[2], s[3 * 65] * s0[3]); o.z = cvt_pk_bf16(s[4 * 65] * s1[0], s[5 * 65] * s1[1]); o.w = cvt_pk_bf16(s[6 * 65] * s1[2], s[7 * 65] * s1[3]);
;         *(v4u*)(ci.dst + (size_t)(ci.drow0 + n) * ci.ldd + ci.k0 + 8 * c) = o; }
;     LDS_WAIT(); asm volatile("" ::: "memory");
; }
	v_mul_f32_e32 v19, v2, v150
	v_mul_f32_e32 v20, v3, v151
	v_cvt_pk_bf16_f32 v19, v19, v20
	v_add_u32_e32 v20, 16, v24
	v_ashrrev_i32_e32 v21, 31, v20
	v_mul_lo_u32 v22, s56, v21
	v_mul_lo_u32 v23, s57, v20
	v_mad_u64_u32 v[20:21], s[6:7], s56, v20, 0
	v_add3_u32 v21, v21, v22, v23
	v_lshl_add_u64 v[20:21], v[20:21], 1, s[60:61]
	v_lshl_add_u64 v[20:21], v[20:21], 0, s[4:5]
	v_lshl_add_u64 v[20:21], v[20:21], 0, v[8:9]
	global_store_dwordx4 v[20:21], v[16:19], off nt
	s_waitcnt lgkmcnt(0)
	s_nop 0
	v_mul_f32_e32 v16, v4, v152
	v_mul_f32_e32 v17, v5, v153
	v_cvt_pk_bf16_f32 v16, v16, v17
	s_waitcnt lgkmcnt(0)
	v_mul_f32_e32 v17, v6, v154
	v_mul_f32_e32 v18, v7, v155
	v_cvt_pk_bf16_f32 v17, v17, v18
	s_waitcnt lgkmcnt(0)
	v_mul_f32_e32 v18, v0, v156
	v_mul_f32_e32 v19, v1, v157
	v_cvt_pk_bf16_f32 v18, v18, v19
	s_waitcnt lgkmcnt(0)
	v_mul_f32_e32 v19, v2, v158
	v_mul_f32_e32 v20, v3, v159
	v_cvt_pk_bf16_f32 v19, v19, v20
	v_add_u32_e32 v20, 24, v24
	v_ashrrev_i32_e32 v21, 31, v20
	v_mul_lo_u32 v22, s56, v21
	v_mul_lo_u32 v23, s57, v20
	v_mad_u64_u32 v[20:21], s[6:7], s56, v20, 0
	v_add3_u32 v21, v21, v22, v23
	v_lshl_add_u64 v[20:21], v[20:21], 1, s[60:61]
	v_lshl_add_u64 v[20:21], v[20:21], 0, s[4:5]
	v_lshl_add_u64 v[20:21], v[20:21], 0, v[8:9]
	global_store_dwordx4 v[20:21], v[16:19], off nt
	s_waitcnt lgkmcnt(0)
	s_nop 0
	v_mul_f32_e32 v16, v4, v160
	v_mul_f32_e32 v17, v5, v161
	v_cvt_pk_bf16_f32 v16, v16, v17
	s_waitcnt lgkmcnt(0)
	v_mul_f32_e32 v17, v6, v162
	v_mul_f32_e32 v18, v7, v163
	v_cvt_pk_bf16_f32 v17, v17, v18
	s_waitcnt lgkmcnt(0)
	v_mul_f32_e32 v18, v0, v164
	v_mul_f32_e32 v19, v1, v165
	v_cvt_pk_bf16_f32 v18, v18, v19
	s_waitcnt lgkmcnt(0)
	v_mul_f32_e32 v19, v2, v166
	v_mul_f32_e32 v20, v3, v167
	v_cvt_pk_bf16_f32 v19, v19, v20
	v_add_u32_e32 v20, 32, v24
	v_ashrrev_i32_e32 v21, 31, v20
	v_mul_lo_u32 v22, s56, v21
	v_mul_lo_u32 v23, s57, v20
	v_mad_u64_u32 v[20:21], s[6:7], s56, v20, 0
	v_add3_u32 v21, v21, v22, v23
	v_lshl_add_u64 v[20:21], v[20:21], 1, s[60:61]
	v_lshl_add_u64 v[20:21], v[20:21], 0, s[4:5]
	v_lshl_add_u64 v[20:21], v[20:21], 0, v[8:9]
	global_store_dwordx4 v[20:21], v[16:19], off nt
	s_waitcnt lgkmcnt(0)
	s_nop 0
	v_mul_f32_e32 v16, v4, v168
	v_mul_f32_e32 v17, v5, v169
	v_cvt_pk_bf16_f32 v16, v16, v17
	s_waitcnt lgkmcnt(0)
	v_mul_f32_e32 v17, v6, v170
	v_mul_f32_e32 v18, v7, v171
	v_cvt_pk_bf16_f32 v17, v17, v18
	s_waitcnt lgkmcnt(0)
	v_mul_f32_e32 v18, v0, v172
	v_mul_f32_e32 v19, v1, v173
	v_cvt_pk_bf16_f32 v18, v18, v19
	s_waitcnt lgkmcnt(0)
	v_mul_f32_e32 v19, v2, v174
	v_mul_f32_e32 v20, v3, v175
	v_cvt_pk_bf16_f32 v19, v19, v20
	v_add_u32_e32 v20, 40, v24
	v_ashrrev_i32_e32 v21, 31, v20
	v_mul_lo_u32 v22, s56, v21
	v_mul_lo_u32 v23, s57, v20
	v_mad_u64_u32 v[20:21], s[6:7], s56, v20, 0
	v_add3_u32 v21, v21, v22, v23
	v_lshl_add_u64 v[20:21], v[20:21], 1, s[60:61]
	v_lshl_add_u64 v[20:21], v[20:21], 0, s[4:5]
	v_lshl_add_u64 v[20:21], v[20:21], 0, v[8:9]
	global_store_dwordx4 v[20:21], v[16:19], off nt
	s_waitcnt lgkmcnt(0)
	s_nop 0
	v_mul_f32_e32 v16, v4, v176
	v_mul_f32_e32 v17, v5, v177
	v_cvt_pk_bf16_f32 v16, v16, v17
	s_waitcnt lgkmcnt(0)
	v_mul_f32_e32 v17, v6, v178
	v_mul_f32_e32 v18, v7, v179
	v_cvt_pk_bf16_f32 v17, v17, v18
	s_waitcnt lgkmcnt(0)
	v_mul_f32_e32 v18, v0, v180
	v_mul_f32_e32 v19, v1, v181
	v_cvt_pk_bf16_f32 v18, v18, v19
	s_waitcnt lgkmcnt(0)
	v_mul_f32_e32 v19, v2, v182
	v_mul_f32_e32 v20, v3, v183
	v_cvt_pk_bf16_f32 v19, v19, v20
	v_add_u32_e32 v20, 48, v24
	v_ashrrev_i32_e32 v21, 31, v20
	v_mul_lo_u32 v22, s56, v21
	v_mul_lo_u32 v23, s57, v20
	v_mad_u64_u32 v[20:21], s[6:7], s56, v20, 0
	v_add3_u32 v21, v21, v22, v23
	v_lshl_add_u64 v[20:21], v[20:21], 1, s[60:61]
	v_lshl_add_u64 v[20:21], v[20:21], 0, s[4:5]
	v_lshl_add_u64 v[20:21], v[20:21], 0, v[8:9]
	global_store_dwordx4 v[20:21], v[16:19], off nt
	s_waitcnt lgkmcnt(0)
	v_mul_f32_e32 v4, v4, v184
	v_mul_f32_e32 v5, v5, v185
	v_cvt_pk_bf16_f32 v4, v4, v5
	s_waitcnt lgkmcnt(0)
	v_mul_f32_e32 v5, v6, v186
	v_mul_f32_e32 v6, v7, v187
	v_cvt_pk_bf16_f32 v5, v5, v6
	s_waitcnt lgkmcnt(0)
	v_mul_f32_e32 v0, v0, v188
	v_mul_f32_e32 v1, v1, v189
	v_cvt_pk_bf16_f32 v6, v0, v1
	s_waitcnt lgkmcnt(0)
	v_mul_f32_e32 v0, v2, v190
	v_mul_f32_e32 v1, v3, v191
	v_cvt_pk_bf16_f32 v7, v0, v1
	v_add_u32_e32 v0, 56, v24
	v_ashrrev_i32_e32 v1, 31, v0
	v_mul_lo_u32 v2, s56, v1
	v_mul_lo_u32 v3, s57, v0
	v_mad_u64_u32 v[0:1], s[6:7], s56, v0, 0
	v_add3_u32 v1, v1, v2, v3
	v_lshl_add_u64 v[0:1], v[0:1], 1, s[60:61]
	v_lshl_add_u64 v[0:1], v[0:1], 0, s[4:5]
	v_lshl_add_u64 v[0:1], v[0:1], 0, v[8:9]
	global_store_dwordx4 v[0:1], v[4:7], off nt
	s_waitcnt lgkmcnt(0)
	s_cbranch_scc0 .Lcvp130_ret
